# v9_xx
# speedup vs baseline: 1.0008x; 1.0008x over previous
.LBB3_46:
	v_cmp_eq_u32_e32 vcc, 2, v3
	s_mov_b64 s[4:5], -1
	s_and_saveexec_b64 s[44:45], vcc
	s_cbranch_execz .LBB3_56
	v_lshrrev_b32_e32 v2, 2, v2
	v_and_b32_e32 v22, 12, v2
	v_mul_u32_u24_e32 v4, 48, v105
	v_or_b32_e32 v3, v22, v4
	v_lshlrev_b32_e32 v5, 2, v3
	v_or_b32_e32 v24, 3, v2
	v_or_b32_e32 v69, 19, v2
	v_or_b32_e32 v2, 35, v2
	v_or_b32_e32 v3, v24, v4
	v_add_lshl_u32 v26, v69, v4, 2
	v_add_lshl_u32 v4, v2, v4, 2
	v_add_u32_e32 v27, 0xc00, v5
	s_waitcnt lgkmcnt(0)
	global_load_dwordx3 v[6:8], v5, s[12:13]
	global_load_dwordx3 v[10:12], v5, s[14:15]
	v_lshlrev_b32_e32 v25, 2, v3
	global_load_dwordx3 v[14:16], v5, s[12:13] offset:64
	global_load_dwordx3 v[18:20], v5, s[14:15] offset:64
	global_load_dword v3, v25, s[12:13]
	global_load_dword v9, v25, s[14:15]
	global_load_dwordx3 v[32:34], v5, s[12:13] offset:128
	global_load_dwordx3 v[36:38], v5, s[14:15] offset:128
	global_load_dword v13, v26, s[12:13]
	global_load_dword v17, v26, s[14:15]
	global_load_dword v21, v4, s[12:13]
	global_load_dword v23, v4, s[14:15]
	global_load_dwordx3 v[40:42], v27, s[12:13] offset:64
	global_load_dwordx3 v[44:46], v27, s[14:15] offset:64
	global_load_dword v35, v26, s[12:13] offset:3072
	global_load_dword v39, v26, s[14:15] offset:3072
	global_load_dwordx3 v[48:50], v27, s[12:13] offset:128
	global_load_dwordx3 v[52:54], v27, s[14:15] offset:128
	v_mov_b32_e32 v26, 0x600
	v_mad_u32_u24 v73, v105, 48, v26
	global_load_dword v43, v4, s[12:13] offset:3072
	global_load_dword v47, v4, s[14:15] offset:3072
	global_load_dwordx2 v[74:75], v5, s[12:13] offset:3072
	global_load_dwordx2 v[76:77], v5, s[14:15] offset:3072
	global_load_dword v79, v25, s[12:13] offset:3072
	global_load_dword v81, v25, s[14:15] offset:3072
	global_load_dword v78, v27, s[12:13] offset:8
	global_load_dword v80, v27, s[14:15] offset:8
	v_or_b32_e32 v4, v22, v73
	v_lshlrev_b32_e32 v4, 2, v4
	v_add_lshl_u32 v2, v2, v73, 2
	global_load_dwordx3 v[56:58], v4, s[12:13] offset:128
	global_load_dwordx3 v[60:62], v4, s[14:15] offset:128
	global_load_dword v51, v2, s[12:13]
	global_load_dword v55, v2, s[14:15]
	global_load_dwordx3 v[66:68], v4, s[12:13]
	global_load_dwordx3 v[70:72], v4, s[14:15]
	v_or_b32_e32 v2, v24, v73
	v_lshlrev_b32_e32 v2, 2, v2
	global_load_dword v59, v2, s[12:13]
	global_load_dword v63, v2, s[14:15]
	global_load_dwordx3 v[28:30], v4, s[12:13] offset:64
	global_load_dwordx3 v[24:26], v4, s[14:15] offset:64
	v_lshl_or_b32 v31, v64, 4, v22
	v_cmp_eq_u32_e64 s[4:5], 3, v64
	s_mov_b32 s6, 0x4038aa3b
	s_mov_b32 s3, 0x3fb8aa3b
	v_cndmask_b32_e64 v2, v31, 0, s[4:5]
	v_lshlrev_b32_e32 v2, 2, v2
	global_load_dword v27, v2, s[24:25]
	s_mov_b32 s33, 0x3f2aaaab
	v_mov_b32_e32 v4, 0
	v_mov_b32_e32 v5, v4
	s_waitcnt vmcnt(36)
	v_mov_b32_e32 v2, v8
	s_waitcnt vmcnt(35)
	v_pk_mul_f32 v[6:7], v[6:7], v[10:11]
	v_mov_b32_e32 v8, v12
	s_waitcnt vmcnt(33)
	v_pk_mul_f32 v[10:11], v[14:15], v[18:19]
	v_mov_b32_e32 v12, v16
	v_mov_b32_e32 v16, v20
	s_waitcnt vmcnt(29)
	v_pk_mul_f32 v[14:15], v[32:33], v[36:37]
	v_mov_b32_e32 v20, v34
	v_mov_b32_e32 v22, v38
	v_pk_mul_f32 v[2:3], v[2:3], v[8:9]
	v_pk_mul_f32 v[8:9], v[10:11], s[6:7] op_sel_hi:[1,0]
	s_waitcnt vmcnt(27)
	v_pk_mul_f32 v[10:11], v[12:13], v[16:17]
	v_pk_mul_f32 v[12:13], v[14:15], s[6:7] op_sel_hi:[1,0]
	s_waitcnt vmcnt(25)
	v_pk_mul_f32 v[14:15], v[20:21], v[22:23]
	v_pk_mul_f32 v[16:17], v[2:3], s[6:7] op_sel_hi:[1,0]
	v_pk_mul_f32 v[10:11], v[10:11], s[6:7] op_sel_hi:[1,0]
	v_cvt_pk_f16_f32 v2, v12, v13
	v_pk_mul_f32 v[12:13], v[14:15], s[6:7] op_sel_hi:[1,0]
	s_waitcnt vmcnt(24)
	v_mov_b32_e32 v34, v42
	s_waitcnt vmcnt(23)
	v_mov_b32_e32 v38, v46
	s_waitcnt vmcnt(1)
	v_pk_mul_f32 v[24:25], v[28:29], v[24:25]
	v_or_b32_e32 v28, 1, v31
	v_cvt_pk_f16_f32 v8, v8, v9
	v_cvt_pk_f16_f32 v9, v10, v11
	v_cvt_pk_f16_f32 v3, v12, v13
	v_pk_mul_f32 v[10:11], v[40:41], v[44:45]
	v_pk_mul_f32 v[12:13], v[34:35], v[38:39]
	v_cndmask_b32_e64 v28, v28, 0, s[4:5]
	v_or_b32_e32 v29, 2, v31
	v_or_b32_e32 v31, 3, v31
	v_pk_mul_f32 v[10:11], v[10:11], s[6:7] op_sel_hi:[1,0]
	v_pk_mul_f32 v[12:13], v[12:13], s[6:7] op_sel_hi:[1,0]
	v_mov_b32_e32 v42, v50
	v_mov_b32_e32 v46, v54
	v_mov_b32_e32 v50, v58
	v_mov_b32_e32 v54, v62
	v_lshlrev_b32_e32 v28, 2, v28
	v_cndmask_b32_e64 v29, v29, 0, s[4:5]
	v_cndmask_b32_e64 v31, v31, 0, s[4:5]
	v_cvt_pk_f16_f32 v10, v10, v11
	v_cvt_pk_f16_f32 v11, v12, v13
	v_pk_mul_f32 v[12:13], v[48:49], v[52:53]
	v_pk_mul_f32 v[20:21], v[50:51], v[54:55]
	v_lshlrev_b32_e32 v29, 2, v29
	v_lshlrev_b32_e32 v31, 2, v31
	global_load_dword v50, v28, s[24:25]
	global_load_dword v52, v29, s[24:25]
	global_load_dword v54, v31, s[24:25]
	s_waitcnt vmcnt(3)
	v_mul_f32_e32 v28, 0x3fb8aa3b, v27
	v_fma_f32 v29, v27, s3, -v28
	v_rndne_f32_e32 v31, v28
	v_pk_mul_f32 v[14:15], v[42:43], v[46:47]
	v_fmac_f32_e32 v29, 0x32a5705f, v27
	v_sub_f32_e32 v28, v28, v31
	v_pk_mul_f32 v[12:13], v[12:13], s[6:7] op_sel_hi:[1,0]
	v_pk_mul_f32 v[14:15], v[14:15], s[6:7] op_sel_hi:[1,0]
	v_add_f32_e32 v28, v28, v29
	v_cvt_pk_f16_f32 v12, v12, v13
	v_cvt_pk_f16_f32 v13, v14, v15
	v_pk_mul_f32 v[14:15], v[74:75], v[76:77]
	v_exp_f32_e32 v28, v28
	v_cvt_i32_f32_e32 v29, v31
	v_pk_mul_f32 v[6:7], v[6:7], s[6:7] op_sel_hi:[1,0]
	v_pk_mul_f32 v[14:15], v[14:15], s[6:7] op_sel_hi:[1,0]
	v_mov_b32_e32 v58, v68
	v_mov_b32_e32 v62, v72
	v_cvt_pk_f16_f32 v6, v6, v7
	v_cvt_pk_f16_f32 v7, v16, v17
	v_cvt_pk_f16_f32 v16, v14, v15
	v_pk_mul_f32 v[14:15], v[78:79], v[80:81]
	v_pk_mul_f32 v[18:19], v[56:57], v[60:61]
	v_pk_mul_f32 v[22:23], v[66:67], v[70:71]
	v_pk_mul_f32 v[32:33], v[58:59], v[62:63]
	v_pk_mul_f32 v[24:25], v[24:25], s[6:7] op_sel_hi:[1,0]
	v_pk_mul_f32 v[14:15], v[14:15], s[6:7] op_sel_hi:[1,0]
	v_pk_mul_f32 v[18:19], v[18:19], s[6:7] op_sel_hi:[1,0]
	v_pk_mul_f32 v[20:21], v[20:21], s[6:7] op_sel_hi:[1,0]
	v_pk_mul_f32 v[22:23], v[22:23], s[6:7] op_sel_hi:[1,0]
	v_pk_mul_f32 v[32:33], v[32:33], s[6:7] op_sel_hi:[1,0]
	v_cvt_pk_f16_f32 v24, v24, v25
	v_add_lshl_u32 v25, v69, v73, 2
	s_mov_b32 s7, 0xc2ce8ed0
	v_cvt_pk_f16_f32 v22, v22, v23
	v_cvt_pk_f16_f32 v23, v32, v33
	global_load_dword v33, v25, s[12:13]
	global_load_dword v35, v25, s[14:15]
	v_ldexp_f32 v25, v28, v29
	v_cmp_ngt_f32_e32 vcc, s7, v27
	s_mov_b32 s12, 0x42b17218
	v_mov_b32_e32 v32, v30
	v_cndmask_b32_e32 v25, 0, v25, vcc
	v_mov_b32_e32 v30, 0x7f800000
	v_cmp_nlt_f32_e32 vcc, s12, v27
	v_mov_b32_e32 v55, 0x3ecc95a3
	s_mov_b32 s25, 0x3f317218
	v_cndmask_b32_e32 v25, v30, v25, vcc
	v_add_f32_e32 v27, 1.0, v25
	v_add_f32_e32 v28, -1.0, v27
	v_sub_f32_e32 v29, v28, v27
	v_add_f32_e32 v29, 1.0, v29
	v_sub_f32_e32 v28, v25, v28
	v_add_f32_e32 v31, v28, v29
	v_frexp_mant_f32_e32 v34, v27
	v_cvt_f64_f32_e32 v[28:29], v27
	v_frexp_exp_i32_f64_e32 v28, v[28:29]
	v_cmp_gt_f32_e32 vcc, s33, v34
	s_mov_b32 s13, 0x7f800000
	s_mov_b32 s15, 0x33800000
	v_subbrev_co_u32_e32 v34, vcc, 0, v28, vcc
	v_sub_u32_e32 v28, 0, v34
	v_ldexp_f32 v27, v27, v28
	v_ldexp_f32 v28, v31, v28
	v_add_f32_e32 v31, -1.0, v27
	v_add_f32_e32 v29, 1.0, v31
	v_sub_f32_e32 v29, v27, v29
	v_add_f32_e32 v36, v28, v29
	v_add_f32_e32 v29, 1.0, v27
	v_add_f32_e32 v37, -1.0, v29
	v_sub_f32_e32 v27, v27, v37
	v_add_f32_e32 v27, v28, v27
	v_add_f32_e32 v42, v29, v27
	v_rcp_f32_e32 v43, v42
	v_sub_f32_e32 v28, v29, v42
	v_add_f32_e32 v29, v31, v36
	v_add_f32_e32 v27, v27, v28
	v_sub_f32_e32 v28, v31, v29
	v_mul_f32_e32 v44, v29, v43
	v_add_f32_e32 v31, v36, v28
	v_mul_f32_e32 v36, v42, v44
	v_fma_f32 v38, v44, v42, -v36
	v_fmac_f32_e32 v38, v44, v27
	v_add_f32_e32 v28, v36, v38
	v_sub_f32_e32 v37, v29, v28
	v_pk_add_f32 v[40:41], v[28:29], v[36:37] neg_lo:[0,1] neg_hi:[0,1]
	v_mov_b32_e32 v39, v28
	v_pk_add_f32 v[28:29], v[40:41], v[38:39] neg_lo:[0,1] neg_hi:[0,1]
	v_cmp_neq_f32_e32 vcc, s13, v25
	v_add_f32_e32 v29, v31, v29
	v_add_f32_e32 v28, v28, v29
	v_add_f32_e32 v29, v37, v28
	v_mul_f32_e32 v31, v43, v29
	v_mul_f32_e32 v36, v42, v31
	v_fma_f32 v38, v31, v42, -v36
	v_fmac_f32_e32 v38, v31, v27
	v_sub_f32_e32 v27, v37, v29
	v_add_f32_e32 v27, v28, v27
	v_add_f32_e32 v28, v36, v38
	v_sub_f32_e32 v37, v29, v28
	v_pk_add_f32 v[40:41], v[28:29], v[36:37] neg_lo:[0,1] neg_hi:[0,1]
	v_mov_b32_e32 v39, v28
	v_pk_add_f32 v[28:29], v[40:41], v[38:39] neg_lo:[0,1] neg_hi:[0,1]
	v_cvt_f32_i32_e32 v36, v34
	v_add_f32_e32 v27, v27, v29
	v_add_f32_e32 v27, v28, v27
	v_add_f32_e32 v28, v44, v31
	v_add_f32_e32 v27, v37, v27
	v_sub_f32_e32 v29, v28, v44
	v_mul_f32_e32 v27, v43, v27
	v_sub_f32_e32 v29, v31, v29
	v_add_f32_e32 v27, v29, v27
	v_add_f32_e32 v31, v28, v27
	v_mul_f32_e32 v37, v31, v31
	v_fmamk_f32 v29, v37, 0x3e9b6dac, v55
	v_sub_f32_e32 v28, v31, v28
	v_fmaak_f32 v29, v37, v29, 0x3f2aaada
	v_sub_f32_e32 v27, v27, v28
	v_mul_f32_e32 v37, v31, v37
	v_mov_b32_e32 v28, 0x3f317218
	v_pk_mul_f32 v[40:41], v[36:37], v[28:29]
	v_ldexp_f32 v39, v31, 1
	v_fma_f32 v38, v36, s25, -v40
	v_fmac_f32_e32 v38, 0xb102e308, v36
	v_pk_add_f32 v[36:37], v[40:41], v[38:39]
	v_ldexp_f32 v27, v27, 1
	v_sub_f32_e32 v29, v37, v39
	v_sub_f32_e32 v29, v41, v29
	v_add_f32_e32 v43, v27, v29
	v_mov_b32_e32 v42, v40
	v_pk_add_f32 v[40:41], v[36:37], v[40:41] neg_lo:[0,1] neg_hi:[0,1]
	v_pk_add_f32 v[44:45], v[36:37], v[42:43]
	v_mov_b32_e32 v39, v36
	v_mov_b32_e32 v41, v45
	v_pk_add_f32 v[46:47], v[38:39], v[40:41] neg_lo:[0,1] neg_hi:[0,1]
	v_pk_add_f32 v[38:39], v[38:39], v[40:41]
	v_mov_b32_e32 v42, v43
	v_pk_add_f32 v[40:41], v[38:39], v[36:37] op_sel:[1,0] op_sel_hi:[0,1] neg_lo:[0,1] neg_hi:[0,1]
	v_pk_add_f32 v[48:49], v[44:45], v[40:41] op_sel_hi:[1,0] neg_lo:[0,1] neg_hi:[0,1]
	v_mov_b32_e32 v44, v45
	v_mov_b32_e32 v45, v39
	v_pk_mov_b32 v[40:41], v[36:37], v[40:41] op_sel:[1,0]
	v_mov_b32_e32 v43, v36
	v_pk_add_f32 v[40:41], v[44:45], v[40:41] neg_lo:[0,1] neg_hi:[0,1]
	v_mov_b32_e32 v48, v46
	v_pk_add_f32 v[36:37], v[42:43], v[40:41] neg_lo:[0,1] neg_hi:[0,1]
	v_mov_b32_e32 v47, v39
	v_pk_add_f32 v[40:41], v[48:49], v[36:37]
	s_mov_b32 s24, 0x3c23d70a
	v_pk_add_f32 v[42:43], v[40:41], v[40:41] op_sel:[0,1] op_sel_hi:[1,0]
	v_mov_b32_e32 v31, 0x41200000
	v_pk_add_f32 v[38:39], v[38:39], v[42:43] op_sel:[1,0] op_sel_hi:[0,1]
	v_mov_b32_e32 v41, v38
	v_pk_add_f32 v[44:45], v[40:41], v[46:47] neg_lo:[0,1] neg_hi:[0,1]
	v_mov_b32_e32 v37, v42
	v_sub_f32_e32 v27, v40, v44
	v_pk_add_f32 v[36:37], v[36:37], v[44:45] neg_lo:[0,1] neg_hi:[0,1]
	v_sub_f32_e32 v27, v46, v27
	v_add_f32_e32 v27, v36, v27
	v_add_f32_e32 v27, v27, v37
	v_add_f32_e32 v27, v38, v27
	v_cndmask_b32_e32 v27, v30, v27, vcc
	v_cmp_lt_f32_e64 vcc, |v25|, s15
	s_mov_b32 s14, 0xbd23d70a
	v_mov_b32_e32 v34, v26
	v_cndmask_b32_e32 v25, v27, v25, vcc
	v_add_f32_e32 v25, 0x358637bd, v25
	v_med3_f32 v25, v25, s24, v31
	v_div_scale_f32 v29, s[46:47], v25, v25, s14
	v_rcp_f32_e32 v36, v29
	s_waitcnt vmcnt(0)
	v_pk_mul_f32 v[26:27], v[32:33], v[34:35]
	v_mov_b32_e32 v49, 0x3f2aaada
	v_pk_mul_f32 v[26:27], v[26:27], s[6:7] op_sel_hi:[1,0]
	v_fma_f32 v32, -v29, v36, 1.0
	v_fmac_f32_e32 v36, v32, v36
	v_div_scale_f32 v32, vcc, s14, v25, s14
	v_mul_f32_e32 v33, v32, v36
	v_fma_f32 v34, -v29, v33, v32
	v_fmac_f32_e32 v33, v34, v36
	v_fma_f32 v29, -v29, v33, v32
	v_div_fmas_f32 v29, v29, v36, v33
	v_mul_f32_e32 v33, 0x3fb8aa3b, v50
	v_fma_f32 v34, v50, s3, -v33
	v_rndne_f32_e32 v35, v33
	v_fmac_f32_e32 v34, 0x32a5705f, v50
	v_sub_f32_e32 v33, v33, v35
	v_div_fixup_f32 v46, v29, v25, s14
	v_add_f32_e32 v33, v33, v34
	v_mul_f32_e32 v25, 0x3fb8aa3b, v46
	v_exp_f32_e32 v33, v33
	v_cvt_i32_f32_e32 v34, v35
	v_fma_f32 v29, v46, s3, -v25
	v_rndne_f32_e32 v32, v25
	v_fmac_f32_e32 v29, 0x32a5705f, v46
	v_sub_f32_e32 v25, v25, v32
	v_add_f32_e32 v25, v25, v29
	v_exp_f32_e32 v47, v25
	v_ldexp_f32 v25, v33, v34
	v_cmp_ngt_f32_e32 vcc, s7, v50
	v_cvt_i32_f32_e32 v48, v32
	v_cvt_pk_f16_f32 v17, v14, v15
	v_cndmask_b32_e32 v25, 0, v25, vcc
	v_cmp_nlt_f32_e32 vcc, s12, v50
	v_mov_b32_e32 v14, v4
	v_mov_b32_e32 v15, v4
	v_cndmask_b32_e32 v25, v30, v25, vcc
	v_add_f32_e32 v29, 1.0, v25
	v_add_f32_e32 v32, -1.0, v29
	v_sub_f32_e32 v33, v32, v29
	v_add_f32_e32 v33, 1.0, v33
	v_sub_f32_e32 v32, v25, v32
	v_add_f32_e32 v34, v32, v33
	v_frexp_mant_f32_e32 v35, v29
	v_cvt_f64_f32_e32 v[32:33], v29
	v_frexp_exp_i32_f64_e32 v32, v[32:33]
	v_cmp_gt_f32_e32 vcc, s33, v35
	v_cvt_pk_f16_f32 v18, v18, v19
	v_cvt_pk_f16_f32 v19, v20, v21
	v_subbrev_co_u32_e32 v40, vcc, 0, v32, vcc
	v_sub_u32_e32 v32, 0, v40
	v_ldexp_f32 v29, v29, v32
	v_ldexp_f32 v32, v34, v32
	v_add_f32_e32 v34, -1.0, v29
	v_add_f32_e32 v33, 1.0, v34
	v_sub_f32_e32 v33, v29, v33
	v_add_f32_e32 v35, v32, v33
	v_add_f32_e32 v33, 1.0, v29
	v_add_f32_e32 v36, -1.0, v33
	v_sub_f32_e32 v29, v29, v36
	v_add_f32_e32 v29, v32, v29
	v_add_f32_e32 v41, v33, v29
	v_rcp_f32_e32 v42, v41
	v_sub_f32_e32 v32, v33, v41
	v_add_f32_e32 v33, v34, v35
	v_add_f32_e32 v29, v29, v32
	v_mul_f32_e32 v44, v33, v42
	v_sub_f32_e32 v32, v34, v33
	v_mul_f32_e32 v34, v41, v44
	v_fma_f32 v36, v44, v41, -v34
	v_fmac_f32_e32 v36, v44, v29
	v_add_f32_e32 v43, v35, v32
	v_add_f32_e32 v32, v34, v36
	v_sub_f32_e32 v35, v33, v32
	v_pk_add_f32 v[38:39], v[32:33], v[34:35] neg_lo:[0,1] neg_hi:[0,1]
	v_mov_b32_e32 v37, v32
	v_pk_add_f32 v[32:33], v[38:39], v[36:37] neg_lo:[0,1] neg_hi:[0,1]
	v_cmp_neq_f32_e32 vcc, s13, v25
	v_add_f32_e32 v33, v43, v33
	v_add_f32_e32 v32, v32, v33
	v_add_f32_e32 v33, v35, v32
	v_mul_f32_e32 v43, v42, v33
	v_mul_f32_e32 v34, v41, v43
	v_fma_f32 v36, v43, v41, -v34
	v_fmac_f32_e32 v36, v43, v29
	v_sub_f32_e32 v29, v35, v33
	v_add_f32_e32 v29, v32, v29
	v_add_f32_e32 v32, v34, v36
	v_sub_f32_e32 v35, v33, v32
	v_pk_add_f32 v[38:39], v[32:33], v[34:35] neg_lo:[0,1] neg_hi:[0,1]
	v_mov_b32_e32 v37, v32
	v_pk_add_f32 v[32:33], v[38:39], v[36:37] neg_lo:[0,1] neg_hi:[0,1]
	v_mov_b32_e32 v20, v4
	v_add_f32_e32 v29, v29, v33
	v_add_f32_e32 v29, v32, v29
	v_add_f32_e32 v33, v44, v43
	v_add_f32_e32 v29, v35, v29
	v_sub_f32_e32 v32, v33, v44
	v_mul_f32_e32 v29, v42, v29
	v_sub_f32_e32 v32, v43, v32
	v_add_f32_e32 v34, v32, v29
	v_add_f32_e32 v36, v33, v34
	v_cvt_f32_i32_e32 v32, v40
	v_mul_f32_e32 v37, v36, v36
	v_sub_f32_e32 v33, v36, v33
	v_fmamk_f32 v29, v37, 0x3e9b6dac, v55
	v_sub_f32_e32 v33, v34, v33
	v_fmaak_f32 v29, v37, v29, 0x3f2aaada
	v_ldexp_f32 v38, v33, 1
	v_mul_f32_e32 v33, v36, v37
	v_ldexp_f32 v35, v36, 1
	v_pk_mul_f32 v[36:37], v[32:33], v[28:29]
	v_mov_b32_e32 v21, v4
	v_fma_f32 v34, v32, s25, -v36
	v_fmac_f32_e32 v34, 0xb102e308, v32
	v_pk_add_f32 v[32:33], v[36:37], v[34:35]
	s_nop 0
	v_sub_f32_e32 v29, v33, v35
	v_sub_f32_e32 v29, v37, v29
	v_add_f32_e32 v39, v38, v29
	v_mov_b32_e32 v38, v36
	v_pk_add_f32 v[36:37], v[32:33], v[36:37] neg_lo:[0,1] neg_hi:[0,1]
	v_pk_add_f32 v[40:41], v[32:33], v[38:39]
	v_mov_b32_e32 v35, v32
	v_mov_b32_e32 v37, v41
	v_pk_add_f32 v[42:43], v[34:35], v[36:37] neg_lo:[0,1] neg_hi:[0,1]
	v_pk_add_f32 v[34:35], v[34:35], v[36:37]
	v_mov_b32_e32 v38, v39
	v_pk_add_f32 v[36:37], v[34:35], v[32:33] op_sel:[1,0] op_sel_hi:[0,1] neg_lo:[0,1] neg_hi:[0,1]
	v_pk_add_f32 v[44:45], v[40:41], v[36:37] op_sel_hi:[1,0] neg_lo:[0,1] neg_hi:[0,1]
	v_mov_b32_e32 v40, v41
	v_mov_b32_e32 v41, v35
	v_pk_mov_b32 v[36:37], v[32:33], v[36:37] op_sel:[1,0]
	v_mov_b32_e32 v39, v32
	v_pk_add_f32 v[36:37], v[40:41], v[36:37] neg_lo:[0,1] neg_hi:[0,1]
	v_mov_b32_e32 v44, v42
	v_pk_add_f32 v[32:33], v[38:39], v[36:37] neg_lo:[0,1] neg_hi:[0,1]
	v_mov_b32_e32 v43, v35
	v_pk_add_f32 v[36:37], v[44:45], v[32:33]
	s_nop 0
	v_pk_add_f32 v[38:39], v[36:37], v[36:37] op_sel:[0,1] op_sel_hi:[1,0]
	s_nop 0
	v_pk_add_f32 v[34:35], v[34:35], v[38:39] op_sel:[1,0] op_sel_hi:[0,1]
	v_mov_b32_e32 v37, v34
	v_pk_add_f32 v[40:41], v[36:37], v[42:43] neg_lo:[0,1] neg_hi:[0,1]
	v_mov_b32_e32 v33, v38
	v_sub_f32_e32 v29, v36, v40
	v_pk_add_f32 v[32:33], v[32:33], v[40:41] neg_lo:[0,1] neg_hi:[0,1]
	v_sub_f32_e32 v29, v42, v29
	v_add_f32_e32 v29, v32, v29
	v_add_f32_e32 v29, v29, v33
	v_add_f32_e32 v29, v34, v29
	v_cndmask_b32_e32 v29, v30, v29, vcc
	v_cmp_lt_f32_e64 vcc, |v25|, s15
	s_nop 1
	v_cndmask_b32_e32 v25, v29, v25, vcc
	v_add_f32_e32 v25, 0x358637bd, v25
	v_med3_f32 v29, v25, s24, v31
	v_div_scale_f32 v32, s[46:47], v29, v29, s14
	v_rcp_f32_e32 v33, v32
	v_cvt_pk_f16_f32 v25, v26, v27
	v_ldexp_f32 v26, v47, v48
	v_fma_f32 v27, -v32, v33, 1.0
	v_fmac_f32_e32 v33, v27, v33
	v_div_scale_f32 v27, vcc, s14, v29, s14
	v_mul_f32_e32 v34, v27, v33
	v_fma_f32 v35, -v32, v34, v27
	v_fmac_f32_e32 v34, v35, v33
	v_fma_f32 v27, -v32, v34, v27
	v_div_fmas_f32 v27, v27, v33, v34
	v_div_fixup_f32 v27, v27, v29, s14
	v_mul_f32_e32 v29, 0x3fb8aa3b, v27
	v_fma_f32 v32, v27, s3, -v29
	v_rndne_f32_e32 v33, v29
	v_fmac_f32_e32 v32, 0x32a5705f, v27
	v_sub_f32_e32 v29, v29, v33
	v_add_f32_e32 v29, v29, v32
	v_exp_f32_e32 v29, v29
	v_cvt_i32_f32_e32 v32, v33
	v_cmp_ngt_f32_e32 vcc, s7, v46
	v_ldexp_f32 v29, v29, v32
	s_nop 0
	v_cndmask_b32_e32 v26, 0, v26, vcc
	v_cmp_nlt_f32_e32 vcc, s12, v46
	s_nop 1
	v_cndmask_b32_e32 v26, v30, v26, vcc
	v_cmp_ngt_f32_e32 vcc, s7, v27
	v_cndmask_b32_e64 v50, v26, 0, s[4:5]
	s_nop 0
	v_cndmask_b32_e32 v29, 0, v29, vcc
	v_cmp_nlt_f32_e32 vcc, s12, v27
	s_nop 1
	v_cndmask_b32_e32 v27, v30, v29, vcc
	v_mul_f32_e32 v29, 0x3fb8aa3b, v52
	v_fma_f32 v32, v52, s3, -v29
	v_rndne_f32_e32 v33, v29
	v_fmac_f32_e32 v32, 0x32a5705f, v52
	v_sub_f32_e32 v29, v29, v33
	v_add_f32_e32 v29, v29, v32
	v_exp_f32_e32 v29, v29
	v_cvt_i32_f32_e32 v32, v33
	v_cmp_ngt_f32_e32 vcc, s7, v52
	v_cndmask_b32_e64 v51, v27, 0, s[4:5]
	v_pk_add_f32 v[26:27], v[26:27], 1.0 op_sel_hi:[1,0] neg_lo:[1,0] neg_hi:[1,0]
	v_ldexp_f32 v29, v29, v32
	v_cndmask_b32_e32 v29, 0, v29, vcc
	v_cmp_nlt_f32_e32 vcc, s12, v52
	v_cndmask_b32_e64 v52, v26, 0, s[4:5]
	v_cndmask_b32_e64 v53, v27, 0, s[4:5]
	v_cndmask_b32_e32 v46, v30, v29, vcc
	v_add_f32_e32 v29, 1.0, v46
	v_add_f32_e32 v32, -1.0, v29
	v_sub_f32_e32 v33, v32, v29
	v_add_f32_e32 v33, 1.0, v33
	v_sub_f32_e32 v32, v46, v32
	v_add_f32_e32 v34, v32, v33
	v_frexp_mant_f32_e32 v35, v29
	v_cvt_f64_f32_e32 v[32:33], v29
	v_frexp_exp_i32_f64_e32 v32, v[32:33]
	v_cmp_gt_f32_e32 vcc, s33, v35
	s_nop 1
	v_subbrev_co_u32_e32 v40, vcc, 0, v32, vcc
	v_sub_u32_e32 v32, 0, v40
	v_ldexp_f32 v29, v29, v32
	v_ldexp_f32 v32, v34, v32
	v_add_f32_e32 v34, -1.0, v29
	v_add_f32_e32 v33, 1.0, v34
	v_sub_f32_e32 v33, v29, v33
	v_add_f32_e32 v35, v32, v33
	v_add_f32_e32 v33, 1.0, v29
	v_add_f32_e32 v36, -1.0, v33
	v_sub_f32_e32 v29, v29, v36
	v_add_f32_e32 v29, v32, v29
	v_add_f32_e32 v41, v33, v29
	v_rcp_f32_e32 v42, v41
	v_sub_f32_e32 v32, v33, v41
	v_add_f32_e32 v33, v34, v35
	v_add_f32_e32 v29, v29, v32
	v_mul_f32_e32 v44, v33, v42
	v_sub_f32_e32 v32, v34, v33
	v_mul_f32_e32 v34, v41, v44
	v_fma_f32 v36, v44, v41, -v34
	v_fmac_f32_e32 v36, v44, v29
	v_add_f32_e32 v43, v35, v32
	v_add_f32_e32 v32, v34, v36
	v_sub_f32_e32 v35, v33, v32
	v_pk_add_f32 v[38:39], v[32:33], v[34:35] neg_lo:[0,1] neg_hi:[0,1]
	v_mov_b32_e32 v37, v32
	v_pk_add_f32 v[32:33], v[38:39], v[36:37] neg_lo:[0,1] neg_hi:[0,1]
	v_cmp_neq_f32_e32 vcc, s13, v46
	v_add_f32_e32 v33, v43, v33
	v_add_f32_e32 v32, v32, v33
	v_add_f32_e32 v33, v35, v32
	v_mul_f32_e32 v43, v42, v33
	v_mul_f32_e32 v34, v41, v43
	v_fma_f32 v36, v43, v41, -v34
	v_fmac_f32_e32 v36, v43, v29
	v_sub_f32_e32 v29, v35, v33
	v_add_f32_e32 v29, v32, v29
	v_add_f32_e32 v32, v34, v36
	v_sub_f32_e32 v35, v33, v32
	v_pk_add_f32 v[38:39], v[32:33], v[34:35] neg_lo:[0,1] neg_hi:[0,1]
	v_mov_b32_e32 v37, v32
	v_pk_add_f32 v[32:33], v[38:39], v[36:37] neg_lo:[0,1] neg_hi:[0,1]
	s_nop 0
	v_add_f32_e32 v29, v29, v33
	v_add_f32_e32 v29, v32, v29
	v_add_f32_e32 v33, v44, v43
	v_add_f32_e32 v29, v35, v29
	v_sub_f32_e32 v32, v33, v44
	v_mul_f32_e32 v29, v42, v29
	v_sub_f32_e32 v32, v43, v32
	v_add_f32_e32 v34, v32, v29
	v_add_f32_e32 v36, v33, v34
	v_cvt_f32_i32_e32 v32, v40
	v_mul_f32_e32 v37, v36, v36
	v_sub_f32_e32 v33, v36, v33
	v_fmamk_f32 v29, v37, 0x3e9b6dac, v55
	v_sub_f32_e32 v33, v34, v33
	v_fmaak_f32 v29, v37, v29, 0x3f2aaada
	v_ldexp_f32 v38, v33, 1
	v_mul_f32_e32 v33, v36, v37
	v_ldexp_f32 v35, v36, 1
	v_pk_mul_f32 v[36:37], v[32:33], v[28:29]
	s_nop 0
	v_fma_f32 v34, v32, s25, -v36
	v_fmac_f32_e32 v34, 0xb102e308, v32
	v_pk_add_f32 v[32:33], v[36:37], v[34:35]
	s_nop 0
	v_sub_f32_e32 v29, v33, v35
	v_sub_f32_e32 v29, v37, v29
	v_add_f32_e32 v39, v38, v29
	v_mov_b32_e32 v38, v36
	v_pk_add_f32 v[36:37], v[32:33], v[36:37] neg_lo:[0,1] neg_hi:[0,1]
	v_pk_add_f32 v[40:41], v[32:33], v[38:39]
	v_mov_b32_e32 v35, v32
	v_mov_b32_e32 v37, v41
	v_pk_add_f32 v[42:43], v[34:35], v[36:37] neg_lo:[0,1] neg_hi:[0,1]
	v_pk_add_f32 v[34:35], v[34:35], v[36:37]
	v_mov_b32_e32 v38, v39
	v_pk_add_f32 v[36:37], v[34:35], v[32:33] op_sel:[1,0] op_sel_hi:[0,1] neg_lo:[0,1] neg_hi:[0,1]
	v_pk_add_f32 v[44:45], v[40:41], v[36:37] op_sel_hi:[1,0] neg_lo:[0,1] neg_hi:[0,1]
	v_mov_b32_e32 v40, v41
	v_mov_b32_e32 v41, v35
	v_pk_mov_b32 v[36:37], v[32:33], v[36:37] op_sel:[1,0]
	v_mov_b32_e32 v39, v32
	v_pk_add_f32 v[36:37], v[40:41], v[36:37] neg_lo:[0,1] neg_hi:[0,1]
	v_mov_b32_e32 v44, v42
	v_pk_add_f32 v[32:33], v[38:39], v[36:37] neg_lo:[0,1] neg_hi:[0,1]
	v_mov_b32_e32 v43, v35
	v_pk_add_f32 v[36:37], v[44:45], v[32:33]
	s_nop 0
	v_pk_add_f32 v[38:39], v[36:37], v[36:37] op_sel:[0,1] op_sel_hi:[1,0]
	s_nop 0
	v_pk_add_f32 v[34:35], v[34:35], v[38:39] op_sel:[1,0] op_sel_hi:[0,1]
	v_mov_b32_e32 v37, v34
	v_pk_add_f32 v[40:41], v[36:37], v[42:43] neg_lo:[0,1] neg_hi:[0,1]
	v_mov_b32_e32 v33, v38
	v_sub_f32_e32 v29, v36, v40
	v_pk_add_f32 v[32:33], v[32:33], v[40:41] neg_lo:[0,1] neg_hi:[0,1]
	v_sub_f32_e32 v29, v42, v29
	v_add_f32_e32 v29, v32, v29
	v_add_f32_e32 v29, v29, v33
	v_add_f32_e32 v29, v34, v29
	v_cndmask_b32_e32 v29, v30, v29, vcc
	v_cmp_lt_f32_e64 vcc, |v46|, s15
	v_pk_mul_f32 v[32:33], v[26:27], -2.0 op_sel_hi:[1,0]
	s_nop 0
	v_cndmask_b32_e32 v29, v29, v46, vcc
	v_add_f32_e32 v29, 0x358637bd, v29
	v_med3_f32 v29, v29, s24, v31
	v_div_scale_f32 v34, s[46:47], v29, v29, s14
	v_rcp_f32_e32 v35, v34
	s_nop 0
	v_fma_f32 v26, -v34, v35, 1.0
	v_fmac_f32_e32 v35, v26, v35
	v_div_scale_f32 v26, vcc, s14, v29, s14
	v_mul_f32_e32 v27, v26, v35
	v_fma_f32 v36, -v34, v27, v26
	v_fmac_f32_e32 v27, v36, v35
	v_fma_f32 v26, -v34, v27, v26
	v_mul_f32_e32 v34, 0x3fb8aa3b, v54
	v_div_fmas_f32 v26, v26, v35, v27
	v_fma_f32 v35, v54, s3, -v34
	v_rndne_f32_e32 v36, v34
	v_fmac_f32_e32 v35, 0x32a5705f, v54
	v_sub_f32_e32 v34, v34, v36
	v_div_fixup_f32 v44, v26, v29, s14
	v_add_f32_e32 v34, v34, v35
	v_mul_f32_e32 v26, 0x3fb8aa3b, v44
	v_exp_f32_e32 v34, v34
	v_cvt_i32_f32_e32 v35, v36
	v_fma_f32 v27, v44, s3, -v26
	v_rndne_f32_e32 v29, v26
	v_fmac_f32_e32 v27, 0x32a5705f, v44
	v_sub_f32_e32 v26, v26, v29
	v_add_f32_e32 v26, v26, v27
	v_exp_f32_e32 v45, v26
	v_ldexp_f32 v26, v34, v35
	v_cmp_ngt_f32_e32 vcc, s7, v54
	v_cvt_i32_f32_e32 v46, v29
	s_nop 0
	v_cndmask_b32_e32 v26, 0, v26, vcc
	v_cmp_nlt_f32_e32 vcc, s12, v54
	v_cndmask_b32_e64 v54, v32, 0, s[4:5]
	s_nop 0
	v_cndmask_b32_e32 v47, v30, v26, vcc
	v_add_f32_e32 v29, 1.0, v47
	v_add_f32_e32 v26, -1.0, v29
	v_sub_f32_e32 v27, v26, v29
	v_add_f32_e32 v27, 1.0, v27
	v_sub_f32_e32 v26, v47, v26
	v_add_f32_e32 v34, v26, v27
	v_frexp_mant_f32_e32 v35, v29
	v_cvt_f64_f32_e32 v[26:27], v29
	v_frexp_exp_i32_f64_e32 v26, v[26:27]
	v_cmp_gt_f32_e32 vcc, s33, v35
	s_nop 1
	v_subbrev_co_u32_e32 v40, vcc, 0, v26, vcc
	v_sub_u32_e32 v26, 0, v40
	v_ldexp_f32 v27, v29, v26
	v_add_f32_e32 v29, -1.0, v27
	v_add_f32_e32 v35, 1.0, v27
	v_ldexp_f32 v26, v34, v26
	v_add_f32_e32 v34, 1.0, v29
	v_add_f32_e32 v36, -1.0, v35
	v_sub_f32_e32 v34, v27, v34
	v_sub_f32_e32 v27, v27, v36
	v_add_f32_e32 v34, v26, v34
	v_add_f32_e32 v26, v26, v27
	v_add_f32_e32 v41, v35, v26
	v_rcp_f32_e32 v43, v41
	v_sub_f32_e32 v27, v35, v41
	v_add_f32_e32 v42, v26, v27
	v_add_f32_e32 v27, v29, v34
	v_sub_f32_e32 v26, v29, v27
	v_mul_f32_e32 v48, v27, v43
	v_add_f32_e32 v29, v34, v26
	v_mul_f32_e32 v34, v41, v48
	v_fma_f32 v36, v48, v41, -v34
	v_fmac_f32_e32 v36, v48, v42
	v_add_f32_e32 v26, v34, v36
	v_sub_f32_e32 v35, v27, v26
	v_pk_add_f32 v[38:39], v[26:27], v[34:35] neg_lo:[0,1] neg_hi:[0,1]
	v_mov_b32_e32 v37, v26
	v_pk_add_f32 v[26:27], v[38:39], v[36:37] neg_lo:[0,1] neg_hi:[0,1]
	v_cmp_neq_f32_e32 vcc, s13, v47
	v_add_f32_e32 v27, v29, v27
	v_add_f32_e32 v26, v26, v27
	v_add_f32_e32 v27, v35, v26
	v_mul_f32_e32 v29, v43, v27
	v_mul_f32_e32 v34, v41, v29
	v_fma_f32 v36, v29, v41, -v34
	v_fmac_f32_e32 v36, v29, v42
	v_sub_f32_e32 v35, v35, v27
	v_add_f32_e32 v41, v26, v35
	v_add_f32_e32 v26, v34, v36
	v_sub_f32_e32 v35, v27, v26
	v_pk_add_f32 v[38:39], v[26:27], v[34:35] neg_lo:[0,1] neg_hi:[0,1]
	v_mov_b32_e32 v37, v26
	v_pk_add_f32 v[26:27], v[38:39], v[36:37] neg_lo:[0,1] neg_hi:[0,1]
	s_nop 0
	v_add_f32_e32 v27, v41, v27
	v_add_f32_e32 v26, v26, v27
	v_add_f32_e32 v27, v48, v29
	v_add_f32_e32 v26, v35, v26
	v_sub_f32_e32 v34, v27, v48
	v_mul_f32_e32 v26, v43, v26
	v_sub_f32_e32 v29, v29, v34
	v_add_f32_e32 v29, v29, v26
	v_add_f32_e32 v34, v27, v29
	v_mul_f32_e32 v36, v34, v34
	v_cvt_f32_i32_e32 v26, v40
	v_fmac_f32_e32 v55, 0x3e9b6dac, v36
	v_sub_f32_e32 v27, v34, v27
	v_fmac_f32_e32 v49, v36, v55
	v_sub_f32_e32 v27, v29, v27
	v_ldexp_f32 v37, v27, 1
	v_mul_f32_e32 v27, v34, v36
	v_mov_b32_e32 v29, v49
	v_pk_mul_f32 v[28:29], v[26:27], v[28:29]
	v_ldexp_f32 v35, v34, 1
	v_fma_f32 v34, v26, s25, -v28
	v_fmac_f32_e32 v34, 0xb102e308, v26
	v_pk_add_f32 v[26:27], v[28:29], v[34:35]
	v_mov_b32_e32 v36, v28
	v_sub_f32_e32 v35, v27, v35
	v_sub_f32_e32 v35, v29, v35
	v_add_f32_e32 v37, v37, v35
	v_pk_add_f32 v[28:29], v[26:27], v[28:29] neg_lo:[0,1] neg_hi:[0,1]
	v_pk_add_f32 v[38:39], v[26:27], v[36:37]
	v_mov_b32_e32 v35, v26
	v_mov_b32_e32 v29, v39
	v_pk_add_f32 v[40:41], v[34:35], v[28:29] neg_lo:[0,1] neg_hi:[0,1]
	v_pk_add_f32 v[28:29], v[34:35], v[28:29]
	v_mov_b32_e32 v36, v37
	v_pk_add_f32 v[34:35], v[28:29], v[26:27] op_sel:[1,0] op_sel_hi:[0,1] neg_lo:[0,1] neg_hi:[0,1]
	v_pk_add_f32 v[42:43], v[38:39], v[34:35] op_sel_hi:[1,0] neg_lo:[0,1] neg_hi:[0,1]
	v_mov_b32_e32 v38, v39
	v_mov_b32_e32 v39, v29
	v_pk_mov_b32 v[34:35], v[26:27], v[34:35] op_sel:[1,0]
	v_mov_b32_e32 v37, v26
	v_pk_add_f32 v[34:35], v[38:39], v[34:35] neg_lo:[0,1] neg_hi:[0,1]
	v_mov_b32_e32 v42, v40
	v_pk_add_f32 v[26:27], v[36:37], v[34:35] neg_lo:[0,1] neg_hi:[0,1]
	v_mov_b32_e32 v41, v29
	v_pk_add_f32 v[34:35], v[42:43], v[26:27]
	v_cndmask_b32_e64 v55, v33, 0, s[4:5]
	v_pk_add_f32 v[36:37], v[34:35], v[34:35] op_sel:[0,1] op_sel_hi:[1,0]
	s_nop 0
	v_pk_add_f32 v[28:29], v[28:29], v[36:37] op_sel:[1,0] op_sel_hi:[0,1]
	v_mov_b32_e32 v35, v28
	v_pk_add_f32 v[38:39], v[34:35], v[40:41] neg_lo:[0,1] neg_hi:[0,1]
	v_mov_b32_e32 v27, v36
	v_sub_f32_e32 v29, v34, v38
	v_pk_add_f32 v[26:27], v[26:27], v[38:39] neg_lo:[0,1] neg_hi:[0,1]
	v_sub_f32_e32 v29, v40, v29
	v_add_f32_e32 v26, v26, v29
	v_add_f32_e32 v26, v26, v27
	v_add_f32_e32 v26, v28, v26
	v_cndmask_b32_e32 v26, v30, v26, vcc
	v_cmp_lt_f32_e64 vcc, |v47|, s15
	v_ldexp_f32 v29, v45, v46
	s_nop 0
	v_cndmask_b32_e32 v26, v26, v47, vcc
	v_add_f32_e32 v26, 0x358637bd, v26
	v_med3_f32 v26, v26, s24, v31
	v_div_scale_f32 v27, s[24:25], v26, v26, s14
	v_rcp_f32_e32 v28, v27
	s_nop 0
	v_fma_f32 v31, -v27, v28, 1.0
	v_fmac_f32_e32 v28, v31, v28
	v_div_scale_f32 v31, vcc, s14, v26, s14
	v_mul_f32_e32 v32, v31, v28
	v_fma_f32 v33, -v27, v32, v31
	v_fmac_f32_e32 v32, v33, v28
	v_fma_f32 v27, -v27, v32, v31
	v_div_fmas_f32 v27, v27, v28, v32
	v_div_fixup_f32 v27, v27, v26, s14
	v_mul_f32_e32 v26, 0x3fb8aa3b, v27
	v_fma_f32 v28, v27, s3, -v26
	v_rndne_f32_e32 v31, v26
	v_fmac_f32_e32 v28, 0x32a5705f, v27
	v_sub_f32_e32 v26, v26, v31
	v_add_f32_e32 v26, v26, v28
	v_exp_f32_e32 v28, v26
	v_cvt_i32_f32_e32 v31, v31
	v_cmp_ngt_f32_e32 vcc, s7, v44
	s_movk_i32 s3, 0xc0
	v_mov_b32_e32 v32, v4
	v_cndmask_b32_e32 v26, 0, v29, vcc
	v_cmp_nlt_f32_e32 vcc, s12, v44
	v_ldexp_f32 v28, v28, v31
	v_mov_b32_e32 v31, v4
	v_cndmask_b32_e32 v26, v30, v26, vcc
	v_cmp_ngt_f32_e32 vcc, s7, v27
	v_cndmask_b32_e64 v56, v26, 0, s[4:5]
	v_cmp_eq_u32_e64 s[6:7], 0, v64
	v_cndmask_b32_e32 v28, 0, v28, vcc
	v_cmp_nlt_f32_e32 vcc, s12, v27
	v_mov_b32_e32 v33, v4
	s_nop 0
	v_cndmask_b32_e32 v27, v30, v28, vcc
	v_cndmask_b32_e64 v57, v27, 0, s[4:5]
	v_pk_add_f32 v[26:27], v[26:27], 1.0 op_sel_hi:[1,0] neg_lo:[1,0] neg_hi:[1,0]
	v_mov_b32_e32 v30, v4
	v_pk_mul_f32 v[28:29], v[26:27], -2.0 op_sel_hi:[1,0]
	v_cndmask_b32_e64 v59, v27, 0, s[4:5]
	v_cndmask_b32_e64 v60, v28, 0, s[4:5]
	v_lshlrev_b32_e32 v27, 6, v64
	v_mov_b32_e32 v28, 0x80
	v_cndmask_b32_e64 v27, v27, v28, s[4:5]
	v_mad_u32_u24 v27, v65, s3, v27
	v_cndmask_b32_e64 v58, v26, 0, s[4:5]
	v_mul_u32_u24_e32 v26, 0xc0, v65
	v_and_or_b32 v62, v0, 48, v27
	v_lshlrev_b32_e32 v27, 6, v65
	v_sub_u32_e32 v26, v26, v27
	v_lshl_add_u32 v26, v1, 5, v26
	v_cndmask_b32_e64 v61, v29, 0, s[4:5]
	v_lshl_or_b32 v63, v64, 3, v26
	v_cmp_gt_u32_e64 s[4:5], 2, v64
	s_mov_b32 s3, -2
	v_mov_b32_e32 v166, v6
	v_mov_b32_e32 v167, v7
	v_mov_b32_e32 v168, v8
	v_mov_b32_e32 v169, v9
	v_mov_b32_e32 v170, v2
	v_mov_b32_e32 v171, v3
	v_mov_b32_e32 v172, v4
	v_mov_b32_e32 v173, v5
	v_mov_b32_e32 v6, v166
	v_mov_b32_e32 v7, v168
	v_mov_b32_e32 v8, v170
	v_mov_b32_e32 v9, v172
	v_mov_b32_e32 v2, v167
	v_mov_b32_e32 v3, v169
	v_mov_b32_e32 v4, v171
	v_mov_b32_e32 v5, v173
	v_mov_b32_e32 v166, v10
	v_mov_b32_e32 v167, v11
	v_mov_b32_e32 v168, v12
	v_mov_b32_e32 v169, v13
	v_mov_b32_e32 v170, v14
	v_mov_b32_e32 v171, v15
	v_mov_b32_e32 v172, v16
	v_mov_b32_e32 v173, v17
	v_mov_b32_e32 v10, v166
	v_mov_b32_e32 v11, v168
	v_mov_b32_e32 v12, v170
	v_mov_b32_e32 v13, v172
	v_mov_b32_e32 v14, v167
	v_mov_b32_e32 v15, v169
	v_mov_b32_e32 v16, v171
	v_mov_b32_e32 v17, v173
	v_mov_b32_e32 v166, v18
	v_mov_b32_e32 v167, v19
	v_mov_b32_e32 v168, v20
	v_mov_b32_e32 v169, v21
	v_mov_b32_e32 v170, v22
	v_mov_b32_e32 v171, v23
	v_mov_b32_e32 v172, v24
	v_mov_b32_e32 v173, v25
	v_mov_b32_e32 v18, v166
	v_mov_b32_e32 v19, v168
	v_mov_b32_e32 v20, v170
	v_mov_b32_e32 v21, v172
	v_mov_b32_e32 v22, v167
	v_mov_b32_e32 v23, v169
	v_mov_b32_e32 v24, v171
	v_mov_b32_e32 v25, v173
	v_mov_b32_e32 v124, 0
	v_mov_b32_e32 v125, 0
	v_mov_b32_e32 v126, 0
	v_mov_b32_e32 v127, 0
	v_mov_b32_e32 v128, 0
	v_mov_b32_e32 v129, 0
	v_mov_b32_e32 v130, 0
	v_mov_b32_e32 v131, 0
	v_mov_b32_e32 v148, 0
	v_mov_b32_e32 v149, 0
	v_mov_b32_e32 v150, 0
	v_mov_b32_e32 v151, 0
	v_mov_b32_e32 v168, 0
	v_mov_b32_e32 v169, 0
	v_mov_b32_e32 v170, 0
	v_mov_b32_e32 v171, 0
	v_mov_b32_e32 v152, v52
	v_mov_b32_e32 v153, v53
	v_mov_b32_e32 v154, v58
	v_mov_b32_e32 v155, v59
	s_waitcnt lgkmcnt(0)
	s_barrier
	s_waitcnt lgkmcnt(0)
	s_barrier
	s_mov_b32 s3, 0
	v_mfma_f32_16x16x32_f16 v[132:135], v[6:9], v[124:127], v[168:171]
	v_mfma_f32_16x16x32_f16 v[136:139], v[10:13], v[124:127], v[168:171]
	v_mfma_f32_16x16x32_f16 v[140:143], v[18:21], v[124:127], v[168:171]
	s_nop 0
	v_mfma_f32_16x16x32_f16 v[132:135], v[2:5], v[128:131], v[132:135]
	s_nop 2
	v_mfma_f32_16x16x32_f16 v[136:139], v[14:17], v[128:131], v[136:139]
	s_nop 2
	v_mfma_f32_16x16x32_f16 v[140:143], v[22:25], v[128:131], v[140:143]
	s_branch .LBB3_49
.LBB3_48:
	v_mov_b32_e32 v164, v63
	v_mov_b32_e32 v165, v62
	s_nop 0
	ds_read_b128 v[64:67], v165 offset:33792
	s_waitcnt lgkmcnt(0)
	s_nop 2
	v_cndmask_b32_e64 v160, v136, v132, s[6:7]
	v_cndmask_b32_e64 v161, v137, v133, s[6:7]
	v_cndmask_b32_e64 v162, v138, v134, s[6:7]
	v_cndmask_b32_e64 v163, v139, v135, s[6:7]
	v_cndmask_b32_e64 v156, v140, v160, s[4:5]
	v_cndmask_b32_e64 v157, v141, v161, s[4:5]
	v_add_f32_e32 v156, v156, v64
	v_add_f32_e32 v157, v157, v65
	v_exp_f32_e32 v156, v156
	v_exp_f32_e32 v157, v157
	v_cndmask_b32_e64 v158, v142, v162, s[4:5]
	v_cndmask_b32_e64 v159, v143, v163, s[4:5]
	v_add_f32_e32 v158, v158, v66
	v_add_f32_e32 v159, v159, v67
	v_pk_add_f32 v[156:157], v[156:157], 1.0 op_sel_hi:[1,0]
	v_exp_f32_e32 v158, v158
	v_rcp_f32_e32 v156, v156
	v_rcp_f32_e32 v157, v157
	v_exp_f32_e32 v159, v159
	v_pk_fma_f32 v[148:149], v[54:55], v[156:157], v[152:153]
	v_pk_add_f32 v[158:159], v[158:159], 1.0 op_sel_hi:[1,0]
	v_cvt_pk_f16_f32 v124, v148, v149
	v_rcp_f32_e32 v158, v158
	v_rcp_f32_e32 v159, v159
	v_mov_b32_dpp v125, v124 quad_perm:[1,2,3,0] row_mask:0xf bank_mask:0xf bound_ctrl:1
	v_mov_b32_dpp v126, v124 quad_perm:[2,3,0,1] row_mask:0xf bank_mask:0xf bound_ctrl:1
	v_mov_b32_dpp v127, v124 quad_perm:[3,0,1,2] row_mask:0xf bank_mask:0xf bound_ctrl:1
	v_pk_fma_f32 v[150:151], v[60:61], v[158:159], v[154:155]
	s_nop 0
	v_cvt_pk_f16_f32 v128, v150, v151
	ds_write_b32 v164, v124 offset:16896
	s_nop 0
	v_mov_b32_dpp v129, v128 quad_perm:[1,2,3,0] row_mask:0xf bank_mask:0xf bound_ctrl:1
	v_mov_b32_dpp v130, v128 quad_perm:[2,3,0,1] row_mask:0xf bank_mask:0xf bound_ctrl:1
	v_mov_b32_dpp v131, v128 quad_perm:[3,0,1,2] row_mask:0xf bank_mask:0xf bound_ctrl:1
	ds_write_b32 v164, v128 offset:16900
	s_waitcnt lgkmcnt(0)
	s_barrier
	s_waitcnt lgkmcnt(0)
	s_barrier
	s_branch .LBB3_55
.LBB3_49:
	s_and_b32 s12, s3, 1
	s_mul_i32 s13, s12, 0x3100
	s_mulk_i32 s12, 0x2100
	v_add_u32_e32 v165, s13, v62
	v_add_u32_e32 v164, s12, v63
	s_nop 0
	ds_read_b128 v[64:67], v165 offset:33792
	ds_read_b128 v[68:71], v165 offset:34576
	ds_read_b128 v[72:75], v165 offset:35360
	ds_read_b128 v[76:79], v165 offset:36144
	ds_read_b128 v[80:83], v165 offset:36928
	ds_read_b128 v[84:87], v165 offset:37712
	ds_read_b128 v[88:91], v165 offset:38496
	ds_read_b128 v[92:95], v165 offset:39280
	ds_read_b128 v[96:99], v165 offset:40064
	ds_read_b128 v[100:103], v165 offset:40848
	ds_read_b128 v[104:107], v165 offset:41632
	ds_read_b128 v[108:111], v165 offset:42416
	ds_read_b128 v[112:115], v165 offset:43200
	ds_read_b128 v[116:119], v165 offset:43984
	ds_read_b128 v[120:123], v165 offset:44768
	ds_read_b128 v[44:47], v165 offset:45552
	s_waitcnt lgkmcnt(15)
	s_nop 2
	v_cndmask_b32_e64 v160, v136, v132, s[6:7]
	v_cndmask_b32_e64 v161, v137, v133, s[6:7]
	v_cndmask_b32_e64 v162, v138, v134, s[6:7]
	v_cndmask_b32_e64 v163, v139, v135, s[6:7]
	v_cndmask_b32_e64 v156, v140, v160, s[4:5]
	v_cndmask_b32_e64 v157, v141, v161, s[4:5]
	v_add_f32_e32 v156, v156, v64
	v_add_f32_e32 v157, v157, v65
	v_exp_f32_e32 v156, v156
	v_exp_f32_e32 v157, v157
	v_cndmask_b32_e64 v158, v142, v162, s[4:5]
	v_cndmask_b32_e64 v159, v143, v163, s[4:5]
	v_add_f32_e32 v158, v158, v66
	v_add_f32_e32 v159, v159, v67
	v_pk_add_f32 v[156:157], v[156:157], 1.0 op_sel_hi:[1,0]
	v_exp_f32_e32 v158, v158
	v_rcp_f32_e32 v156, v156
	v_rcp_f32_e32 v157, v157
	v_exp_f32_e32 v159, v159
	v_pk_fma_f32 v[148:149], v[54:55], v[156:157], v[152:153]
	v_pk_add_f32 v[158:159], v[158:159], 1.0 op_sel_hi:[1,0]
	v_cvt_pk_f16_f32 v124, v148, v149
	v_rcp_f32_e32 v158, v158
	v_rcp_f32_e32 v159, v159
	v_mov_b32_dpp v125, v124 quad_perm:[1,2,3,0] row_mask:0xf bank_mask:0xf bound_ctrl:1
	v_mov_b32_dpp v126, v124 quad_perm:[2,3,0,1] row_mask:0xf bank_mask:0xf bound_ctrl:1
	v_mov_b32_dpp v127, v124 quad_perm:[3,0,1,2] row_mask:0xf bank_mask:0xf bound_ctrl:1
	v_pk_fma_f32 v[150:151], v[60:61], v[158:159], v[154:155]
	s_waitcnt lgkmcnt(14)
	v_mfma_f32_16x16x32_f16 v[132:135], v[6:9], v[124:127], v[68:71]
	v_cvt_pk_f16_f32 v128, v150, v151
	s_nop 0
	v_mfma_f32_16x16x32_f16 v[136:139], v[10:13], v[124:127], v[68:71]
	v_mov_b32_dpp v129, v128 quad_perm:[1,2,3,0] row_mask:0xf bank_mask:0xf bound_ctrl:1
	v_mov_b32_dpp v130, v128 quad_perm:[2,3,0,1] row_mask:0xf bank_mask:0xf bound_ctrl:1
	v_mfma_f32_16x16x32_f16 v[140:143], v[18:21], v[124:127], v[68:71]
	v_mov_b32_dpp v131, v128 quad_perm:[3,0,1,2] row_mask:0xf bank_mask:0xf bound_ctrl:1
	s_nop 1
	v_mfma_f32_16x16x32_f16 v[132:135], v[2:5], v[128:131], v[132:135]
	v_fma_f32 v154, v56, v150, v58
	v_fma_f32 v155, v57, v151, v59
	ds_write_b32 v164, v124 offset:16896
	v_mfma_f32_16x16x32_f16 v[136:139], v[14:17], v[128:131], v[136:139]
	v_fma_f32 v152, v50, v148, v52
	v_fma_f32 v153, v51, v149, v53
	ds_write_b32 v164, v128 offset:16900
	v_mfma_f32_16x16x32_f16 v[140:143], v[22:25], v[128:131], v[140:143]
	s_nop 3
	v_cndmask_b32_e64 v160, v136, v132, s[6:7]
	v_cndmask_b32_e64 v161, v137, v133, s[6:7]
	v_cndmask_b32_e64 v162, v138, v134, s[6:7]
	v_cndmask_b32_e64 v163, v139, v135, s[6:7]
	v_cndmask_b32_e64 v156, v140, v160, s[4:5]
	v_cndmask_b32_e64 v157, v141, v161, s[4:5]
	v_exp_f32_e32 v156, v156
	v_exp_f32_e32 v157, v157
	v_cndmask_b32_e64 v158, v142, v162, s[4:5]
	v_cndmask_b32_e64 v159, v143, v163, s[4:5]
	v_pk_add_f32 v[156:157], v[156:157], 1.0 op_sel_hi:[1,0]
	v_exp_f32_e32 v158, v158
	v_rcp_f32_e32 v156, v156
	v_rcp_f32_e32 v157, v157
	v_exp_f32_e32 v159, v159
	v_pk_fma_f32 v[148:149], v[54:55], v[156:157], v[152:153]
	v_pk_add_f32 v[158:159], v[158:159], 1.0 op_sel_hi:[1,0]
	v_cvt_pk_f16_f32 v124, v148, v149
	v_rcp_f32_e32 v158, v158
	v_rcp_f32_e32 v159, v159
	v_mov_b32_dpp v125, v124 quad_perm:[1,2,3,0] row_mask:0xf bank_mask:0xf bound_ctrl:1
	v_mov_b32_dpp v126, v124 quad_perm:[2,3,0,1] row_mask:0xf bank_mask:0xf bound_ctrl:1
	v_mov_b32_dpp v127, v124 quad_perm:[3,0,1,2] row_mask:0xf bank_mask:0xf bound_ctrl:1
	v_pk_fma_f32 v[150:151], v[60:61], v[158:159], v[154:155]
	s_waitcnt lgkmcnt(15)
	v_mfma_f32_16x16x32_f16 v[132:135], v[6:9], v[124:127], v[72:75]
	v_cvt_pk_f16_f32 v128, v150, v151
	s_nop 0
	v_mfma_f32_16x16x32_f16 v[136:139], v[10:13], v[124:127], v[72:75]
	v_mov_b32_dpp v129, v128 quad_perm:[1,2,3,0] row_mask:0xf bank_mask:0xf bound_ctrl:1
	v_mov_b32_dpp v130, v128 quad_perm:[2,3,0,1] row_mask:0xf bank_mask:0xf bound_ctrl:1
	v_mfma_f32_16x16x32_f16 v[140:143], v[18:21], v[124:127], v[72:75]
	v_mov_b32_dpp v131, v128 quad_perm:[3,0,1,2] row_mask:0xf bank_mask:0xf bound_ctrl:1
	s_nop 1
	v_mfma_f32_16x16x32_f16 v[132:135], v[2:5], v[128:131], v[132:135]
	v_fma_f32 v154, v56, v150, v58
	v_fma_f32 v155, v57, v151, v59
	ds_write_b32 v164, v124 offset:17424
	v_mfma_f32_16x16x32_f16 v[136:139], v[14:17], v[128:131], v[136:139]
	v_fma_f32 v152, v50, v148, v52
	v_fma_f32 v153, v51, v149, v53
	ds_write_b32 v164, v128 offset:17428
	v_mfma_f32_16x16x32_f16 v[140:143], v[22:25], v[128:131], v[140:143]
	s_nop 3
	v_cndmask_b32_e64 v160, v136, v132, s[6:7]
	v_cndmask_b32_e64 v161, v137, v133, s[6:7]
	v_cndmask_b32_e64 v162, v138, v134, s[6:7]
	v_cndmask_b32_e64 v163, v139, v135, s[6:7]
	v_cndmask_b32_e64 v156, v140, v160, s[4:5]
	v_cndmask_b32_e64 v157, v141, v161, s[4:5]
	v_exp_f32_e32 v156, v156
	v_exp_f32_e32 v157, v157
	v_cndmask_b32_e64 v158, v142, v162, s[4:5]
	v_cndmask_b32_e64 v159, v143, v163, s[4:5]
	v_pk_add_f32 v[156:157], v[156:157], 1.0 op_sel_hi:[1,0]
	v_exp_f32_e32 v158, v158
	v_rcp_f32_e32 v156, v156
	v_rcp_f32_e32 v157, v157
	v_exp_f32_e32 v159, v159
	v_pk_fma_f32 v[148:149], v[54:55], v[156:157], v[152:153]
	v_pk_add_f32 v[158:159], v[158:159], 1.0 op_sel_hi:[1,0]
	v_cvt_pk_f16_f32 v124, v148, v149
	v_rcp_f32_e32 v158, v158
	v_rcp_f32_e32 v159, v159
	v_mov_b32_dpp v125, v124 quad_perm:[1,2,3,0] row_mask:0xf bank_mask:0xf bound_ctrl:1
	v_mov_b32_dpp v126, v124 quad_perm:[2,3,0,1] row_mask:0xf bank_mask:0xf bound_ctrl:1
	v_mov_b32_dpp v127, v124 quad_perm:[3,0,1,2] row_mask:0xf bank_mask:0xf bound_ctrl:1
	v_pk_fma_f32 v[150:151], v[60:61], v[158:159], v[154:155]
	s_waitcnt lgkmcnt(15)
	v_mfma_f32_16x16x32_f16 v[132:135], v[6:9], v[124:127], v[76:79]
	v_cvt_pk_f16_f32 v128, v150, v151
	s_nop 0
	v_mfma_f32_16x16x32_f16 v[136:139], v[10:13], v[124:127], v[76:79]
	v_mov_b32_dpp v129, v128 quad_perm:[1,2,3,0] row_mask:0xf bank_mask:0xf bound_ctrl:1
	v_mov_b32_dpp v130, v128 quad_perm:[2,3,0,1] row_mask:0xf bank_mask:0xf bound_ctrl:1
	v_mfma_f32_16x16x32_f16 v[140:143], v[18:21], v[124:127], v[76:79]
	v_mov_b32_dpp v131, v128 quad_perm:[3,0,1,2] row_mask:0xf bank_mask:0xf bound_ctrl:1
	s_nop 1
	v_mfma_f32_16x16x32_f16 v[132:135], v[2:5], v[128:131], v[132:135]
	v_fma_f32 v154, v56, v150, v58
	v_fma_f32 v155, v57, v151, v59
	ds_write_b32 v164, v124 offset:17952
	v_mfma_f32_16x16x32_f16 v[136:139], v[14:17], v[128:131], v[136:139]
	v_fma_f32 v152, v50, v148, v52
	v_fma_f32 v153, v51, v149, v53
	ds_write_b32 v164, v128 offset:17956
	v_mfma_f32_16x16x32_f16 v[140:143], v[22:25], v[128:131], v[140:143]
	s_nop 3
	v_cndmask_b32_e64 v160, v136, v132, s[6:7]
	v_cndmask_b32_e64 v161, v137, v133, s[6:7]
	v_cndmask_b32_e64 v162, v138, v134, s[6:7]
	v_cndmask_b32_e64 v163, v139, v135, s[6:7]
	v_cndmask_b32_e64 v156, v140, v160, s[4:5]
	v_cndmask_b32_e64 v157, v141, v161, s[4:5]
	v_exp_f32_e32 v156, v156
	v_exp_f32_e32 v157, v157
	v_cndmask_b32_e64 v158, v142, v162, s[4:5]
	v_cndmask_b32_e64 v159, v143, v163, s[4:5]
	v_pk_add_f32 v[156:157], v[156:157], 1.0 op_sel_hi:[1,0]
	v_exp_f32_e32 v158, v158
	v_rcp_f32_e32 v156, v156
	v_rcp_f32_e32 v157, v157
	v_exp_f32_e32 v159, v159
	v_pk_fma_f32 v[148:149], v[54:55], v[156:157], v[152:153]
	v_pk_add_f32 v[158:159], v[158:159], 1.0 op_sel_hi:[1,0]
	v_cvt_pk_f16_f32 v124, v148, v149
	v_rcp_f32_e32 v158, v158
	v_rcp_f32_e32 v159, v159
	v_mov_b32_dpp v125, v124 quad_perm:[1,2,3,0] row_mask:0xf bank_mask:0xf bound_ctrl:1
	v_mov_b32_dpp v126, v124 quad_perm:[2,3,0,1] row_mask:0xf bank_mask:0xf bound_ctrl:1
	v_mov_b32_dpp v127, v124 quad_perm:[3,0,1,2] row_mask:0xf bank_mask:0xf bound_ctrl:1
	v_pk_fma_f32 v[150:151], v[60:61], v[158:159], v[154:155]
	s_waitcnt lgkmcnt(15)
	v_mfma_f32_16x16x32_f16 v[132:135], v[6:9], v[124:127], v[80:83]
	v_cvt_pk_f16_f32 v128, v150, v151
	s_nop 0
	v_mfma_f32_16x16x32_f16 v[136:139], v[10:13], v[124:127], v[80:83]
	v_mov_b32_dpp v129, v128 quad_perm:[1,2,3,0] row_mask:0xf bank_mask:0xf bound_ctrl:1
	v_mov_b32_dpp v130, v128 quad_perm:[2,3,0,1] row_mask:0xf bank_mask:0xf bound_ctrl:1
	v_mfma_f32_16x16x32_f16 v[140:143], v[18:21], v[124:127], v[80:83]
	v_mov_b32_dpp v131, v128 quad_perm:[3,0,1,2] row_mask:0xf bank_mask:0xf bound_ctrl:1
	s_nop 1
	v_mfma_f32_16x16x32_f16 v[132:135], v[2:5], v[128:131], v[132:135]
	v_fma_f32 v154, v56, v150, v58
	v_fma_f32 v155, v57, v151, v59
	ds_write_b32 v164, v124 offset:18480
	v_mfma_f32_16x16x32_f16 v[136:139], v[14:17], v[128:131], v[136:139]
	v_fma_f32 v152, v50, v148, v52
	v_fma_f32 v153, v51, v149, v53
	ds_write_b32 v164, v128 offset:18484
	v_mfma_f32_16x16x32_f16 v[140:143], v[22:25], v[128:131], v[140:143]
	s_nop 3
	v_cndmask_b32_e64 v160, v136, v132, s[6:7]
	v_cndmask_b32_e64 v161, v137, v133, s[6:7]
	v_cndmask_b32_e64 v162, v138, v134, s[6:7]
	v_cndmask_b32_e64 v163, v139, v135, s[6:7]
	v_cndmask_b32_e64 v156, v140, v160, s[4:5]
	v_cndmask_b32_e64 v157, v141, v161, s[4:5]
	v_exp_f32_e32 v156, v156
	v_exp_f32_e32 v157, v157
	v_cndmask_b32_e64 v158, v142, v162, s[4:5]
	v_cndmask_b32_e64 v159, v143, v163, s[4:5]
	v_pk_add_f32 v[156:157], v[156:157], 1.0 op_sel_hi:[1,0]
	v_exp_f32_e32 v158, v158
	v_rcp_f32_e32 v156, v156
	v_rcp_f32_e32 v157, v157
	v_exp_f32_e32 v159, v159
	v_pk_fma_f32 v[148:149], v[54:55], v[156:157], v[152:153]
	v_pk_add_f32 v[158:159], v[158:159], 1.0 op_sel_hi:[1,0]
	v_cvt_pk_f16_f32 v124, v148, v149
	v_rcp_f32_e32 v158, v158
	v_rcp_f32_e32 v159, v159
	v_mov_b32_dpp v125, v124 quad_perm:[1,2,3,0] row_mask:0xf bank_mask:0xf bound_ctrl:1
	v_mov_b32_dpp v126, v124 quad_perm:[2,3,0,1] row_mask:0xf bank_mask:0xf bound_ctrl:1
	v_mov_b32_dpp v127, v124 quad_perm:[3,0,1,2] row_mask:0xf bank_mask:0xf bound_ctrl:1
	v_pk_fma_f32 v[150:151], v[60:61], v[158:159], v[154:155]
	s_waitcnt lgkmcnt(15)
	v_mfma_f32_16x16x32_f16 v[132:135], v[6:9], v[124:127], v[84:87]
	v_cvt_pk_f16_f32 v128, v150, v151
	s_nop 0
	v_mfma_f32_16x16x32_f16 v[136:139], v[10:13], v[124:127], v[84:87]
	v_mov_b32_dpp v129, v128 quad_perm:[1,2,3,0] row_mask:0xf bank_mask:0xf bound_ctrl:1
	v_mov_b32_dpp v130, v128 quad_perm:[2,3,0,1] row_mask:0xf bank_mask:0xf bound_ctrl:1
	v_mfma_f32_16x16x32_f16 v[140:143], v[18:21], v[124:127], v[84:87]
	v_mov_b32_dpp v131, v128 quad_perm:[3,0,1,2] row_mask:0xf bank_mask:0xf bound_ctrl:1
	s_nop 1
	v_mfma_f32_16x16x32_f16 v[132:135], v[2:5], v[128:131], v[132:135]
	v_fma_f32 v154, v56, v150, v58
	v_fma_f32 v155, v57, v151, v59
	ds_write_b32 v164, v124 offset:19008
	v_mfma_f32_16x16x32_f16 v[136:139], v[14:17], v[128:131], v[136:139]
	v_fma_f32 v152, v50, v148, v52
	v_fma_f32 v153, v51, v149, v53
	ds_write_b32 v164, v128 offset:19012
	v_mfma_f32_16x16x32_f16 v[140:143], v[22:25], v[128:131], v[140:143]
	s_nop 3
	v_cndmask_b32_e64 v160, v136, v132, s[6:7]
	v_cndmask_b32_e64 v161, v137, v133, s[6:7]
	v_cndmask_b32_e64 v162, v138, v134, s[6:7]
	v_cndmask_b32_e64 v163, v139, v135, s[6:7]
	v_cndmask_b32_e64 v156, v140, v160, s[4:5]
	v_cndmask_b32_e64 v157, v141, v161, s[4:5]
	v_exp_f32_e32 v156, v156
	v_exp_f32_e32 v157, v157
	v_cndmask_b32_e64 v158, v142, v162, s[4:5]
	v_cndmask_b32_e64 v159, v143, v163, s[4:5]
	v_pk_add_f32 v[156:157], v[156:157], 1.0 op_sel_hi:[1,0]
	v_exp_f32_e32 v158, v158
	v_rcp_f32_e32 v156, v156
	v_rcp_f32_e32 v157, v157
	v_exp_f32_e32 v159, v159
	v_pk_fma_f32 v[148:149], v[54:55], v[156:157], v[152:153]
	v_pk_add_f32 v[158:159], v[158:159], 1.0 op_sel_hi:[1,0]
	v_cvt_pk_f16_f32 v124, v148, v149
	v_rcp_f32_e32 v158, v158
	v_rcp_f32_e32 v159, v159
	v_mov_b32_dpp v125, v124 quad_perm:[1,2,3,0] row_mask:0xf bank_mask:0xf bound_ctrl:1
	v_mov_b32_dpp v126, v124 quad_perm:[2,3,0,1] row_mask:0xf bank_mask:0xf bound_ctrl:1
	v_mov_b32_dpp v127, v124 quad_perm:[3,0,1,2] row_mask:0xf bank_mask:0xf bound_ctrl:1
	v_pk_fma_f32 v[150:151], v[60:61], v[158:159], v[154:155]
	s_waitcnt lgkmcnt(15)
	v_mfma_f32_16x16x32_f16 v[132:135], v[6:9], v[124:127], v[88:91]
	v_cvt_pk_f16_f32 v128, v150, v151
	s_nop 0
	v_mfma_f32_16x16x32_f16 v[136:139], v[10:13], v[124:127], v[88:91]
	v_mov_b32_dpp v129, v128 quad_perm:[1,2,3,0] row_mask:0xf bank_mask:0xf bound_ctrl:1
	v_mov_b32_dpp v130, v128 quad_perm:[2,3,0,1] row_mask:0xf bank_mask:0xf bound_ctrl:1
	v_mfma_f32_16x16x32_f16 v[140:143], v[18:21], v[124:127], v[88:91]
	v_mov_b32_dpp v131, v128 quad_perm:[3,0,1,2] row_mask:0xf bank_mask:0xf bound_ctrl:1
	s_nop 1
	v_mfma_f32_16x16x32_f16 v[132:135], v[2:5], v[128:131], v[132:135]
	v_fma_f32 v154, v56, v150, v58
	v_fma_f32 v155, v57, v151, v59
	ds_write_b32 v164, v124 offset:19536
	v_mfma_f32_16x16x32_f16 v[136:139], v[14:17], v[128:131], v[136:139]
	v_fma_f32 v152, v50, v148, v52
	v_fma_f32 v153, v51, v149, v53
	ds_write_b32 v164, v128 offset:19540
	v_mfma_f32_16x16x32_f16 v[140:143], v[22:25], v[128:131], v[140:143]
	s_nop 3
	v_cndmask_b32_e64 v160, v136, v132, s[6:7]
	v_cndmask_b32_e64 v161, v137, v133, s[6:7]
	v_cndmask_b32_e64 v162, v138, v134, s[6:7]
	v_cndmask_b32_e64 v163, v139, v135, s[6:7]
	v_cndmask_b32_e64 v156, v140, v160, s[4:5]
	v_cndmask_b32_e64 v157, v141, v161, s[4:5]
	v_exp_f32_e32 v156, v156
	v_exp_f32_e32 v157, v157
	v_cndmask_b32_e64 v158, v142, v162, s[4:5]
	v_cndmask_b32_e64 v159, v143, v163, s[4:5]
	v_pk_add_f32 v[156:157], v[156:157], 1.0 op_sel_hi:[1,0]
	v_exp_f32_e32 v158, v158
	v_rcp_f32_e32 v156, v156
	v_rcp_f32_e32 v157, v157
	v_exp_f32_e32 v159, v159
	v_pk_fma_f32 v[148:149], v[54:55], v[156:157], v[152:153]
	v_pk_add_f32 v[158:159], v[158:159], 1.0 op_sel_hi:[1,0]
	v_cvt_pk_f16_f32 v124, v148, v149
	v_rcp_f32_e32 v158, v158
	v_rcp_f32_e32 v159, v159
	v_mov_b32_dpp v125, v124 quad_perm:[1,2,3,0] row_mask:0xf bank_mask:0xf bound_ctrl:1
	v_mov_b32_dpp v126, v124 quad_perm:[2,3,0,1] row_mask:0xf bank_mask:0xf bound_ctrl:1
	v_mov_b32_dpp v127, v124 quad_perm:[3,0,1,2] row_mask:0xf bank_mask:0xf bound_ctrl:1
	v_pk_fma_f32 v[150:151], v[60:61], v[158:159], v[154:155]
	s_waitcnt lgkmcnt(15)
	v_mfma_f32_16x16x32_f16 v[132:135], v[6:9], v[124:127], v[92:95]
	v_cvt_pk_f16_f32 v128, v150, v151
	s_nop 0
	v_mfma_f32_16x16x32_f16 v[136:139], v[10:13], v[124:127], v[92:95]
	v_mov_b32_dpp v129, v128 quad_perm:[1,2,3,0] row_mask:0xf bank_mask:0xf bound_ctrl:1
	v_mov_b32_dpp v130, v128 quad_perm:[2,3,0,1] row_mask:0xf bank_mask:0xf bound_ctrl:1
	v_mfma_f32_16x16x32_f16 v[140:143], v[18:21], v[124:127], v[92:95]
	v_mov_b32_dpp v131, v128 quad_perm:[3,0,1,2] row_mask:0xf bank_mask:0xf bound_ctrl:1
	s_nop 1
	v_mfma_f32_16x16x32_f16 v[132:135], v[2:5], v[128:131], v[132:135]
	v_fma_f32 v154, v56, v150, v58
	v_fma_f32 v155, v57, v151, v59
	ds_write_b32 v164, v124 offset:20064
	v_mfma_f32_16x16x32_f16 v[136:139], v[14:17], v[128:131], v[136:139]
	v_fma_f32 v152, v50, v148, v52
	v_fma_f32 v153, v51, v149, v53
	ds_write_b32 v164, v128 offset:20068
	v_mfma_f32_16x16x32_f16 v[140:143], v[22:25], v[128:131], v[140:143]
	s_nop 3
	v_cndmask_b32_e64 v160, v136, v132, s[6:7]
	v_cndmask_b32_e64 v161, v137, v133, s[6:7]
	v_cndmask_b32_e64 v162, v138, v134, s[6:7]
	v_cndmask_b32_e64 v163, v139, v135, s[6:7]
	v_cndmask_b32_e64 v156, v140, v160, s[4:5]
	v_cndmask_b32_e64 v157, v141, v161, s[4:5]
	v_exp_f32_e32 v156, v156
	v_exp_f32_e32 v157, v157
	v_cndmask_b32_e64 v158, v142, v162, s[4:5]
	v_cndmask_b32_e64 v159, v143, v163, s[4:5]
	v_pk_add_f32 v[156:157], v[156:157], 1.0 op_sel_hi:[1,0]
	v_exp_f32_e32 v158, v158
	v_rcp_f32_e32 v156, v156
	v_rcp_f32_e32 v157, v157
	v_exp_f32_e32 v159, v159
	v_pk_fma_f32 v[148:149], v[54:55], v[156:157], v[152:153]
	v_pk_add_f32 v[158:159], v[158:159], 1.0 op_sel_hi:[1,0]
	v_cvt_pk_f16_f32 v124, v148, v149
	v_rcp_f32_e32 v158, v158
	v_rcp_f32_e32 v159, v159
	v_mov_b32_dpp v125, v124 quad_perm:[1,2,3,0] row_mask:0xf bank_mask:0xf bound_ctrl:1
	v_mov_b32_dpp v126, v124 quad_perm:[2,3,0,1] row_mask:0xf bank_mask:0xf bound_ctrl:1
	v_mov_b32_dpp v127, v124 quad_perm:[3,0,1,2] row_mask:0xf bank_mask:0xf bound_ctrl:1
	v_pk_fma_f32 v[150:151], v[60:61], v[158:159], v[154:155]
	s_waitcnt lgkmcnt(15)
	v_mfma_f32_16x16x32_f16 v[132:135], v[6:9], v[124:127], v[96:99]
	v_cvt_pk_f16_f32 v128, v150, v151
	s_nop 0
	v_mfma_f32_16x16x32_f16 v[136:139], v[10:13], v[124:127], v[96:99]
	v_mov_b32_dpp v129, v128 quad_perm:[1,2,3,0] row_mask:0xf bank_mask:0xf bound_ctrl:1
	v_mov_b32_dpp v130, v128 quad_perm:[2,3,0,1] row_mask:0xf bank_mask:0xf bound_ctrl:1
	v_mfma_f32_16x16x32_f16 v[140:143], v[18:21], v[124:127], v[96:99]
	v_mov_b32_dpp v131, v128 quad_perm:[3,0,1,2] row_mask:0xf bank_mask:0xf bound_ctrl:1
	s_nop 1
	v_mfma_f32_16x16x32_f16 v[132:135], v[2:5], v[128:131], v[132:135]
	v_fma_f32 v154, v56, v150, v58
	v_fma_f32 v155, v57, v151, v59
	ds_write_b32 v164, v124 offset:20592
	v_mfma_f32_16x16x32_f16 v[136:139], v[14:17], v[128:131], v[136:139]
	v_fma_f32 v152, v50, v148, v52
	v_fma_f32 v153, v51, v149, v53
	ds_write_b32 v164, v128 offset:20596
	v_mfma_f32_16x16x32_f16 v[140:143], v[22:25], v[128:131], v[140:143]
	s_nop 3
	v_cndmask_b32_e64 v160, v136, v132, s[6:7]
	v_cndmask_b32_e64 v161, v137, v133, s[6:7]
	v_cndmask_b32_e64 v162, v138, v134, s[6:7]
	v_cndmask_b32_e64 v163, v139, v135, s[6:7]
	v_cndmask_b32_e64 v156, v140, v160, s[4:5]
	v_cndmask_b32_e64 v157, v141, v161, s[4:5]
	v_exp_f32_e32 v156, v156
	v_exp_f32_e32 v157, v157
	v_cndmask_b32_e64 v158, v142, v162, s[4:5]
	v_cndmask_b32_e64 v159, v143, v163, s[4:5]
	v_pk_add_f32 v[156:157], v[156:157], 1.0 op_sel_hi:[1,0]
	v_exp_f32_e32 v158, v158
	v_rcp_f32_e32 v156, v156
	v_rcp_f32_e32 v157, v157
	v_exp_f32_e32 v159, v159
	v_pk_fma_f32 v[148:149], v[54:55], v[156:157], v[152:153]
	v_pk_add_f32 v[158:159], v[158:159], 1.0 op_sel_hi:[1,0]
	v_cvt_pk_f16_f32 v124, v148, v149
	v_rcp_f32_e32 v158, v158
	v_rcp_f32_e32 v159, v159
	v_mov_b32_dpp v125, v124 quad_perm:[1,2,3,0] row_mask:0xf bank_mask:0xf bound_ctrl:1
	v_mov_b32_dpp v126, v124 quad_perm:[2,3,0,1] row_mask:0xf bank_mask:0xf bound_ctrl:1
	v_mov_b32_dpp v127, v124 quad_perm:[3,0,1,2] row_mask:0xf bank_mask:0xf bound_ctrl:1
	v_pk_fma_f32 v[150:151], v[60:61], v[158:159], v[154:155]
	s_waitcnt lgkmcnt(15)
	v_mfma_f32_16x16x32_f16 v[132:135], v[6:9], v[124:127], v[100:103]
	v_cvt_pk_f16_f32 v128, v150, v151
	s_nop 0
	v_mfma_f32_16x16x32_f16 v[136:139], v[10:13], v[124:127], v[100:103]
	v_mov_b32_dpp v129, v128 quad_perm:[1,2,3,0] row_mask:0xf bank_mask:0xf bound_ctrl:1
	v_mov_b32_dpp v130, v128 quad_perm:[2,3,0,1] row_mask:0xf bank_mask:0xf bound_ctrl:1
	v_mfma_f32_16x16x32_f16 v[140:143], v[18:21], v[124:127], v[100:103]
	v_mov_b32_dpp v131, v128 quad_perm:[3,0,1,2] row_mask:0xf bank_mask:0xf bound_ctrl:1
	s_nop 1
	v_mfma_f32_16x16x32_f16 v[132:135], v[2:5], v[128:131], v[132:135]
	v_fma_f32 v154, v56, v150, v58
	v_fma_f32 v155, v57, v151, v59
	ds_write_b32 v164, v124 offset:21120
	v_mfma_f32_16x16x32_f16 v[136:139], v[14:17], v[128:131], v[136:139]
	v_fma_f32 v152, v50, v148, v52
	v_fma_f32 v153, v51, v149, v53
	ds_write_b32 v164, v128 offset:21124
	v_mfma_f32_16x16x32_f16 v[140:143], v[22:25], v[128:131], v[140:143]
	s_nop 3
	v_cndmask_b32_e64 v160, v136, v132, s[6:7]
	v_cndmask_b32_e64 v161, v137, v133, s[6:7]
	v_cndmask_b32_e64 v162, v138, v134, s[6:7]
	v_cndmask_b32_e64 v163, v139, v135, s[6:7]
	v_cndmask_b32_e64 v156, v140, v160, s[4:5]
	v_cndmask_b32_e64 v157, v141, v161, s[4:5]
	v_exp_f32_e32 v156, v156
	v_exp_f32_e32 v157, v157
	v_cndmask_b32_e64 v158, v142, v162, s[4:5]
	v_cndmask_b32_e64 v159, v143, v163, s[4:5]
	v_pk_add_f32 v[156:157], v[156:157], 1.0 op_sel_hi:[1,0]
	v_exp_f32_e32 v158, v158
	v_rcp_f32_e32 v156, v156
	v_rcp_f32_e32 v157, v157
	v_exp_f32_e32 v159, v159
	v_pk_fma_f32 v[148:149], v[54:55], v[156:157], v[152:153]
	v_pk_add_f32 v[158:159], v[158:159], 1.0 op_sel_hi:[1,0]
	v_cvt_pk_f16_f32 v124, v148, v149
	v_rcp_f32_e32 v158, v158
	v_rcp_f32_e32 v159, v159
	v_mov_b32_dpp v125, v124 quad_perm:[1,2,3,0] row_mask:0xf bank_mask:0xf bound_ctrl:1
	v_mov_b32_dpp v126, v124 quad_perm:[2,3,0,1] row_mask:0xf bank_mask:0xf bound_ctrl:1
	v_mov_b32_dpp v127, v124 quad_perm:[3,0,1,2] row_mask:0xf bank_mask:0xf bound_ctrl:1
	v_pk_fma_f32 v[150:151], v[60:61], v[158:159], v[154:155]
	s_waitcnt lgkmcnt(15)
	v_mfma_f32_16x16x32_f16 v[132:135], v[6:9], v[124:127], v[104:107]
	v_cvt_pk_f16_f32 v128, v150, v151
	s_nop 0
	v_mfma_f32_16x16x32_f16 v[136:139], v[10:13], v[124:127], v[104:107]
	v_mov_b32_dpp v129, v128 quad_perm:[1,2,3,0] row_mask:0xf bank_mask:0xf bound_ctrl:1
	v_mov_b32_dpp v130, v128 quad_perm:[2,3,0,1] row_mask:0xf bank_mask:0xf bound_ctrl:1
	v_mfma_f32_16x16x32_f16 v[140:143], v[18:21], v[124:127], v[104:107]
	v_mov_b32_dpp v131, v128 quad_perm:[3,0,1,2] row_mask:0xf bank_mask:0xf bound_ctrl:1
	s_nop 1
	v_mfma_f32_16x16x32_f16 v[132:135], v[2:5], v[128:131], v[132:135]
	v_fma_f32 v154, v56, v150, v58
	v_fma_f32 v155, v57, v151, v59
	ds_write_b32 v164, v124 offset:21648
	v_mfma_f32_16x16x32_f16 v[136:139], v[14:17], v[128:131], v[136:139]
	v_fma_f32 v152, v50, v148, v52
	v_fma_f32 v153, v51, v149, v53
	ds_write_b32 v164, v128 offset:21652
	v_mfma_f32_16x16x32_f16 v[140:143], v[22:25], v[128:131], v[140:143]
	s_nop 3
	v_cndmask_b32_e64 v160, v136, v132, s[6:7]
	v_cndmask_b32_e64 v161, v137, v133, s[6:7]
	v_cndmask_b32_e64 v162, v138, v134, s[6:7]
	v_cndmask_b32_e64 v163, v139, v135, s[6:7]
	v_cndmask_b32_e64 v156, v140, v160, s[4:5]
	v_cndmask_b32_e64 v157, v141, v161, s[4:5]
	v_exp_f32_e32 v156, v156
	v_exp_f32_e32 v157, v157
	v_cndmask_b32_e64 v158, v142, v162, s[4:5]
	v_cndmask_b32_e64 v159, v143, v163, s[4:5]
	v_pk_add_f32 v[156:157], v[156:157], 1.0 op_sel_hi:[1,0]
	v_exp_f32_e32 v158, v158
	v_rcp_f32_e32 v156, v156
	v_rcp_f32_e32 v157, v157
	v_exp_f32_e32 v159, v159
	v_pk_fma_f32 v[148:149], v[54:55], v[156:157], v[152:153]
	v_pk_add_f32 v[158:159], v[158:159], 1.0 op_sel_hi:[1,0]
	v_cvt_pk_f16_f32 v124, v148, v149
	v_rcp_f32_e32 v158, v158
	v_rcp_f32_e32 v159, v159
	v_mov_b32_dpp v125, v124 quad_perm:[1,2,3,0] row_mask:0xf bank_mask:0xf bound_ctrl:1
	v_mov_b32_dpp v126, v124 quad_perm:[2,3,0,1] row_mask:0xf bank_mask:0xf bound_ctrl:1
	v_mov_b32_dpp v127, v124 quad_perm:[3,0,1,2] row_mask:0xf bank_mask:0xf bound_ctrl:1
	v_pk_fma_f32 v[150:151], v[60:61], v[158:159], v[154:155]
	s_waitcnt lgkmcnt(15)
	v_mfma_f32_16x16x32_f16 v[132:135], v[6:9], v[124:127], v[108:111]
	v_cvt_pk_f16_f32 v128, v150, v151
	s_nop 0
	v_mfma_f32_16x16x32_f16 v[136:139], v[10:13], v[124:127], v[108:111]
	v_mov_b32_dpp v129, v128 quad_perm:[1,2,3,0] row_mask:0xf bank_mask:0xf bound_ctrl:1
	v_mov_b32_dpp v130, v128 quad_perm:[2,3,0,1] row_mask:0xf bank_mask:0xf bound_ctrl:1
	v_mfma_f32_16x16x32_f16 v[140:143], v[18:21], v[124:127], v[108:111]
	v_mov_b32_dpp v131, v128 quad_perm:[3,0,1,2] row_mask:0xf bank_mask:0xf bound_ctrl:1
	s_nop 1
	v_mfma_f32_16x16x32_f16 v[132:135], v[2:5], v[128:131], v[132:135]
	v_fma_f32 v154, v56, v150, v58
	v_fma_f32 v155, v57, v151, v59
	ds_write_b32 v164, v124 offset:22176
	v_mfma_f32_16x16x32_f16 v[136:139], v[14:17], v[128:131], v[136:139]
	v_fma_f32 v152, v50, v148, v52
	v_fma_f32 v153, v51, v149, v53
	ds_write_b32 v164, v128 offset:22180
	v_mfma_f32_16x16x32_f16 v[140:143], v[22:25], v[128:131], v[140:143]
	s_nop 3
	v_cndmask_b32_e64 v160, v136, v132, s[6:7]
	v_cndmask_b32_e64 v161, v137, v133, s[6:7]
	v_cndmask_b32_e64 v162, v138, v134, s[6:7]
	v_cndmask_b32_e64 v163, v139, v135, s[6:7]
	v_cndmask_b32_e64 v156, v140, v160, s[4:5]
	v_cndmask_b32_e64 v157, v141, v161, s[4:5]
	v_exp_f32_e32 v156, v156
	v_exp_f32_e32 v157, v157
	v_cndmask_b32_e64 v158, v142, v162, s[4:5]
	v_cndmask_b32_e64 v159, v143, v163, s[4:5]
	v_pk_add_f32 v[156:157], v[156:157], 1.0 op_sel_hi:[1,0]
	v_exp_f32_e32 v158, v158
	v_rcp_f32_e32 v156, v156
	v_rcp_f32_e32 v157, v157
	v_exp_f32_e32 v159, v159
	v_pk_fma_f32 v[148:149], v[54:55], v[156:157], v[152:153]
	v_pk_add_f32 v[158:159], v[158:159], 1.0 op_sel_hi:[1,0]
	v_cvt_pk_f16_f32 v124, v148, v149
	v_rcp_f32_e32 v158, v158
	v_rcp_f32_e32 v159, v159
	v_mov_b32_dpp v125, v124 quad_perm:[1,2,3,0] row_mask:0xf bank_mask:0xf bound_ctrl:1
	v_mov_b32_dpp v126, v124 quad_perm:[2,3,0,1] row_mask:0xf bank_mask:0xf bound_ctrl:1
	v_mov_b32_dpp v127, v124 quad_perm:[3,0,1,2] row_mask:0xf bank_mask:0xf bound_ctrl:1
	v_pk_fma_f32 v[150:151], v[60:61], v[158:159], v[154:155]
	s_waitcnt lgkmcnt(15)
	v_mfma_f32_16x16x32_f16 v[132:135], v[6:9], v[124:127], v[112:115]
	v_cvt_pk_f16_f32 v128, v150, v151
	s_nop 0
	v_mfma_f32_16x16x32_f16 v[136:139], v[10:13], v[124:127], v[112:115]
	v_mov_b32_dpp v129, v128 quad_perm:[1,2,3,0] row_mask:0xf bank_mask:0xf bound_ctrl:1
	v_mov_b32_dpp v130, v128 quad_perm:[2,3,0,1] row_mask:0xf bank_mask:0xf bound_ctrl:1
	v_mfma_f32_16x16x32_f16 v[140:143], v[18:21], v[124:127], v[112:115]
	v_mov_b32_dpp v131, v128 quad_perm:[3,0,1,2] row_mask:0xf bank_mask:0xf bound_ctrl:1
	s_nop 1
	v_mfma_f32_16x16x32_f16 v[132:135], v[2:5], v[128:131], v[132:135]
	v_fma_f32 v154, v56, v150, v58
	v_fma_f32 v155, v57, v151, v59
	ds_write_b32 v164, v124 offset:22704
	v_mfma_f32_16x16x32_f16 v[136:139], v[14:17], v[128:131], v[136:139]
	v_fma_f32 v152, v50, v148, v52
	v_fma_f32 v153, v51, v149, v53
	ds_write_b32 v164, v128 offset:22708
	v_mfma_f32_16x16x32_f16 v[140:143], v[22:25], v[128:131], v[140:143]
	s_nop 3
	v_cndmask_b32_e64 v160, v136, v132, s[6:7]
	v_cndmask_b32_e64 v161, v137, v133, s[6:7]
	v_cndmask_b32_e64 v162, v138, v134, s[6:7]
	v_cndmask_b32_e64 v163, v139, v135, s[6:7]
	v_cndmask_b32_e64 v156, v140, v160, s[4:5]
	v_cndmask_b32_e64 v157, v141, v161, s[4:5]
	v_exp_f32_e32 v156, v156
	v_exp_f32_e32 v157, v157
	v_cndmask_b32_e64 v158, v142, v162, s[4:5]
	v_cndmask_b32_e64 v159, v143, v163, s[4:5]
	v_pk_add_f32 v[156:157], v[156:157], 1.0 op_sel_hi:[1,0]
	v_exp_f32_e32 v158, v158
	v_rcp_f32_e32 v156, v156
	v_rcp_f32_e32 v157, v157
	v_exp_f32_e32 v159, v159
	v_pk_fma_f32 v[148:149], v[54:55], v[156:157], v[152:153]
	v_pk_add_f32 v[158:159], v[158:159], 1.0 op_sel_hi:[1,0]
	v_cvt_pk_f16_f32 v124, v148, v149
	v_rcp_f32_e32 v158, v158
	v_rcp_f32_e32 v159, v159
	v_mov_b32_dpp v125, v124 quad_perm:[1,2,3,0] row_mask:0xf bank_mask:0xf bound_ctrl:1
	v_mov_b32_dpp v126, v124 quad_perm:[2,3,0,1] row_mask:0xf bank_mask:0xf bound_ctrl:1
	v_mov_b32_dpp v127, v124 quad_perm:[3,0,1,2] row_mask:0xf bank_mask:0xf bound_ctrl:1
	v_pk_fma_f32 v[150:151], v[60:61], v[158:159], v[154:155]
	s_waitcnt lgkmcnt(15)
	v_mfma_f32_16x16x32_f16 v[132:135], v[6:9], v[124:127], v[116:119]
	v_cvt_pk_f16_f32 v128, v150, v151
	s_nop 0
	v_mfma_f32_16x16x32_f16 v[136:139], v[10:13], v[124:127], v[116:119]
	v_mov_b32_dpp v129, v128 quad_perm:[1,2,3,0] row_mask:0xf bank_mask:0xf bound_ctrl:1
	v_mov_b32_dpp v130, v128 quad_perm:[2,3,0,1] row_mask:0xf bank_mask:0xf bound_ctrl:1
	v_mfma_f32_16x16x32_f16 v[140:143], v[18:21], v[124:127], v[116:119]
	v_mov_b32_dpp v131, v128 quad_perm:[3,0,1,2] row_mask:0xf bank_mask:0xf bound_ctrl:1
	s_nop 1
	v_mfma_f32_16x16x32_f16 v[132:135], v[2:5], v[128:131], v[132:135]
	v_fma_f32 v154, v56, v150, v58
	v_fma_f32 v155, v57, v151, v59
	ds_write_b32 v164, v124 offset:23232
	v_mfma_f32_16x16x32_f16 v[136:139], v[14:17], v[128:131], v[136:139]
	v_fma_f32 v152, v50, v148, v52
	v_fma_f32 v153, v51, v149, v53
	ds_write_b32 v164, v128 offset:23236
	v_mfma_f32_16x16x32_f16 v[140:143], v[22:25], v[128:131], v[140:143]
	s_nop 3
	v_cndmask_b32_e64 v160, v136, v132, s[6:7]
	v_cndmask_b32_e64 v161, v137, v133, s[6:7]
	v_cndmask_b32_e64 v162, v138, v134, s[6:7]
	v_cndmask_b32_e64 v163, v139, v135, s[6:7]
	v_cndmask_b32_e64 v156, v140, v160, s[4:5]
	v_cndmask_b32_e64 v157, v141, v161, s[4:5]
	v_exp_f32_e32 v156, v156
	v_exp_f32_e32 v157, v157
	v_cndmask_b32_e64 v158, v142, v162, s[4:5]
	v_cndmask_b32_e64 v159, v143, v163, s[4:5]
	v_pk_add_f32 v[156:157], v[156:157], 1.0 op_sel_hi:[1,0]
	v_exp_f32_e32 v158, v158
	v_rcp_f32_e32 v156, v156
	v_rcp_f32_e32 v157, v157
	v_exp_f32_e32 v159, v159
	v_pk_fma_f32 v[148:149], v[54:55], v[156:157], v[152:153]
	v_pk_add_f32 v[158:159], v[158:159], 1.0 op_sel_hi:[1,0]
	v_cvt_pk_f16_f32 v124, v148, v149
	v_rcp_f32_e32 v158, v158
	v_rcp_f32_e32 v159, v159
	v_mov_b32_dpp v125, v124 quad_perm:[1,2,3,0] row_mask:0xf bank_mask:0xf bound_ctrl:1
	v_mov_b32_dpp v126, v124 quad_perm:[2,3,0,1] row_mask:0xf bank_mask:0xf bound_ctrl:1
	v_mov_b32_dpp v127, v124 quad_perm:[3,0,1,2] row_mask:0xf bank_mask:0xf bound_ctrl:1
	v_pk_fma_f32 v[150:151], v[60:61], v[158:159], v[154:155]
	s_waitcnt lgkmcnt(15)
	v_mfma_f32_16x16x32_f16 v[132:135], v[6:9], v[124:127], v[120:123]
	v_cvt_pk_f16_f32 v128, v150, v151
	s_nop 0
	v_mfma_f32_16x16x32_f16 v[136:139], v[10:13], v[124:127], v[120:123]
	v_mov_b32_dpp v129, v128 quad_perm:[1,2,3,0] row_mask:0xf bank_mask:0xf bound_ctrl:1
	v_mov_b32_dpp v130, v128 quad_perm:[2,3,0,1] row_mask:0xf bank_mask:0xf bound_ctrl:1
	v_mfma_f32_16x16x32_f16 v[140:143], v[18:21], v[124:127], v[120:123]
	v_mov_b32_dpp v131, v128 quad_perm:[3,0,1,2] row_mask:0xf bank_mask:0xf bound_ctrl:1
	s_nop 1
	v_mfma_f32_16x16x32_f16 v[132:135], v[2:5], v[128:131], v[132:135]
	v_fma_f32 v154, v56, v150, v58
	v_fma_f32 v155, v57, v151, v59
	ds_write_b32 v164, v124 offset:23760
	v_mfma_f32_16x16x32_f16 v[136:139], v[14:17], v[128:131], v[136:139]
	v_fma_f32 v152, v50, v148, v52
	v_fma_f32 v153, v51, v149, v53
	ds_write_b32 v164, v128 offset:23764
	v_mfma_f32_16x16x32_f16 v[140:143], v[22:25], v[128:131], v[140:143]
	s_nop 3
	v_cndmask_b32_e64 v160, v136, v132, s[6:7]
	v_cndmask_b32_e64 v161, v137, v133, s[6:7]
	v_cndmask_b32_e64 v162, v138, v134, s[6:7]
	v_cndmask_b32_e64 v163, v139, v135, s[6:7]
	v_cndmask_b32_e64 v156, v140, v160, s[4:5]
	v_cndmask_b32_e64 v157, v141, v161, s[4:5]
	v_exp_f32_e32 v156, v156
	v_exp_f32_e32 v157, v157
	v_cndmask_b32_e64 v158, v142, v162, s[4:5]
	v_cndmask_b32_e64 v159, v143, v163, s[4:5]
	v_pk_add_f32 v[156:157], v[156:157], 1.0 op_sel_hi:[1,0]
	v_exp_f32_e32 v158, v158
	v_rcp_f32_e32 v156, v156
	v_rcp_f32_e32 v157, v157
	v_exp_f32_e32 v159, v159
	v_pk_fma_f32 v[148:149], v[54:55], v[156:157], v[152:153]
	v_pk_add_f32 v[158:159], v[158:159], 1.0 op_sel_hi:[1,0]
	v_cvt_pk_f16_f32 v124, v148, v149
	v_rcp_f32_e32 v158, v158
	v_rcp_f32_e32 v159, v159
	v_mov_b32_dpp v125, v124 quad_perm:[1,2,3,0] row_mask:0xf bank_mask:0xf bound_ctrl:1
	v_mov_b32_dpp v126, v124 quad_perm:[2,3,0,1] row_mask:0xf bank_mask:0xf bound_ctrl:1
	v_mov_b32_dpp v127, v124 quad_perm:[3,0,1,2] row_mask:0xf bank_mask:0xf bound_ctrl:1
	v_pk_fma_f32 v[150:151], v[60:61], v[158:159], v[154:155]
	s_waitcnt lgkmcnt(15)
	v_mfma_f32_16x16x32_f16 v[132:135], v[6:9], v[124:127], v[44:47]
	v_cvt_pk_f16_f32 v128, v150, v151
	s_nop 0
	v_mfma_f32_16x16x32_f16 v[136:139], v[10:13], v[124:127], v[44:47]
	v_mov_b32_dpp v129, v128 quad_perm:[1,2,3,0] row_mask:0xf bank_mask:0xf bound_ctrl:1
	v_mov_b32_dpp v130, v128 quad_perm:[2,3,0,1] row_mask:0xf bank_mask:0xf bound_ctrl:1
	v_mfma_f32_16x16x32_f16 v[140:143], v[18:21], v[124:127], v[44:47]
	v_mov_b32_dpp v131, v128 quad_perm:[3,0,1,2] row_mask:0xf bank_mask:0xf bound_ctrl:1
	s_nop 1
	v_mfma_f32_16x16x32_f16 v[132:135], v[2:5], v[128:131], v[132:135]
	v_fma_f32 v154, v56, v150, v58
	v_fma_f32 v155, v57, v151, v59
	ds_write_b32 v164, v124 offset:24288
	v_mfma_f32_16x16x32_f16 v[136:139], v[14:17], v[128:131], v[136:139]
	v_fma_f32 v152, v50, v148, v52
	v_fma_f32 v153, v51, v149, v53
	ds_write_b32 v164, v128 offset:24292
	v_mfma_f32_16x16x32_f16 v[140:143], v[22:25], v[128:131], v[140:143]
	s_nop 3
	v_cndmask_b32_e64 v160, v136, v132, s[6:7]
	v_cndmask_b32_e64 v161, v137, v133, s[6:7]
	v_cndmask_b32_e64 v162, v138, v134, s[6:7]
	v_cndmask_b32_e64 v163, v139, v135, s[6:7]
	v_cndmask_b32_e64 v156, v140, v160, s[4:5]
	v_cndmask_b32_e64 v157, v141, v161, s[4:5]
	v_exp_f32_e32 v156, v156
	v_exp_f32_e32 v157, v157
	v_cndmask_b32_e64 v158, v142, v162, s[4:5]
	v_cndmask_b32_e64 v159, v143, v163, s[4:5]
	v_pk_add_f32 v[156:157], v[156:157], 1.0 op_sel_hi:[1,0]
	v_exp_f32_e32 v158, v158
	v_rcp_f32_e32 v156, v156
	v_rcp_f32_e32 v157, v157
	v_exp_f32_e32 v159, v159
	v_pk_fma_f32 v[148:149], v[54:55], v[156:157], v[152:153]
	v_pk_add_f32 v[158:159], v[158:159], 1.0 op_sel_hi:[1,0]
	v_cvt_pk_f16_f32 v124, v148, v149
	v_rcp_f32_e32 v158, v158
	v_rcp_f32_e32 v159, v159
	v_mov_b32_dpp v125, v124 quad_perm:[1,2,3,0] row_mask:0xf bank_mask:0xf bound_ctrl:1
	v_mov_b32_dpp v126, v124 quad_perm:[2,3,0,1] row_mask:0xf bank_mask:0xf bound_ctrl:1
	v_mov_b32_dpp v127, v124 quad_perm:[3,0,1,2] row_mask:0xf bank_mask:0xf bound_ctrl:1
	v_pk_fma_f32 v[150:151], v[60:61], v[158:159], v[154:155]
	s_nop 0
	v_mfma_f32_16x16x32_f16 v[132:135], v[6:9], v[124:127], v[168:171]
	v_cvt_pk_f16_f32 v128, v150, v151
	s_nop 0
	v_mfma_f32_16x16x32_f16 v[136:139], v[10:13], v[124:127], v[168:171]
	v_mov_b32_dpp v129, v128 quad_perm:[1,2,3,0] row_mask:0xf bank_mask:0xf bound_ctrl:1
	v_mov_b32_dpp v130, v128 quad_perm:[2,3,0,1] row_mask:0xf bank_mask:0xf bound_ctrl:1
	v_mfma_f32_16x16x32_f16 v[140:143], v[18:21], v[124:127], v[168:171]
	v_mov_b32_dpp v131, v128 quad_perm:[3,0,1,2] row_mask:0xf bank_mask:0xf bound_ctrl:1
	ds_write_b32 v164, v124 offset:24816
	ds_write_b32 v164, v128 offset:24820
	s_waitcnt lgkmcnt(0)
	s_barrier
	s_add_i32 s3, s3, 1
	v_mfma_f32_16x16x32_f16 v[132:135], v[2:5], v[128:131], v[132:135]
	v_fma_f32 v154, v56, v150, v58
	v_fma_f32 v155, v57, v151, v59
	s_nop 0
	v_mfma_f32_16x16x32_f16 v[136:139], v[14:17], v[128:131], v[136:139]
	v_fma_f32 v152, v50, v148, v52
	v_fma_f32 v153, v51, v149, v53
	s_nop 0
	v_mfma_f32_16x16x32_f16 v[140:143], v[22:25], v[128:131], v[140:143]
	s_cmp_lt_u32 s3, 64
	s_cbranch_scc1 .LBB3_49
	s_branch .LBB3_48

.LBB3_166:
	s_waitcnt lgkmcnt(0)
	s_andn2_saveexec_b64 s[8:9], s[38:39]
	s_cbranch_execz .LBB3_175
	s_load_dwordx4 s[4:7], s[0:1], 0xa8
	s_load_dwordx2 s[2:3], s[0:1], 0xb8
	v_lshrrev_b32_e32 v29, 2, v0
	v_lshlrev_b32_e32 v49, 6, v0
	v_and_b32_e32 v41, 12, v29
	v_and_b32_e32 v45, 0x3c0, v49
	v_or_b32_e32 v53, 3, v29
	v_or_b32_e32 v2, v41, v45
	v_or_b32_e32 v5, v53, v45
	v_lshlrev_b32_e32 v21, 2, v2
	v_lshlrev_b32_e32 v13, 2, v5
	v_or_b32_e32 v89, 19, v29
	s_waitcnt lgkmcnt(0)
	global_load_dwordx3 v[2:4], v21, s[4:5]
	global_load_dwordx3 v[6:8], v21, s[6:7]
	global_load_dword v5, v13, s[4:5]
	global_load_dword v9, v13, s[6:7]
	global_load_dwordx3 v[10:12], v21, s[4:5] offset:64
	global_load_dwordx3 v[14:16], v21, s[6:7] offset:64
	v_or_b32_e32 v13, v89, v45
	v_lshlrev_b32_e32 v25, 2, v13
	v_or_b32_e32 v93, 35, v29
	v_or_b32_e32 v61, 0x400, v45
	global_load_dword v13, v25, s[4:5]
	global_load_dword v17, v25, s[6:7]
	global_load_dwordx3 v[18:20], v21, s[4:5] offset:128
	global_load_dwordx3 v[22:24], v21, s[6:7] offset:128
	v_or_b32_e32 v25, v93, v45
	global_load_dwordx3 v[26:28], v21, s[4:5] offset:192
	global_load_dwordx3 v[30:32], v21, s[6:7] offset:192
	v_or_b32_e32 v21, v61, v41
	v_lshlrev_b32_e32 v62, 2, v21
	v_lshlrev_b32_e32 v33, 2, v25
	global_load_dwordx3 v[34:36], v62, s[4:5] offset:64
	global_load_dwordx3 v[42:44], v62, s[6:7] offset:64
	global_load_dword v21, v33, s[4:5]
	global_load_dword v25, v33, s[6:7]
	v_or_b32_e32 v81, 51, v29
	v_or_b32_e32 v29, v81, v45
	v_lshlrev_b32_e32 v37, 2, v29
	global_load_dword v29, v37, s[4:5]
	global_load_dword v33, v37, s[6:7]
	v_or_b32_e32 v37, v61, v89
	v_lshlrev_b32_e32 v38, 2, v37
	global_load_dword v37, v38, s[4:5]
	global_load_dword v39, v38, s[6:7]
	global_load_dwordx3 v[46:48], v62, s[4:5] offset:128
	global_load_dwordx3 v[50:52], v62, s[6:7] offset:128
	v_or_b32_e32 v38, v61, v93
	v_lshlrev_b32_e32 v38, 2, v38
	global_load_dword v63, v38, s[4:5]
	global_load_dword v95, v38, s[6:7]
	global_load_dwordx3 v[54:56], v62, s[4:5] offset:192
	global_load_dwordx3 v[58:60], v62, s[6:7] offset:192
	s_mov_b32 s0, 0x4038aa3b
	s_mov_b32 s10, 0x3f2aaaab
	s_mov_b32 s11, 0x3f317218
	v_or_b32_e32 v40, s34, v65
	v_lshlrev_b32_e32 v118, 6, v64
	v_lshlrev_b32_e32 v65, 7, v65
	s_waitcnt vmcnt(24)
	v_pk_mul_f32 v[2:3], v[2:3], v[6:7]
	s_waitcnt vmcnt(20)
	v_pk_mul_f32 v[6:7], v[10:11], v[14:15]
	v_pk_mul_f32 v[4:5], v[4:5], v[8:9]
	v_pk_mul_f32 v[6:7], v[6:7], s[0:1] op_sel_hi:[1,0]
	s_waitcnt vmcnt(18)
	v_pk_mul_f32 v[8:9], v[12:13], v[16:17]
	v_pk_mul_f32 v[2:3], v[2:3], s[0:1] op_sel_hi:[1,0]
	s_waitcnt vmcnt(16)
	v_pk_mul_f32 v[10:11], v[18:19], v[22:23]
	v_pk_mul_f32 v[22:23], v[8:9], s[0:1] op_sel_hi:[1,0]
	v_pk_mul_f32 v[10:11], v[10:11], s[0:1] op_sel_hi:[1,0]
	s_waitcnt vmcnt(14)
	v_pk_mul_f32 v[14:15], v[26:27], v[30:31]
	v_cvt_pk_f16_f32 v2, v2, v3
	v_pk_mul_f32 v[14:15], v[14:15], s[0:1] op_sel_hi:[1,0]
	s_waitcnt vmcnt(12)
	v_pk_mul_f32 v[18:19], v[34:35], v[42:43]
	s_waitcnt vmcnt(10)
	v_pk_mul_f32 v[12:13], v[20:21], v[24:25]
	v_pk_mul_f32 v[20:21], v[4:5], s[0:1] op_sel_hi:[1,0]
	v_cvt_pk_f16_f32 v4, v6, v7
	v_cvt_pk_f16_f32 v6, v10, v11
	v_pk_mul_f32 v[10:11], v[12:13], s[0:1] op_sel_hi:[1,0]
	s_waitcnt vmcnt(8)
	v_pk_mul_f32 v[16:17], v[28:29], v[32:33]
	v_cvt_pk_f16_f32 v7, v10, v11
	v_or_b32_e32 v10, v61, v81
	v_or_b32_e32 v11, v61, v53
	v_pk_mul_f32 v[18:19], v[18:19], s[0:1] op_sel_hi:[1,0]
	v_cvt_pk_f16_f32 v8, v14, v15
	v_lshlrev_b32_e32 v10, 2, v10
	v_lshlrev_b32_e32 v11, 2, v11
	v_or_b32_e32 v14, 0x800, v45
	v_pk_mul_f32 v[12:13], v[16:17], s[0:1] op_sel_hi:[1,0]
	v_cvt_pk_f16_f32 v3, v20, v21
	v_cvt_pk_f16_f32 v5, v22, v23
	global_load_dword v33, v10, s[4:5]
	global_load_dword v57, v10, s[6:7]
	v_cvt_pk_f16_f32 v10, v18, v19
	v_mov_b32_e32 v38, v44
	global_load_dwordx3 v[16:18], v62, s[4:5]
	global_load_dwordx3 v[20:22], v62, s[6:7]
	global_load_dword v19, v11, s[4:5]
	global_load_dword v23, v11, s[6:7]
	v_or_b32_e32 v11, v14, v41
	v_cvt_pk_f16_f32 v9, v12, v13
	s_waitcnt vmcnt(12)
	v_pk_mul_f32 v[12:13], v[36:37], v[38:39]
	v_lshlrev_b32_e32 v15, 2, v11
	v_or_b32_e32 v11, v14, v93
	v_pk_mul_f32 v[12:13], v[12:13], s[0:1] op_sel_hi:[1,0]
	v_lshlrev_b32_e32 v11, 2, v11
	global_load_dwordx3 v[24:26], v15, s[4:5] offset:128
	global_load_dwordx3 v[28:30], v15, s[6:7] offset:128
	global_load_dword v27, v11, s[4:5]
	global_load_dword v31, v11, s[6:7]
	v_cvt_pk_f16_f32 v11, v12, v13
	s_waitcnt vmcnt(14)
	v_pk_mul_f32 v[12:13], v[46:47], v[50:51]
	v_or_b32_e32 v32, v14, v81
	v_pk_mul_f32 v[12:13], v[12:13], s[0:1] op_sel_hi:[1,0]
	global_load_dwordx3 v[42:44], v15, s[4:5] offset:192
	global_load_dwordx3 v[66:68], v15, s[6:7] offset:192
	v_lshlrev_b32_e32 v32, 2, v32
	v_cvt_pk_f16_f32 v12, v12, v13
	v_or_b32_e32 v13, v14, v53
	global_load_dword v39, v32, s[4:5]
	global_load_dword v45, v32, s[6:7]
	v_lshlrev_b32_e32 v13, 2, v13
	global_load_dwordx3 v[70:72], v15, s[4:5]
	global_load_dwordx3 v[74:76], v15, s[6:7]
	global_load_dword v61, v13, s[4:5]
	global_load_dword v69, v13, s[6:7]
	global_load_dwordx3 v[78:80], v15, s[4:5] offset:64
	global_load_dwordx3 v[82:84], v15, s[6:7] offset:64
	v_or_b32_e32 v13, v14, v89
	v_lshlrev_b32_e32 v13, 2, v13
	v_or_b32_e32 v38, 0xc00, v49
	global_load_dword v73, v13, s[4:5]
	global_load_dword v77, v13, s[6:7]
	v_or_b32_e32 v13, v41, v38
	v_lshlrev_b32_e32 v32, 2, v13
	v_or_b32_e32 v13, v81, v38
	global_load_dwordx3 v[86:88], v32, s[4:5] offset:192
	global_load_dwordx3 v[90:92], v32, s[6:7] offset:192
	v_mov_b32_e32 v62, v48
	v_lshlrev_b32_e32 v13, 2, v13
	v_mov_b32_e32 v94, v52
	global_load_dword v81, v13, s[4:5]
	global_load_dword v85, v13, s[6:7]
	s_waitcnt vmcnt(28)
	v_pk_mul_f32 v[14:15], v[62:63], v[94:95]
	v_or_b32_e32 v13, v53, v38
	v_lshlrev_b32_e32 v13, 2, v13
	v_pk_mul_f32 v[14:15], v[14:15], s[0:1] op_sel_hi:[1,0]
	global_load_dwordx3 v[46:48], v32, s[4:5]
	global_load_dwordx3 v[50:52], v32, s[6:7]
	global_load_dword v49, v13, s[4:5]
	global_load_dword v53, v13, s[6:7]
	v_cvt_pk_f16_f32 v13, v14, v15
	v_or_b32_e32 v14, v89, v38
	global_load_dwordx3 v[94:96], v32, s[4:5] offset:64
	global_load_dwordx3 v[98:100], v32, s[6:7] offset:64
	v_lshlrev_b32_e32 v14, 2, v14
	global_load_dword v63, v14, s[4:5]
	global_load_dword v89, v14, s[6:7]
	global_load_dwordx3 v[102:104], v32, s[4:5] offset:128
	global_load_dwordx3 v[106:108], v32, s[6:7] offset:128
	v_lshlrev_b32_e32 v32, 4, v0
	v_and_or_b32 v32, v32, 48, v41
	v_lshlrev_b32_e32 v32, 2, v32
	global_load_dwordx4 v[34:37], v32, s[2:3]
	s_waitcnt vmcnt(37)
	v_pk_mul_f32 v[14:15], v[54:55], v[58:59]
	v_mov_b32_e32 v32, v56
	v_pk_mul_f32 v[14:15], v[14:15], s[0:1] op_sel_hi:[1,0]
	v_mov_b32_e32 v56, v60
	v_cvt_pk_f16_f32 v14, v14, v15
	v_or_b32_e32 v15, v93, v38
	v_lshlrev_b32_e32 v15, 2, v15
	s_mov_b32 s2, 0xc2ce8ed0
	s_mov_b32 s3, 0x42b17218
	v_and_b32_e32 v0, 48, v0
	s_waitcnt vmcnt(35)
	v_pk_mul_f32 v[32:33], v[32:33], v[56:57]
	global_load_dword v55, v15, s[4:5]
	global_load_dword v57, v15, s[6:7]
	v_pk_mul_f32 v[32:33], v[32:33], s[0:1] op_sel_hi:[1,0]
	s_waitcnt vmcnt(35)
	v_pk_mul_f32 v[16:17], v[16:17], v[20:21]
	s_waitcnt vmcnt(33)
	v_pk_mul_f32 v[18:19], v[18:19], v[22:23]
	v_pk_mul_f32 v[16:17], v[16:17], s[0:1] op_sel_hi:[1,0]
	v_pk_mul_f32 v[18:19], v[18:19], s[0:1] op_sel_hi:[1,0]
	v_cvt_pk_f16_f32 v16, v16, v17
	v_cvt_pk_f16_f32 v17, v18, v19
	v_cvt_pk_f16_f32 v15, v32, v33
	s_mov_b32 s4, 0x7f800000
	s_mov_b32 s6, 0x33800000
	s_waitcnt vmcnt(31)
	v_pk_mul_f32 v[18:19], v[24:25], v[28:29]
	s_waitcnt vmcnt(29)
	v_pk_mul_f32 v[20:21], v[26:27], v[30:31]
	v_pk_mul_f32 v[18:19], v[18:19], s[0:1] op_sel_hi:[1,0]
	v_pk_mul_f32 v[20:21], v[20:21], s[0:1] op_sel_hi:[1,0]
	v_cvt_pk_f16_f32 v18, v18, v19
	s_waitcnt vmcnt(28)
	v_mov_b32_e32 v38, v44
	s_waitcnt vmcnt(27)
	v_mov_b32_e32 v44, v68
	v_cvt_pk_f16_f32 v19, v20, v21
	v_pk_mul_f32 v[20:21], v[42:43], v[66:67]
	s_mov_b32 s7, 0x3c23d70a
	s_waitcnt vmcnt(25)
	v_pk_mul_f32 v[22:23], v[38:39], v[44:45]
	v_pk_mul_f32 v[20:21], v[20:21], s[0:1] op_sel_hi:[1,0]
	v_pk_mul_f32 v[22:23], v[22:23], s[0:1] op_sel_hi:[1,0]
	s_waitcnt vmcnt(24)
	v_mov_b32_e32 v60, v72
	s_waitcnt vmcnt(23)
	v_mov_b32_e32 v68, v76
	v_cvt_pk_f16_f32 v20, v20, v21
	v_cvt_pk_f16_f32 v21, v22, v23
	v_pk_mul_f32 v[22:23], v[70:71], v[74:75]
	s_waitcnt vmcnt(21)
	v_pk_mul_f32 v[24:25], v[60:61], v[68:69]
	v_pk_mul_f32 v[22:23], v[22:23], s[0:1] op_sel_hi:[1,0]
	v_pk_mul_f32 v[24:25], v[24:25], s[0:1] op_sel_hi:[1,0]
	s_waitcnt vmcnt(20)
	v_mov_b32_e32 v72, v80
	s_waitcnt vmcnt(19)
	v_mov_b32_e32 v76, v84
	v_cvt_pk_f16_f32 v22, v22, v23
	v_cvt_pk_f16_f32 v23, v24, v25
	v_pk_mul_f32 v[24:25], v[78:79], v[82:83]
	s_waitcnt vmcnt(17)
	v_pk_mul_f32 v[26:27], v[72:73], v[76:77]
	v_pk_mul_f32 v[24:25], v[24:25], s[0:1] op_sel_hi:[1,0]
	v_pk_mul_f32 v[26:27], v[26:27], s[0:1] op_sel_hi:[1,0]
	s_waitcnt vmcnt(16)
	v_mov_b32_e32 v80, v88
	s_waitcnt vmcnt(15)
	v_mov_b32_e32 v84, v92
	v_cvt_pk_f16_f32 v24, v24, v25
	v_cvt_pk_f16_f32 v25, v26, v27
	v_pk_mul_f32 v[26:27], v[86:87], v[90:91]
	s_waitcnt vmcnt(13)
	v_pk_mul_f32 v[28:29], v[80:81], v[84:85]
	v_pk_mul_f32 v[26:27], v[26:27], s[0:1] op_sel_hi:[1,0]
	v_pk_mul_f32 v[28:29], v[28:29], s[0:1] op_sel_hi:[1,0]
	v_cvt_pk_f16_f32 v26, v26, v27
	v_cvt_pk_f16_f32 v27, v28, v29
	s_waitcnt vmcnt(11)
	v_pk_mul_f32 v[28:29], v[46:47], v[50:51]
	s_waitcnt vmcnt(9)
	v_pk_mul_f32 v[30:31], v[48:49], v[52:53]
	v_pk_mul_f32 v[28:29], v[28:29], s[0:1] op_sel_hi:[1,0]
	v_pk_mul_f32 v[30:31], v[30:31], s[0:1] op_sel_hi:[1,0]
	s_waitcnt vmcnt(8)
	v_mov_b32_e32 v62, v96
	s_waitcnt vmcnt(7)
	v_mov_b32_e32 v88, v100
	v_cvt_pk_f16_f32 v28, v28, v29
	v_cvt_pk_f16_f32 v29, v30, v31
	v_pk_mul_f32 v[30:31], v[94:95], v[98:99]
	s_waitcnt vmcnt(5)
	v_pk_mul_f32 v[32:33], v[62:63], v[88:89]
	v_pk_mul_f32 v[30:31], v[30:31], s[0:1] op_sel_hi:[1,0]
	v_pk_mul_f32 v[32:33], v[32:33], s[0:1] op_sel_hi:[1,0]
	v_cvt_pk_f16_f32 v30, v30, v31
	v_cvt_pk_f16_f32 v31, v32, v33
	s_waitcnt vmcnt(3)
	v_pk_mul_f32 v[32:33], v[102:103], v[106:107]
	s_waitcnt vmcnt(2)
	v_cmp_ngt_f32_e32 vcc, s2, v34
	v_pk_mul_f32 v[32:33], v[32:33], s[0:1] op_sel_hi:[1,0]
	s_mov_b32 s1, 0x3fb8aa3b
	v_cvt_pk_f16_f32 v32, v32, v33
	v_mul_f32_e32 v33, 0x3fb8aa3b, v34
	v_fma_f32 v38, v34, s1, -v33
	v_rndne_f32_e32 v39, v33
	v_fmac_f32_e32 v38, 0x32a5705f, v34
	v_sub_f32_e32 v33, v33, v39
	v_add_f32_e32 v33, v33, v38
	v_exp_f32_e32 v33, v33
	v_cvt_i32_f32_e32 v38, v39
	v_mov_b32_e32 v107, 0x7f800000
	v_mov_b32_e32 v54, v104
	v_mov_b32_e32 v56, v108
	v_ldexp_f32 v33, v33, v38
	v_cndmask_b32_e32 v33, 0, v33, vcc
	v_cmp_nlt_f32_e32 vcc, s3, v34
	s_waitcnt vmcnt(0)
	v_pk_mul_f32 v[42:43], v[54:55], v[56:57]
	v_mov_b32_e32 v103, 0x41200000
	v_cndmask_b32_e32 v33, v107, v33, vcc
	v_add_f32_e32 v34, 1.0, v33
	v_add_f32_e32 v38, -1.0, v34
	v_sub_f32_e32 v39, v38, v34
	v_add_f32_e32 v39, 1.0, v39
	v_sub_f32_e32 v38, v33, v38
	v_add_f32_e32 v41, v38, v39
	v_frexp_mant_f32_e32 v44, v34
	v_cvt_f64_f32_e32 v[38:39], v34
	v_frexp_exp_i32_f64_e32 v38, v[38:39]
	v_cmp_gt_f32_e32 vcc, s10, v44
	s_mov_b32 s5, 0xbd23d70a
	v_pk_mul_f32 v[42:43], v[42:43], s[0:1] op_sel_hi:[1,0]
	v_subbrev_co_u32_e32 v50, vcc, 0, v38, vcc
	v_sub_u32_e32 v38, 0, v50
	v_ldexp_f32 v34, v34, v38
	v_ldexp_f32 v38, v41, v38
	v_add_f32_e32 v41, -1.0, v34
	v_add_f32_e32 v39, 1.0, v41
	v_sub_f32_e32 v39, v34, v39
	v_add_f32_e32 v44, v38, v39
	v_add_f32_e32 v39, 1.0, v34
	v_add_f32_e32 v45, -1.0, v39
	v_sub_f32_e32 v34, v34, v45
	v_add_f32_e32 v34, v38, v34
	v_add_f32_e32 v51, v39, v34
	v_rcp_f32_e32 v52, v51
	v_sub_f32_e32 v38, v39, v51
	v_add_f32_e32 v39, v41, v44
	v_add_f32_e32 v34, v34, v38
	v_sub_f32_e32 v38, v41, v39
	v_mul_f32_e32 v53, v39, v52
	v_add_f32_e32 v41, v44, v38
	v_mul_f32_e32 v44, v51, v53
	v_fma_f32 v46, v53, v51, -v44
	v_fmac_f32_e32 v46, v53, v34
	v_add_f32_e32 v38, v44, v46
	v_sub_f32_e32 v45, v39, v38
	v_pk_add_f32 v[48:49], v[38:39], v[44:45] neg_lo:[0,1] neg_hi:[0,1]
	v_mov_b32_e32 v47, v38
	v_pk_add_f32 v[38:39], v[48:49], v[46:47] neg_lo:[0,1] neg_hi:[0,1]
	v_cmp_neq_f32_e32 vcc, s4, v33
	v_add_f32_e32 v39, v41, v39
	v_add_f32_e32 v38, v38, v39
	v_add_f32_e32 v39, v45, v38
	v_mul_f32_e32 v41, v52, v39
	v_mul_f32_e32 v44, v51, v41
	v_fma_f32 v46, v41, v51, -v44
	v_fmac_f32_e32 v46, v41, v34
	v_sub_f32_e32 v34, v45, v39
	v_add_f32_e32 v34, v38, v34
	v_add_f32_e32 v38, v44, v46
	v_sub_f32_e32 v45, v39, v38
	v_pk_add_f32 v[48:49], v[38:39], v[44:45] neg_lo:[0,1] neg_hi:[0,1]
	v_mov_b32_e32 v47, v38
	v_pk_add_f32 v[38:39], v[48:49], v[46:47] neg_lo:[0,1] neg_hi:[0,1]
	v_cvt_f32_i32_e32 v44, v50
	v_add_f32_e32 v34, v34, v39
	v_add_f32_e32 v34, v38, v34
	v_add_f32_e32 v38, v53, v41
	v_add_f32_e32 v34, v45, v34
	v_sub_f32_e32 v39, v38, v53
	v_mul_f32_e32 v34, v52, v34
	v_sub_f32_e32 v39, v41, v39
	v_add_f32_e32 v41, v39, v34
	v_add_f32_e32 v45, v38, v41
	v_mul_f32_e32 v46, v45, v45
	v_mov_b32_e32 v34, 0x3ecc95a3
	v_sub_f32_e32 v38, v45, v38
	v_fmamk_f32 v39, v46, 0x3e9b6dac, v34
	v_sub_f32_e32 v38, v41, v38
	v_fmaak_f32 v39, v46, v39, 0x3f2aaada
	v_ldexp_f32 v47, v45, 1
	v_ldexp_f32 v41, v38, 1
	v_mul_f32_e32 v45, v45, v46
	v_mov_b32_e32 v38, 0x3f317218
	v_pk_mul_f32 v[48:49], v[44:45], v[38:39]
	s_mov_b32 s0, 0x42000
	v_fma_f32 v46, v44, s11, -v48
	v_fmac_f32_e32 v46, 0xb102e308, v44
	v_pk_add_f32 v[44:45], v[48:49], v[46:47]
	v_mov_b32_e32 v50, v48
	v_sub_f32_e32 v39, v45, v47
	v_sub_f32_e32 v39, v49, v39
	v_add_f32_e32 v51, v41, v39
	v_pk_add_f32 v[48:49], v[44:45], v[48:49] neg_lo:[0,1] neg_hi:[0,1]
	v_pk_add_f32 v[52:53], v[44:45], v[50:51]
	v_mov_b32_e32 v47, v44
	v_mov_b32_e32 v49, v53
	v_pk_add_f32 v[54:55], v[46:47], v[48:49] neg_lo:[0,1] neg_hi:[0,1]
	v_pk_add_f32 v[46:47], v[46:47], v[48:49]
	v_mov_b32_e32 v50, v51
	v_pk_add_f32 v[48:49], v[46:47], v[44:45] op_sel:[1,0] op_sel_hi:[0,1] neg_lo:[0,1] neg_hi:[0,1]
	v_pk_add_f32 v[56:57], v[52:53], v[48:49] op_sel_hi:[1,0] neg_lo:[0,1] neg_hi:[0,1]
	v_mov_b32_e32 v52, v53
	v_mov_b32_e32 v53, v47
	v_pk_mov_b32 v[48:49], v[44:45], v[48:49] op_sel:[1,0]
	v_mov_b32_e32 v51, v44
	v_pk_add_f32 v[48:49], v[52:53], v[48:49] neg_lo:[0,1] neg_hi:[0,1]
	v_mov_b32_e32 v56, v54
	v_pk_add_f32 v[44:45], v[50:51], v[48:49] neg_lo:[0,1] neg_hi:[0,1]
	v_mov_b32_e32 v55, v47
	v_pk_add_f32 v[48:49], v[56:57], v[44:45]
	v_mov_b32_e32 v56, 0x3f2aaada
	v_pk_add_f32 v[50:51], v[48:49], v[48:49] op_sel:[0,1] op_sel_hi:[1,0]
	v_mov_b32_e32 v63, 0
	v_pk_add_f32 v[46:47], v[46:47], v[50:51] op_sel:[1,0] op_sel_hi:[0,1]
	v_mov_b32_e32 v49, v46
	v_pk_add_f32 v[52:53], v[48:49], v[54:55] neg_lo:[0,1] neg_hi:[0,1]
	v_mov_b32_e32 v45, v50
	v_sub_f32_e32 v39, v48, v52
	v_pk_add_f32 v[44:45], v[44:45], v[52:53] neg_lo:[0,1] neg_hi:[0,1]
	v_sub_f32_e32 v39, v54, v39
	v_add_f32_e32 v39, v44, v39
	v_add_f32_e32 v39, v39, v45
	v_add_f32_e32 v39, v46, v39
	v_cndmask_b32_e32 v39, v107, v39, vcc
	v_cmp_lt_f32_e64 vcc, |v33|, s6
	v_mul_lo_u32 v62, v40, s0
	v_mov_b32_e32 v119, v63
	v_cndmask_b32_e32 v33, v39, v33, vcc
	v_add_f32_e32 v33, 0x358637bd, v33
	v_med3_f32 v39, v33, s7, v103
	v_div_scale_f32 v41, s[12:13], v39, v39, s5
	v_rcp_f32_e32 v44, v41
	v_cvt_pk_f16_f32 v33, v42, v43
	s_mov_b32 s12, 0
	v_fma_f32 v42, -v41, v44, 1.0
	v_fmac_f32_e32 v44, v42, v44
	v_div_scale_f32 v42, vcc, s5, v39, s5
	v_mul_f32_e32 v43, v42, v44
	v_fma_f32 v45, -v41, v43, v42
	v_fmac_f32_e32 v43, v45, v44
	v_fma_f32 v41, -v41, v43, v42
	v_div_fmas_f32 v41, v41, v44, v43
	v_div_fixup_f32 v41, v41, v39, s5
	v_mul_f32_e32 v39, 0x3fb8aa3b, v41
	v_fma_f32 v42, v41, s1, -v39
	v_rndne_f32_e32 v43, v39
	v_fmac_f32_e32 v42, 0x32a5705f, v41
	v_sub_f32_e32 v39, v39, v43
	v_add_f32_e32 v39, v39, v42
	v_cvt_i32_f32_e32 v42, v43
	v_mul_f32_e32 v43, 0x3fb8aa3b, v35
	v_fma_f32 v44, v35, s1, -v43
	v_rndne_f32_e32 v45, v43
	v_fmac_f32_e32 v44, 0x32a5705f, v35
	v_sub_f32_e32 v43, v43, v45
	v_add_f32_e32 v43, v43, v44
	v_exp_f32_e32 v39, v39
	v_exp_f32_e32 v43, v43
	v_cvt_i32_f32_e32 v44, v45
	v_cmp_ngt_f32_e32 vcc, s2, v35
	v_ldexp_f32 v57, v39, v42
	v_ldexp_f32 v39, v43, v44
	v_cndmask_b32_e32 v39, 0, v39, vcc
	v_cmp_nlt_f32_e32 vcc, s3, v35
	s_nop 1
	v_cndmask_b32_e32 v35, v107, v39, vcc
	v_add_f32_e32 v39, 1.0, v35
	v_add_f32_e32 v42, -1.0, v39
	v_sub_f32_e32 v43, v42, v39
	v_add_f32_e32 v43, 1.0, v43
	v_sub_f32_e32 v42, v35, v42
	v_add_f32_e32 v44, v42, v43
	v_frexp_mant_f32_e32 v45, v39
	v_cvt_f64_f32_e32 v[42:43], v39
	v_frexp_exp_i32_f64_e32 v42, v[42:43]
	v_cmp_gt_f32_e32 vcc, s10, v45
	s_nop 1
	v_subbrev_co_u32_e32 v50, vcc, 0, v42, vcc
	v_sub_u32_e32 v42, 0, v50
	v_ldexp_f32 v39, v39, v42
	v_ldexp_f32 v42, v44, v42
	v_add_f32_e32 v44, -1.0, v39
	v_add_f32_e32 v43, 1.0, v44
	v_sub_f32_e32 v43, v39, v43
	v_add_f32_e32 v45, v42, v43
	v_add_f32_e32 v43, 1.0, v39
	v_add_f32_e32 v46, -1.0, v43
	v_sub_f32_e32 v39, v39, v46
	v_add_f32_e32 v39, v42, v39
	v_add_f32_e32 v51, v43, v39
	v_rcp_f32_e32 v52, v51
	v_sub_f32_e32 v42, v43, v51
	v_add_f32_e32 v43, v44, v45
	v_add_f32_e32 v39, v39, v42
	v_mul_f32_e32 v54, v43, v52
	v_sub_f32_e32 v42, v44, v43
	v_mul_f32_e32 v44, v51, v54
	v_fma_f32 v46, v54, v51, -v44
	v_fmac_f32_e32 v46, v54, v39
	v_add_f32_e32 v53, v45, v42
	v_add_f32_e32 v42, v44, v46
	v_sub_f32_e32 v45, v43, v42
	v_pk_add_f32 v[48:49], v[42:43], v[44:45] neg_lo:[0,1] neg_hi:[0,1]
	v_mov_b32_e32 v47, v42
	v_pk_add_f32 v[42:43], v[48:49], v[46:47] neg_lo:[0,1] neg_hi:[0,1]
	v_cmp_neq_f32_e32 vcc, s4, v35
	v_add_f32_e32 v43, v53, v43
	v_add_f32_e32 v42, v42, v43
	v_add_f32_e32 v43, v45, v42
	v_mul_f32_e32 v53, v52, v43
	v_mul_f32_e32 v44, v51, v53
	v_fma_f32 v46, v53, v51, -v44
	v_fmac_f32_e32 v46, v53, v39
	v_sub_f32_e32 v39, v45, v43
	v_add_f32_e32 v39, v42, v39
	v_add_f32_e32 v42, v44, v46
	v_sub_f32_e32 v45, v43, v42
	v_pk_add_f32 v[48:49], v[42:43], v[44:45] neg_lo:[0,1] neg_hi:[0,1]
	v_mov_b32_e32 v47, v42
	v_pk_add_f32 v[42:43], v[48:49], v[46:47] neg_lo:[0,1] neg_hi:[0,1]
	s_nop 0
	v_add_f32_e32 v39, v39, v43
	v_add_f32_e32 v39, v42, v39
	v_add_f32_e32 v43, v54, v53
	v_add_f32_e32 v39, v45, v39
	v_sub_f32_e32 v42, v43, v54
	v_mul_f32_e32 v39, v52, v39
	v_sub_f32_e32 v42, v53, v42
	v_add_f32_e32 v44, v42, v39
	v_add_f32_e32 v46, v43, v44
	v_cvt_f32_i32_e32 v42, v50
	v_mul_f32_e32 v47, v46, v46
	v_sub_f32_e32 v43, v46, v43
	v_fmamk_f32 v39, v47, 0x3e9b6dac, v34
	v_sub_f32_e32 v43, v44, v43
	v_fmaak_f32 v39, v47, v39, 0x3f2aaada
	v_ldexp_f32 v48, v43, 1
	v_mul_f32_e32 v43, v46, v47
	v_ldexp_f32 v45, v46, 1
	v_pk_mul_f32 v[46:47], v[42:43], v[38:39]
	s_nop 0
	v_fma_f32 v44, v42, s11, -v46
	v_fmac_f32_e32 v44, 0xb102e308, v42
	v_pk_add_f32 v[42:43], v[46:47], v[44:45]
	s_nop 0
	v_sub_f32_e32 v39, v43, v45
	v_sub_f32_e32 v39, v47, v39
	v_add_f32_e32 v49, v48, v39
	v_mov_b32_e32 v48, v46
	v_pk_add_f32 v[46:47], v[42:43], v[46:47] neg_lo:[0,1] neg_hi:[0,1]
	v_pk_add_f32 v[50:51], v[42:43], v[48:49]
	v_mov_b32_e32 v45, v42
	v_mov_b32_e32 v47, v51
	v_pk_add_f32 v[52:53], v[44:45], v[46:47] neg_lo:[0,1] neg_hi:[0,1]
	v_pk_add_f32 v[44:45], v[44:45], v[46:47]
	v_mov_b32_e32 v48, v49
	v_pk_add_f32 v[46:47], v[44:45], v[42:43] op_sel:[1,0] op_sel_hi:[0,1] neg_lo:[0,1] neg_hi:[0,1]
	v_pk_add_f32 v[54:55], v[50:51], v[46:47] op_sel_hi:[1,0] neg_lo:[0,1] neg_hi:[0,1]
	v_mov_b32_e32 v50, v51
	v_mov_b32_e32 v51, v45
	v_pk_mov_b32 v[46:47], v[42:43], v[46:47] op_sel:[1,0]
	v_mov_b32_e32 v49, v42
	v_pk_add_f32 v[46:47], v[50:51], v[46:47] neg_lo:[0,1] neg_hi:[0,1]
	v_mov_b32_e32 v54, v52
	v_pk_add_f32 v[42:43], v[48:49], v[46:47] neg_lo:[0,1] neg_hi:[0,1]
	v_mov_b32_e32 v53, v45
	v_pk_add_f32 v[46:47], v[54:55], v[42:43]
	s_nop 0
	v_pk_add_f32 v[48:49], v[46:47], v[46:47] op_sel:[0,1] op_sel_hi:[1,0]
	s_nop 0
	v_pk_add_f32 v[44:45], v[44:45], v[48:49] op_sel:[1,0] op_sel_hi:[0,1]
	v_mov_b32_e32 v47, v44
	v_pk_add_f32 v[50:51], v[46:47], v[52:53] neg_lo:[0,1] neg_hi:[0,1]
	v_mov_b32_e32 v43, v48
	v_sub_f32_e32 v39, v46, v50
	v_pk_add_f32 v[42:43], v[42:43], v[50:51] neg_lo:[0,1] neg_hi:[0,1]
	v_sub_f32_e32 v39, v52, v39
	v_add_f32_e32 v39, v42, v39
	v_add_f32_e32 v39, v39, v43
	v_add_f32_e32 v39, v44, v39
	v_cndmask_b32_e32 v39, v107, v39, vcc
	v_cmp_lt_f32_e64 vcc, |v35|, s6
	s_nop 1
	v_cndmask_b32_e32 v35, v39, v35, vcc
	v_add_f32_e32 v35, 0x358637bd, v35
	v_med3_f32 v35, v35, s7, v103
	v_div_scale_f32 v39, s[14:15], v35, v35, s5
	v_rcp_f32_e32 v42, v39
	v_cmp_ngt_f32_e32 vcc, s2, v41
	s_nop 1
	v_cndmask_b32_e32 v43, 0, v57, vcc
	v_cmp_nlt_f32_e32 vcc, s3, v41
	v_fma_f32 v41, -v39, v42, 1.0
	v_fmac_f32_e32 v42, v41, v42
	v_cndmask_b32_e32 v102, v107, v43, vcc
	v_div_scale_f32 v41, vcc, s5, v35, s5
	v_mul_f32_e32 v43, v41, v42
	v_fma_f32 v44, -v39, v43, v41
	v_fmac_f32_e32 v43, v44, v42
	v_fma_f32 v39, -v39, v43, v41
	v_div_fmas_f32 v39, v39, v42, v43
	v_mul_f32_e32 v42, 0x3fb8aa3b, v36
	v_fma_f32 v43, v36, s1, -v42
	v_rndne_f32_e32 v44, v42
	v_fmac_f32_e32 v43, 0x32a5705f, v36
	v_sub_f32_e32 v42, v42, v44
	v_add_f32_e32 v42, v42, v43
	v_div_fixup_f32 v106, v39, v35, s5
	v_exp_f32_e32 v42, v42
	v_cvt_i32_f32_e32 v43, v44
	v_mul_f32_e32 v35, 0x3fb8aa3b, v106
	v_fma_f32 v39, v106, s1, -v35
	v_rndne_f32_e32 v41, v35
	v_fmac_f32_e32 v39, 0x32a5705f, v106
	v_sub_f32_e32 v35, v35, v41
	v_add_f32_e32 v35, v35, v39
	v_ldexp_f32 v39, v42, v43
	v_cmp_ngt_f32_e32 vcc, s2, v36
	v_exp_f32_e32 v35, v35
	v_cvt_i32_f32_e32 v41, v41
	v_cndmask_b32_e32 v39, 0, v39, vcc
	v_cmp_nlt_f32_e32 vcc, s3, v36
	v_ldexp_f32 v35, v35, v41
	s_nop 0
	v_cndmask_b32_e32 v36, v107, v39, vcc
	v_add_f32_e32 v39, 1.0, v36
	v_add_f32_e32 v42, -1.0, v39
	v_sub_f32_e32 v43, v42, v39
	v_add_f32_e32 v43, 1.0, v43
	v_sub_f32_e32 v42, v36, v42
	v_add_f32_e32 v44, v42, v43
	v_frexp_mant_f32_e32 v45, v39
	v_cvt_f64_f32_e32 v[42:43], v39
	v_frexp_exp_i32_f64_e32 v42, v[42:43]
	v_cmp_gt_f32_e32 vcc, s10, v45
	s_nop 1
	v_subbrev_co_u32_e32 v50, vcc, 0, v42, vcc
	v_sub_u32_e32 v42, 0, v50
	v_ldexp_f32 v39, v39, v42
	v_ldexp_f32 v42, v44, v42
	v_add_f32_e32 v44, -1.0, v39
	v_add_f32_e32 v43, 1.0, v44
	v_sub_f32_e32 v43, v39, v43
	v_add_f32_e32 v45, v42, v43
	v_add_f32_e32 v43, 1.0, v39
	v_add_f32_e32 v46, -1.0, v43
	v_sub_f32_e32 v39, v39, v46
	v_add_f32_e32 v39, v42, v39
	v_add_f32_e32 v51, v43, v39
	v_rcp_f32_e32 v52, v51
	v_sub_f32_e32 v42, v43, v51
	v_add_f32_e32 v43, v44, v45
	v_add_f32_e32 v39, v39, v42
	v_mul_f32_e32 v54, v43, v52
	v_sub_f32_e32 v42, v44, v43
	v_mul_f32_e32 v44, v51, v54
	v_fma_f32 v46, v54, v51, -v44
	v_fmac_f32_e32 v46, v54, v39
	v_add_f32_e32 v53, v45, v42
	v_add_f32_e32 v42, v44, v46
	v_sub_f32_e32 v45, v43, v42
	v_pk_add_f32 v[48:49], v[42:43], v[44:45] neg_lo:[0,1] neg_hi:[0,1]
	v_mov_b32_e32 v47, v42
	v_pk_add_f32 v[42:43], v[48:49], v[46:47] neg_lo:[0,1] neg_hi:[0,1]
	v_cmp_neq_f32_e32 vcc, s4, v36
	v_add_f32_e32 v43, v53, v43
	v_add_f32_e32 v42, v42, v43
	v_add_f32_e32 v43, v45, v42
	v_mul_f32_e32 v53, v52, v43
	v_mul_f32_e32 v44, v51, v53
	v_fma_f32 v46, v53, v51, -v44
	v_fmac_f32_e32 v46, v53, v39
	v_sub_f32_e32 v39, v45, v43
	v_add_f32_e32 v39, v42, v39
	v_add_f32_e32 v42, v44, v46
	v_sub_f32_e32 v45, v43, v42
	v_pk_add_f32 v[48:49], v[42:43], v[44:45] neg_lo:[0,1] neg_hi:[0,1]
	v_mov_b32_e32 v47, v42
	v_pk_add_f32 v[42:43], v[48:49], v[46:47] neg_lo:[0,1] neg_hi:[0,1]
	s_nop 0
	v_add_f32_e32 v39, v39, v43
	v_add_f32_e32 v39, v42, v39
	v_add_f32_e32 v43, v54, v53
	v_add_f32_e32 v39, v45, v39
	v_sub_f32_e32 v42, v43, v54
	v_mul_f32_e32 v39, v52, v39
	v_sub_f32_e32 v42, v53, v42
	v_add_f32_e32 v44, v42, v39
	v_add_f32_e32 v46, v43, v44
	v_cvt_f32_i32_e32 v42, v50
	v_mul_f32_e32 v47, v46, v46
	v_sub_f32_e32 v43, v46, v43
	v_fmamk_f32 v39, v47, 0x3e9b6dac, v34
	v_sub_f32_e32 v43, v44, v43
	v_fmaak_f32 v39, v47, v39, 0x3f2aaada
	v_ldexp_f32 v48, v43, 1
	v_mul_f32_e32 v43, v46, v47
	v_ldexp_f32 v45, v46, 1
	v_pk_mul_f32 v[46:47], v[42:43], v[38:39]
	s_nop 0
	v_fma_f32 v44, v42, s11, -v46
	v_fmac_f32_e32 v44, 0xb102e308, v42
	v_pk_add_f32 v[42:43], v[46:47], v[44:45]
	s_nop 0
	v_sub_f32_e32 v39, v43, v45
	v_sub_f32_e32 v39, v47, v39
	v_add_f32_e32 v49, v48, v39
	v_mov_b32_e32 v48, v46
	v_pk_add_f32 v[46:47], v[42:43], v[46:47] neg_lo:[0,1] neg_hi:[0,1]
	v_pk_add_f32 v[50:51], v[42:43], v[48:49]
	v_mov_b32_e32 v45, v42
	v_mov_b32_e32 v47, v51
	v_pk_add_f32 v[52:53], v[44:45], v[46:47] neg_lo:[0,1] neg_hi:[0,1]
	v_pk_add_f32 v[44:45], v[44:45], v[46:47]
	v_mov_b32_e32 v48, v49
	v_pk_add_f32 v[46:47], v[44:45], v[42:43] op_sel:[1,0] op_sel_hi:[0,1] neg_lo:[0,1] neg_hi:[0,1]
	v_pk_add_f32 v[54:55], v[50:51], v[46:47] op_sel_hi:[1,0] neg_lo:[0,1] neg_hi:[0,1]
	v_mov_b32_e32 v50, v51
	v_mov_b32_e32 v51, v45
	v_pk_mov_b32 v[46:47], v[42:43], v[46:47] op_sel:[1,0]
	v_mov_b32_e32 v49, v42
	v_pk_add_f32 v[46:47], v[50:51], v[46:47] neg_lo:[0,1] neg_hi:[0,1]
	v_mov_b32_e32 v54, v52
	v_pk_add_f32 v[42:43], v[48:49], v[46:47] neg_lo:[0,1] neg_hi:[0,1]
	v_mov_b32_e32 v53, v45
	v_pk_add_f32 v[46:47], v[54:55], v[42:43]
	s_nop 0
	v_pk_add_f32 v[48:49], v[46:47], v[46:47] op_sel:[0,1] op_sel_hi:[1,0]
	s_nop 0
	v_pk_add_f32 v[44:45], v[44:45], v[48:49] op_sel:[1,0] op_sel_hi:[0,1]
	v_mov_b32_e32 v47, v44
	v_pk_add_f32 v[50:51], v[46:47], v[52:53] neg_lo:[0,1] neg_hi:[0,1]
	v_mov_b32_e32 v43, v48
	v_sub_f32_e32 v39, v46, v50
	v_pk_add_f32 v[42:43], v[42:43], v[50:51] neg_lo:[0,1] neg_hi:[0,1]
	v_sub_f32_e32 v39, v52, v39
	v_add_f32_e32 v39, v42, v39
	v_add_f32_e32 v39, v39, v43
	v_add_f32_e32 v39, v44, v39
	v_cndmask_b32_e32 v39, v107, v39, vcc
	v_cmp_lt_f32_e64 vcc, |v36|, s6
	s_nop 1
	v_cndmask_b32_e32 v36, v39, v36, vcc
	v_add_f32_e32 v36, 0x358637bd, v36
	v_med3_f32 v36, v36, s7, v103
	v_div_scale_f32 v39, s[14:15], v36, v36, s5
	v_rcp_f32_e32 v42, v39
	v_cmp_ngt_f32_e32 vcc, s2, v106
	s_nop 1
	v_cndmask_b32_e32 v120, 0, v35, vcc
	v_fma_f32 v35, -v39, v42, 1.0
	v_fmac_f32_e32 v42, v35, v42
	v_div_scale_f32 v35, vcc, s5, v36, s5
	v_mul_f32_e32 v41, v35, v42
	v_fma_f32 v43, -v39, v41, v35
	v_fmac_f32_e32 v41, v43, v42
	v_fma_f32 v35, -v39, v41, v35
	v_div_fmas_f32 v35, v35, v42, v41
	v_mul_f32_e32 v41, 0x3fb8aa3b, v37
	v_fma_f32 v42, v37, s1, -v41
	v_rndne_f32_e32 v43, v41
	v_fmac_f32_e32 v42, 0x32a5705f, v37
	v_sub_f32_e32 v41, v41, v43
	v_div_fixup_f32 v121, v35, v36, s5
	v_add_f32_e32 v41, v41, v42
	v_mul_f32_e32 v35, 0x3fb8aa3b, v121
	v_exp_f32_e32 v41, v41
	v_cvt_i32_f32_e32 v42, v43
	v_fma_f32 v36, v121, s1, -v35
	v_rndne_f32_e32 v39, v35
	v_fmac_f32_e32 v36, 0x32a5705f, v121
	v_sub_f32_e32 v35, v35, v39
	v_add_f32_e32 v35, v35, v36
	v_exp_f32_e32 v122, v35
	v_ldexp_f32 v35, v41, v42
	v_cmp_ngt_f32_e32 vcc, s2, v37
	v_cvt_i32_f32_e32 v123, v39
	s_nop 0
	v_cndmask_b32_e32 v35, 0, v35, vcc
	v_cmp_nlt_f32_e32 vcc, s3, v37
	s_nop 1
	v_cndmask_b32_e32 v124, v107, v35, vcc
	v_add_f32_e32 v35, 1.0, v124
	v_add_f32_e32 v36, -1.0, v35
	v_sub_f32_e32 v37, v36, v35
	v_add_f32_e32 v37, 1.0, v37
	v_sub_f32_e32 v36, v124, v36
	v_add_f32_e32 v39, v36, v37
	v_frexp_mant_f32_e32 v41, v35
	v_cvt_f64_f32_e32 v[36:37], v35
	v_frexp_exp_i32_f64_e32 v36, v[36:37]
	v_cmp_gt_f32_e32 vcc, s10, v41
	s_nop 1
	v_subbrev_co_u32_e32 v41, vcc, 0, v36, vcc
	v_sub_u32_e32 v36, 0, v41
	v_ldexp_f32 v35, v35, v36
	v_ldexp_f32 v36, v39, v36
	v_add_f32_e32 v39, -1.0, v35
	v_add_f32_e32 v37, 1.0, v39
	v_sub_f32_e32 v37, v35, v37
	v_add_f32_e32 v42, v36, v37
	v_add_f32_e32 v37, 1.0, v35
	v_add_f32_e32 v43, -1.0, v37
	v_sub_f32_e32 v35, v35, v43
	v_add_f32_e32 v35, v36, v35
	v_add_f32_e32 v48, v37, v35
	v_rcp_f32_e32 v49, v48
	v_sub_f32_e32 v36, v37, v48
	v_add_f32_e32 v37, v39, v42
	v_add_f32_e32 v35, v35, v36
	v_sub_f32_e32 v36, v39, v37
	v_mul_f32_e32 v50, v37, v49
	v_add_f32_e32 v39, v42, v36
	v_mul_f32_e32 v42, v48, v50
	v_fma_f32 v44, v50, v48, -v42
	v_fmac_f32_e32 v44, v50, v35
	v_add_f32_e32 v36, v42, v44
	v_sub_f32_e32 v43, v37, v36
	v_pk_add_f32 v[46:47], v[36:37], v[42:43] neg_lo:[0,1] neg_hi:[0,1]
	v_mov_b32_e32 v45, v36
	v_pk_add_f32 v[36:37], v[46:47], v[44:45] neg_lo:[0,1] neg_hi:[0,1]
	v_cmp_neq_f32_e32 vcc, s4, v124
	v_add_f32_e32 v37, v39, v37
	v_add_f32_e32 v36, v36, v37
	v_add_f32_e32 v37, v43, v36
	v_mul_f32_e32 v39, v49, v37
	v_mul_f32_e32 v42, v48, v39
	v_fma_f32 v44, v39, v48, -v42
	v_fmac_f32_e32 v44, v39, v35
	v_sub_f32_e32 v35, v43, v37
	v_add_f32_e32 v35, v36, v35
	v_add_f32_e32 v36, v42, v44
	v_sub_f32_e32 v43, v37, v36
	v_pk_add_f32 v[46:47], v[36:37], v[42:43] neg_lo:[0,1] neg_hi:[0,1]
	v_mov_b32_e32 v45, v36
	v_pk_add_f32 v[36:37], v[46:47], v[44:45] neg_lo:[0,1] neg_hi:[0,1]
	s_nop 0
	v_add_f32_e32 v35, v35, v37
	v_add_f32_e32 v35, v36, v35
	v_add_f32_e32 v36, v50, v39
	v_add_f32_e32 v35, v43, v35
	v_sub_f32_e32 v37, v36, v50
	v_mul_f32_e32 v35, v49, v35
	v_sub_f32_e32 v37, v39, v37
	v_add_f32_e32 v35, v37, v35
	v_add_f32_e32 v39, v36, v35
	v_mul_f32_e32 v42, v39, v39
	v_fmac_f32_e32 v34, 0x3e9b6dac, v42
	v_fmac_f32_e32 v56, v42, v34
	v_cvt_f32_i32_e32 v34, v41
	v_sub_f32_e32 v36, v39, v36
	v_sub_f32_e32 v35, v35, v36
	v_ldexp_f32 v37, v39, 1
	v_ldexp_f32 v41, v35, 1
	v_mul_f32_e32 v35, v39, v42
	v_mov_b32_e32 v39, v56
	v_pk_mul_f32 v[38:39], v[34:35], v[38:39]
	s_nop 0
	v_fma_f32 v36, v34, s11, -v38
	v_fmac_f32_e32 v36, 0xb102e308, v34
	v_pk_add_f32 v[104:105], v[38:39], v[36:37]
	s_nop 0
	v_sub_f32_e32 v34, v105, v37
	v_sub_f32_e32 v34, v39, v34
	v_add_f32_e32 v35, v41, v34
	v_mov_b32_e32 v34, v38
	v_pk_add_f32 v[38:39], v[104:105], v[38:39] neg_lo:[0,1] neg_hi:[0,1]
	v_pk_add_f32 v[42:43], v[104:105], v[34:35]
	v_mov_b32_e32 v37, v104
	v_mov_b32_e32 v39, v43
	v_pk_add_f32 v[110:111], v[36:37], v[38:39]
	v_pk_add_f32 v[108:109], v[36:37], v[38:39] neg_lo:[0,1] neg_hi:[0,1]
	v_pk_add_f32 v[36:37], v[110:111], v[104:105] op_sel:[1,0] op_sel_hi:[0,1] neg_lo:[0,1] neg_hi:[0,1]
	v_pk_add_f32 v[112:113], v[42:43], v[36:37] op_sel_hi:[1,0] neg_lo:[0,1] neg_hi:[0,1]
	v_mov_b32_e32 v38, v43
	v_mov_b32_e32 v39, v111
	v_pk_mov_b32 v[36:37], v[104:105], v[36:37] op_sel:[1,0]
	v_mov_b32_e32 v116, v35
	v_lshl_add_u64 v[34:35], s[52:53], 0, v[62:63]
	v_pk_add_f32 v[114:115], v[38:39], v[36:37] neg_lo:[0,1] neg_hi:[0,1]
	v_lshl_add_u64 v[34:35], v[34:35], 0, v[118:119]
	v_lshlrev_b32_e32 v36, 4, v1
	v_mov_b32_e32 v37, v63
	v_lshl_add_u64 v[34:35], v[34:35], 0, v[36:37]
	global_load_dwordx4 v[98:101], v[34:35], off
	global_load_dwordx4 v[70:73], v[34:35], off offset:256
	global_load_dwordx4 v[78:81], v[34:35], off offset:512
	global_load_dwordx4 v[86:89], v[34:35], off offset:768
	global_load_dwordx4 v[94:97], v[34:35], off offset:1024
	global_load_dwordx4 v[90:93], v[34:35], off offset:1280
	global_load_dwordx4 v[82:85], v[34:35], off offset:1536
	global_load_dwordx4 v[74:77], v[34:35], off offset:1792
	global_load_dwordx4 v[66:69], v[34:35], off offset:2048
	global_load_dwordx4 v[58:61], v[34:35], off offset:2304
	global_load_dwordx4 v[54:57], v[34:35], off offset:2560
	global_load_dwordx4 v[50:53], v[34:35], off offset:2816
	global_load_dwordx4 v[46:49], v[34:35], off offset:3072
	global_load_dwordx4 v[42:45], v[34:35], off offset:3328
	global_load_dwordx4 v[38:41], v[34:35], off offset:3584
	s_nop 0
	global_load_dwordx4 v[34:37], v[34:35], off offset:3840
	v_mov_b32_e32 v117, v104
	v_pk_add_f32 v[104:105], v[116:117], v[114:115] neg_lo:[0,1] neg_hi:[0,1]
	v_mov_b32_e32 v112, v108
	v_pk_add_f32 v[112:113], v[112:113], v[104:105]
	v_mov_b32_e32 v109, v111
	v_pk_add_f32 v[114:115], v[112:113], v[112:113] op_sel:[0,1] op_sel_hi:[1,0]
	v_lshlrev_b32_e32 v1, 5, v1
	v_pk_add_f32 v[110:111], v[110:111], v[114:115] op_sel:[1,0] op_sel_hi:[0,1]
	v_mov_b32_e32 v113, v110
	v_pk_add_f32 v[116:117], v[112:113], v[108:109] neg_lo:[0,1] neg_hi:[0,1]
	v_mov_b32_e32 v105, v114
	v_sub_f32_e32 v109, v112, v116
	v_pk_add_f32 v[104:105], v[104:105], v[116:117] neg_lo:[0,1] neg_hi:[0,1]
	v_sub_f32_e32 v108, v108, v109
	v_add_f32_e32 v104, v104, v108
	v_add_f32_e32 v104, v104, v105
	v_add_f32_e32 v104, v110, v104
	v_cndmask_b32_e32 v104, v107, v104, vcc
	v_cmp_lt_f32_e64 vcc, |v124|, s6
	v_lshlrev_b32_e32 v114, 3, v64
	v_or3_b32 v62, v118, v0, v62
	v_cndmask_b32_e32 v104, v104, v124, vcc
	v_add_f32_e32 v104, 0x358637bd, v104
	v_med3_f32 v108, v104, s7, v103
	v_div_scale_f32 v109, s[6:7], v108, v108, s5
	v_rcp_f32_e32 v110, v109
	v_cmp_nlt_f32_e32 vcc, s3, v106
	v_ldexp_f32 v106, v122, v123
	v_or3_b32 v122, v65, v1, v114
	v_fma_f32 v111, -v109, v110, 1.0
	v_cndmask_b32_e32 v103, v107, v120, vcc
	v_fmac_f32_e32 v110, v111, v110
	v_div_scale_f32 v111, vcc, s5, v108, s5
	v_mul_f32_e32 v112, v111, v110
	v_fma_f32 v113, -v109, v112, v111
	v_fmac_f32_e32 v112, v113, v110
	v_fma_f32 v109, -v109, v112, v111
	v_div_fmas_f32 v109, v109, v110, v112
	v_div_fixup_f32 v108, v109, v108, s5
	v_mul_f32_e32 v109, 0x3fb8aa3b, v108
	v_fma_f32 v110, v108, s1, -v109
	v_rndne_f32_e32 v111, v109
	v_fmac_f32_e32 v110, 0x32a5705f, v108
	v_sub_f32_e32 v109, v109, v111
	v_add_f32_e32 v109, v109, v110
	v_exp_f32_e32 v109, v109
	v_cvt_i32_f32_e32 v110, v111
	v_cmp_ngt_f32_e32 vcc, s2, v121
	v_pk_add_f32 v[104:105], v[102:103], 1.0 op_sel_hi:[1,0] neg_lo:[1,0] neg_hi:[1,0]
	v_lshl_add_u64 v[0:1], s[52:53], 0, v[62:63]
	v_cndmask_b32_e32 v106, 0, v106, vcc
	v_cmp_nlt_f32_e32 vcc, s3, v121
	v_ldexp_f32 v109, v109, v110
	s_mov_b64 s[6:7], 0x1800
	v_cndmask_b32_e32 v106, v107, v106, vcc
	v_cmp_ngt_f32_e32 vcc, s2, v108
	v_pk_mul_f32 v[110:111], v[104:105], -2.0 op_sel_hi:[1,0]
	v_cmp_eq_u32_e64 s[0:1], 0, v64
	v_cndmask_b32_e32 v109, 0, v109, vcc
	v_cmp_nlt_f32_e32 vcc, s3, v108
	v_cmp_gt_u32_e64 s[2:3], 2, v64
	v_cmp_eq_u32_e64 s[4:5], 3, v64
	v_cndmask_b32_e32 v107, v107, v109, vcc
	v_pk_add_f32 v[108:109], v[106:107], 1.0 op_sel_hi:[1,0] neg_lo:[1,0] neg_hi:[1,0]
	v_lshl_add_u64 v[0:1], v[0:1], 0, s[6:7]
	v_pk_mul_f32 v[112:113], v[108:109], -2.0 op_sel_hi:[1,0]
	s_mov_b64 s[6:7], 0x1000
	v_mov_b32_e32 v165, v3
	v_mov_b32_e32 v166, v4
	v_mov_b32_e32 v167, v5
	v_mov_b32_e32 v168, v6
	v_mov_b32_e32 v169, v7
	v_mov_b32_e32 v170, v8
	v_mov_b32_e32 v3, v166
	v_mov_b32_e32 v4, v168
	v_mov_b32_e32 v5, v170
	v_mov_b32_e32 v6, v165
	v_mov_b32_e32 v7, v167
	v_mov_b32_e32 v8, v169
	v_mov_b32_e32 v165, v11
	v_mov_b32_e32 v166, v12
	v_mov_b32_e32 v167, v13
	v_mov_b32_e32 v168, v14
	v_mov_b32_e32 v169, v15
	v_mov_b32_e32 v170, v16
	v_mov_b32_e32 v11, v166
	v_mov_b32_e32 v12, v168
	v_mov_b32_e32 v13, v170
	v_mov_b32_e32 v14, v165
	v_mov_b32_e32 v15, v167
	v_mov_b32_e32 v16, v169
	v_mov_b32_e32 v165, v19
	v_mov_b32_e32 v166, v20
	v_mov_b32_e32 v167, v21
	v_mov_b32_e32 v168, v22
	v_mov_b32_e32 v169, v23
	v_mov_b32_e32 v170, v24
	v_mov_b32_e32 v19, v166
	v_mov_b32_e32 v20, v168
	v_mov_b32_e32 v21, v170
	v_mov_b32_e32 v22, v165
	v_mov_b32_e32 v23, v167
	v_mov_b32_e32 v24, v169
	v_mov_b32_e32 v165, v27
	v_mov_b32_e32 v166, v28
	v_mov_b32_e32 v167, v29
	v_mov_b32_e32 v168, v30
	v_mov_b32_e32 v169, v31
	v_mov_b32_e32 v170, v32
	v_mov_b32_e32 v27, v166
	v_mov_b32_e32 v28, v168
	v_mov_b32_e32 v29, v170
	v_mov_b32_e32 v30, v165
	v_mov_b32_e32 v31, v167
	v_mov_b32_e32 v32, v169
	v_mov_b32_e32 v124, 0
	v_mov_b32_e32 v125, 0
	v_mov_b32_e32 v126, 0
	v_mov_b32_e32 v127, 0
	v_mov_b32_e32 v128, 0
	v_mov_b32_e32 v129, 0
	v_mov_b32_e32 v130, 0
	v_mov_b32_e32 v131, 0
	v_mov_b32_e32 v148, 0
	v_mov_b32_e32 v149, 0
	v_mov_b32_e32 v150, 0
	v_mov_b32_e32 v151, 0
	s_nop 1
	s_waitcnt vmcnt(15)
	v_mfma_f32_16x16x32_f16 v[132:135], v[2:5], v[124:127], v[98:101]
	v_mfma_f32_16x16x32_f16 v[136:139], v[10:13], v[124:127], v[98:101]
	v_mfma_f32_16x16x32_f16 v[140:143], v[18:21], v[124:127], v[98:101]
	v_mfma_f32_16x16x32_f16 v[144:147], v[26:29], v[124:127], v[98:101]
	global_load_dwordx4 v[98:101], v[0:1], off offset:-2048
	v_mfma_f32_16x16x32_f16 v[132:135], v[6:9], v[128:131], v[132:135]
	s_nop 1
	v_mfma_f32_16x16x32_f16 v[136:139], v[14:17], v[128:131], v[136:139]
	s_nop 1
	v_mfma_f32_16x16x32_f16 v[140:143], v[22:25], v[128:131], v[140:143]
	s_nop 1
	v_mfma_f32_16x16x32_f16 v[144:147], v[30:33], v[128:131], v[144:147]
	s_branch .LBB3_169
.LBB3_168:
	v_mov_b32_e32 v164, v122
	v_pk_fma_f32 v[154:155], v[106:107], v[150:151], v[108:109]
	v_pk_fma_f32 v[152:153], v[102:103], v[148:149], v[104:105]
	v_cndmask_b32_e64 v160, v136, v132, s[0:1]
	v_cndmask_b32_e64 v161, v137, v133, s[0:1]
	v_cndmask_b32_e64 v162, v138, v134, s[0:1]
	v_cndmask_b32_e64 v160, v140, v160, s[2:3]
	v_cndmask_b32_e64 v161, v141, v161, s[2:3]
	v_cndmask_b32_e64 v163, v139, v135, s[0:1]
	v_cndmask_b32_e64 v156, v160, v144, s[4:5]
	v_cndmask_b32_e64 v157, v161, v145, s[4:5]
	v_exp_f32_e32 v156, v156
	v_exp_f32_e32 v157, v157
	v_cndmask_b32_e64 v162, v142, v162, s[2:3]
	v_cndmask_b32_e64 v163, v143, v163, s[2:3]
	v_cndmask_b32_e64 v158, v162, v146, s[4:5]
	v_cndmask_b32_e64 v159, v163, v147, s[4:5]
	v_pk_add_f32 v[156:157], v[156:157], 1.0 op_sel_hi:[1,0]
	v_exp_f32_e32 v158, v158
	v_rcp_f32_e32 v156, v156
	v_rcp_f32_e32 v157, v157
	v_exp_f32_e32 v159, v159
	v_pk_fma_f32 v[148:149], v[110:111], v[156:157], v[152:153]
	v_pk_add_f32 v[158:159], v[158:159], 1.0 op_sel_hi:[1,0]
	v_cvt_pk_f16_f32 v124, v148, v149
	v_rcp_f32_e32 v158, v158
	v_rcp_f32_e32 v159, v159
	v_mov_b32_dpp v125, v124 quad_perm:[1,2,3,0] row_mask:0xf bank_mask:0xf bound_ctrl:1
	v_mov_b32_dpp v126, v124 quad_perm:[2,3,0,1] row_mask:0xf bank_mask:0xf bound_ctrl:1
	v_mov_b32_dpp v127, v124 quad_perm:[3,0,1,2] row_mask:0xf bank_mask:0xf bound_ctrl:1
	v_pk_fma_f32 v[150:151], v[112:113], v[158:159], v[154:155]
	s_nop 0
	v_cvt_pk_f16_f32 v128, v150, v151
	ds_write_b32 v164, v124 offset:0
	s_nop 0
	v_mov_b32_dpp v129, v128 quad_perm:[1,2,3,0] row_mask:0xf bank_mask:0xf bound_ctrl:1
	v_mov_b32_dpp v130, v128 quad_perm:[2,3,0,1] row_mask:0xf bank_mask:0xf bound_ctrl:1
	v_mov_b32_dpp v131, v128 quad_perm:[3,0,1,2] row_mask:0xf bank_mask:0xf bound_ctrl:1
	ds_write_b32 v164, v128 offset:4
	s_waitcnt lgkmcnt(0)
	s_barrier
	s_waitcnt lgkmcnt(0)
	s_barrier
	s_waitcnt lgkmcnt(0)
	s_barrier
	s_waitcnt lgkmcnt(0)
	s_barrier
	s_branch .LBB3_175
.LBB3_169:
	s_bitcmp1_b32 s12, 0
	s_cselect_b32 s10, 0x2100, 0
	s_nop 0
	v_add_u32_e32 v164, s10, v122
	v_pk_fma_f32 v[154:155], v[106:107], v[150:151], v[108:109]
	v_pk_fma_f32 v[152:153], v[102:103], v[148:149], v[104:105]
	v_cndmask_b32_e64 v160, v136, v132, s[0:1]
	v_cndmask_b32_e64 v161, v137, v133, s[0:1]
	v_cndmask_b32_e64 v162, v138, v134, s[0:1]
	v_cndmask_b32_e64 v160, v140, v160, s[2:3]
	v_cndmask_b32_e64 v161, v141, v161, s[2:3]
	v_cndmask_b32_e64 v163, v139, v135, s[0:1]
	v_cndmask_b32_e64 v156, v160, v144, s[4:5]
	v_cndmask_b32_e64 v157, v161, v145, s[4:5]
	v_exp_f32_e32 v156, v156
	v_exp_f32_e32 v157, v157
	v_cndmask_b32_e64 v162, v142, v162, s[2:3]
	v_cndmask_b32_e64 v163, v143, v163, s[2:3]
	v_cndmask_b32_e64 v158, v162, v146, s[4:5]
	v_cndmask_b32_e64 v159, v163, v147, s[4:5]
	v_pk_add_f32 v[156:157], v[156:157], 1.0 op_sel_hi:[1,0]
	v_exp_f32_e32 v158, v158
	v_rcp_f32_e32 v156, v156
	v_rcp_f32_e32 v157, v157
	v_exp_f32_e32 v159, v159
	v_pk_fma_f32 v[148:149], v[110:111], v[156:157], v[152:153]
	v_pk_add_f32 v[158:159], v[158:159], 1.0 op_sel_hi:[1,0]
	v_cvt_pk_f16_f32 v124, v148, v149
	v_rcp_f32_e32 v158, v158
	v_rcp_f32_e32 v159, v159
	v_mov_b32_dpp v125, v124 quad_perm:[1,2,3,0] row_mask:0xf bank_mask:0xf bound_ctrl:1
	v_mov_b32_dpp v126, v124 quad_perm:[2,3,0,1] row_mask:0xf bank_mask:0xf bound_ctrl:1
	v_mov_b32_dpp v127, v124 quad_perm:[3,0,1,2] row_mask:0xf bank_mask:0xf bound_ctrl:1
	v_pk_fma_f32 v[150:151], v[112:113], v[158:159], v[154:155]
	s_waitcnt vmcnt(15)
	v_mfma_f32_16x16x32_f16 v[132:135], v[2:5], v[124:127], v[70:73]
	v_cvt_pk_f16_f32 v128, v150, v151
	s_nop 0
	v_mfma_f32_16x16x32_f16 v[136:139], v[10:13], v[124:127], v[70:73]
	v_mov_b32_dpp v129, v128 quad_perm:[1,2,3,0] row_mask:0xf bank_mask:0xf bound_ctrl:1
	v_mov_b32_dpp v130, v128 quad_perm:[2,3,0,1] row_mask:0xf bank_mask:0xf bound_ctrl:1
	v_mfma_f32_16x16x32_f16 v[140:143], v[18:21], v[124:127], v[70:73]
	v_mov_b32_dpp v131, v128 quad_perm:[3,0,1,2] row_mask:0xf bank_mask:0xf bound_ctrl:1
	ds_write_b32 v164, v124 offset:0
	v_mfma_f32_16x16x32_f16 v[144:147], v[26:29], v[124:127], v[70:73]
	global_load_dwordx4 v[70:73], v[0:1], off offset:-1792
	ds_write_b32 v164, v128 offset:4
	v_mfma_f32_16x16x32_f16 v[132:135], v[6:9], v[128:131], v[132:135]
	s_nop 1
	v_mfma_f32_16x16x32_f16 v[136:139], v[14:17], v[128:131], v[136:139]
	s_nop 1
	v_mfma_f32_16x16x32_f16 v[140:143], v[22:25], v[128:131], v[140:143]
	s_nop 1
	v_mfma_f32_16x16x32_f16 v[144:147], v[30:33], v[128:131], v[144:147]
	v_pk_fma_f32 v[154:155], v[106:107], v[150:151], v[108:109]
	v_pk_fma_f32 v[152:153], v[102:103], v[148:149], v[104:105]
	v_cndmask_b32_e64 v160, v136, v132, s[0:1]
	v_cndmask_b32_e64 v161, v137, v133, s[0:1]
	v_cndmask_b32_e64 v162, v138, v134, s[0:1]
	v_cndmask_b32_e64 v160, v140, v160, s[2:3]
	v_cndmask_b32_e64 v161, v141, v161, s[2:3]
	v_cndmask_b32_e64 v163, v139, v135, s[0:1]
	v_cndmask_b32_e64 v156, v160, v144, s[4:5]
	v_cndmask_b32_e64 v157, v161, v145, s[4:5]
	v_exp_f32_e32 v156, v156
	v_exp_f32_e32 v157, v157
	v_cndmask_b32_e64 v162, v142, v162, s[2:3]
	v_cndmask_b32_e64 v163, v143, v163, s[2:3]
	v_cndmask_b32_e64 v158, v162, v146, s[4:5]
	v_cndmask_b32_e64 v159, v163, v147, s[4:5]
	v_pk_add_f32 v[156:157], v[156:157], 1.0 op_sel_hi:[1,0]
	v_exp_f32_e32 v158, v158
	v_rcp_f32_e32 v156, v156
	v_rcp_f32_e32 v157, v157
	v_exp_f32_e32 v159, v159
	v_pk_fma_f32 v[148:149], v[110:111], v[156:157], v[152:153]
	v_pk_add_f32 v[158:159], v[158:159], 1.0 op_sel_hi:[1,0]
	v_cvt_pk_f16_f32 v124, v148, v149
	v_rcp_f32_e32 v158, v158
	v_rcp_f32_e32 v159, v159
	v_mov_b32_dpp v125, v124 quad_perm:[1,2,3,0] row_mask:0xf bank_mask:0xf bound_ctrl:1
	v_mov_b32_dpp v126, v124 quad_perm:[2,3,0,1] row_mask:0xf bank_mask:0xf bound_ctrl:1
	v_mov_b32_dpp v127, v124 quad_perm:[3,0,1,2] row_mask:0xf bank_mask:0xf bound_ctrl:1
	v_pk_fma_f32 v[150:151], v[112:113], v[158:159], v[154:155]
	s_waitcnt vmcnt(15)
	v_mfma_f32_16x16x32_f16 v[132:135], v[2:5], v[124:127], v[78:81]
	v_cvt_pk_f16_f32 v128, v150, v151
	s_nop 0
	v_mfma_f32_16x16x32_f16 v[136:139], v[10:13], v[124:127], v[78:81]
	v_mov_b32_dpp v129, v128 quad_perm:[1,2,3,0] row_mask:0xf bank_mask:0xf bound_ctrl:1
	v_mov_b32_dpp v130, v128 quad_perm:[2,3,0,1] row_mask:0xf bank_mask:0xf bound_ctrl:1
	v_mfma_f32_16x16x32_f16 v[140:143], v[18:21], v[124:127], v[78:81]
	v_mov_b32_dpp v131, v128 quad_perm:[3,0,1,2] row_mask:0xf bank_mask:0xf bound_ctrl:1
	ds_write_b32 v164, v124 offset:528
	v_mfma_f32_16x16x32_f16 v[144:147], v[26:29], v[124:127], v[78:81]
	global_load_dwordx4 v[78:81], v[0:1], off offset:-1536
	ds_write_b32 v164, v128 offset:532
	v_mfma_f32_16x16x32_f16 v[132:135], v[6:9], v[128:131], v[132:135]
	s_nop 1
	v_mfma_f32_16x16x32_f16 v[136:139], v[14:17], v[128:131], v[136:139]
	s_nop 1
	v_mfma_f32_16x16x32_f16 v[140:143], v[22:25], v[128:131], v[140:143]
	s_nop 1
	v_mfma_f32_16x16x32_f16 v[144:147], v[30:33], v[128:131], v[144:147]
	v_pk_fma_f32 v[154:155], v[106:107], v[150:151], v[108:109]
	v_pk_fma_f32 v[152:153], v[102:103], v[148:149], v[104:105]
	v_cndmask_b32_e64 v160, v136, v132, s[0:1]
	v_cndmask_b32_e64 v161, v137, v133, s[0:1]
	v_cndmask_b32_e64 v162, v138, v134, s[0:1]
	v_cndmask_b32_e64 v160, v140, v160, s[2:3]
	v_cndmask_b32_e64 v161, v141, v161, s[2:3]
	v_cndmask_b32_e64 v163, v139, v135, s[0:1]
	v_cndmask_b32_e64 v156, v160, v144, s[4:5]
	v_cndmask_b32_e64 v157, v161, v145, s[4:5]
	v_exp_f32_e32 v156, v156
	v_exp_f32_e32 v157, v157
	v_cndmask_b32_e64 v162, v142, v162, s[2:3]
	v_cndmask_b32_e64 v163, v143, v163, s[2:3]
	v_cndmask_b32_e64 v158, v162, v146, s[4:5]
	v_cndmask_b32_e64 v159, v163, v147, s[4:5]
	v_pk_add_f32 v[156:157], v[156:157], 1.0 op_sel_hi:[1,0]
	v_exp_f32_e32 v158, v158
	v_rcp_f32_e32 v156, v156
	v_rcp_f32_e32 v157, v157
	v_exp_f32_e32 v159, v159
	v_pk_fma_f32 v[148:149], v[110:111], v[156:157], v[152:153]
	v_pk_add_f32 v[158:159], v[158:159], 1.0 op_sel_hi:[1,0]
	v_cvt_pk_f16_f32 v124, v148, v149
	v_rcp_f32_e32 v158, v158
	v_rcp_f32_e32 v159, v159
	v_mov_b32_dpp v125, v124 quad_perm:[1,2,3,0] row_mask:0xf bank_mask:0xf bound_ctrl:1
	v_mov_b32_dpp v126, v124 quad_perm:[2,3,0,1] row_mask:0xf bank_mask:0xf bound_ctrl:1
	v_mov_b32_dpp v127, v124 quad_perm:[3,0,1,2] row_mask:0xf bank_mask:0xf bound_ctrl:1
	v_pk_fma_f32 v[150:151], v[112:113], v[158:159], v[154:155]
	s_waitcnt vmcnt(15)
	v_mfma_f32_16x16x32_f16 v[132:135], v[2:5], v[124:127], v[86:89]
	v_cvt_pk_f16_f32 v128, v150, v151
	s_nop 0
	v_mfma_f32_16x16x32_f16 v[136:139], v[10:13], v[124:127], v[86:89]
	v_mov_b32_dpp v129, v128 quad_perm:[1,2,3,0] row_mask:0xf bank_mask:0xf bound_ctrl:1
	v_mov_b32_dpp v130, v128 quad_perm:[2,3,0,1] row_mask:0xf bank_mask:0xf bound_ctrl:1
	v_mfma_f32_16x16x32_f16 v[140:143], v[18:21], v[124:127], v[86:89]
	v_mov_b32_dpp v131, v128 quad_perm:[3,0,1,2] row_mask:0xf bank_mask:0xf bound_ctrl:1
	ds_write_b32 v164, v124 offset:1056
	v_mfma_f32_16x16x32_f16 v[144:147], v[26:29], v[124:127], v[86:89]
	global_load_dwordx4 v[86:89], v[0:1], off offset:-1280
	ds_write_b32 v164, v128 offset:1060
	v_mfma_f32_16x16x32_f16 v[132:135], v[6:9], v[128:131], v[132:135]
	s_nop 1
	v_mfma_f32_16x16x32_f16 v[136:139], v[14:17], v[128:131], v[136:139]
	s_nop 1
	v_mfma_f32_16x16x32_f16 v[140:143], v[22:25], v[128:131], v[140:143]
	s_nop 1
	v_mfma_f32_16x16x32_f16 v[144:147], v[30:33], v[128:131], v[144:147]
	v_pk_fma_f32 v[154:155], v[106:107], v[150:151], v[108:109]
	v_pk_fma_f32 v[152:153], v[102:103], v[148:149], v[104:105]
	v_cndmask_b32_e64 v160, v136, v132, s[0:1]
	v_cndmask_b32_e64 v161, v137, v133, s[0:1]
	v_cndmask_b32_e64 v162, v138, v134, s[0:1]
	v_cndmask_b32_e64 v160, v140, v160, s[2:3]
	v_cndmask_b32_e64 v161, v141, v161, s[2:3]
	v_cndmask_b32_e64 v163, v139, v135, s[0:1]
	v_cndmask_b32_e64 v156, v160, v144, s[4:5]
	v_cndmask_b32_e64 v157, v161, v145, s[4:5]
	v_exp_f32_e32 v156, v156
	v_exp_f32_e32 v157, v157
	v_cndmask_b32_e64 v162, v142, v162, s[2:3]
	v_cndmask_b32_e64 v163, v143, v163, s[2:3]
	v_cndmask_b32_e64 v158, v162, v146, s[4:5]
	v_cndmask_b32_e64 v159, v163, v147, s[4:5]
	v_pk_add_f32 v[156:157], v[156:157], 1.0 op_sel_hi:[1,0]
	v_exp_f32_e32 v158, v158
	v_rcp_f32_e32 v156, v156
	v_rcp_f32_e32 v157, v157
	v_exp_f32_e32 v159, v159
	v_pk_fma_f32 v[148:149], v[110:111], v[156:157], v[152:153]
	v_pk_add_f32 v[158:159], v[158:159], 1.0 op_sel_hi:[1,0]
	v_cvt_pk_f16_f32 v124, v148, v149
	v_rcp_f32_e32 v158, v158
	v_rcp_f32_e32 v159, v159
	v_mov_b32_dpp v125, v124 quad_perm:[1,2,3,0] row_mask:0xf bank_mask:0xf bound_ctrl:1
	v_mov_b32_dpp v126, v124 quad_perm:[2,3,0,1] row_mask:0xf bank_mask:0xf bound_ctrl:1
	v_mov_b32_dpp v127, v124 quad_perm:[3,0,1,2] row_mask:0xf bank_mask:0xf bound_ctrl:1
	v_pk_fma_f32 v[150:151], v[112:113], v[158:159], v[154:155]
	s_waitcnt vmcnt(15)
	v_mfma_f32_16x16x32_f16 v[132:135], v[2:5], v[124:127], v[94:97]
	v_cvt_pk_f16_f32 v128, v150, v151
	s_nop 0
	v_mfma_f32_16x16x32_f16 v[136:139], v[10:13], v[124:127], v[94:97]
	v_mov_b32_dpp v129, v128 quad_perm:[1,2,3,0] row_mask:0xf bank_mask:0xf bound_ctrl:1
	v_mov_b32_dpp v130, v128 quad_perm:[2,3,0,1] row_mask:0xf bank_mask:0xf bound_ctrl:1
	v_mfma_f32_16x16x32_f16 v[140:143], v[18:21], v[124:127], v[94:97]
	v_mov_b32_dpp v131, v128 quad_perm:[3,0,1,2] row_mask:0xf bank_mask:0xf bound_ctrl:1
	ds_write_b32 v164, v124 offset:1584
	v_mfma_f32_16x16x32_f16 v[144:147], v[26:29], v[124:127], v[94:97]
	global_load_dwordx4 v[94:97], v[0:1], off offset:-1024
	ds_write_b32 v164, v128 offset:1588
	v_mfma_f32_16x16x32_f16 v[132:135], v[6:9], v[128:131], v[132:135]
	s_nop 1
	v_mfma_f32_16x16x32_f16 v[136:139], v[14:17], v[128:131], v[136:139]
	s_nop 1
	v_mfma_f32_16x16x32_f16 v[140:143], v[22:25], v[128:131], v[140:143]
	s_nop 1
	v_mfma_f32_16x16x32_f16 v[144:147], v[30:33], v[128:131], v[144:147]
	v_pk_fma_f32 v[154:155], v[106:107], v[150:151], v[108:109]
	v_pk_fma_f32 v[152:153], v[102:103], v[148:149], v[104:105]
	v_cndmask_b32_e64 v160, v136, v132, s[0:1]
	v_cndmask_b32_e64 v161, v137, v133, s[0:1]
	v_cndmask_b32_e64 v162, v138, v134, s[0:1]
	v_cndmask_b32_e64 v160, v140, v160, s[2:3]
	v_cndmask_b32_e64 v161, v141, v161, s[2:3]
	v_cndmask_b32_e64 v163, v139, v135, s[0:1]
	v_cndmask_b32_e64 v156, v160, v144, s[4:5]
	v_cndmask_b32_e64 v157, v161, v145, s[4:5]
	v_exp_f32_e32 v156, v156
	v_exp_f32_e32 v157, v157
	v_cndmask_b32_e64 v162, v142, v162, s[2:3]
	v_cndmask_b32_e64 v163, v143, v163, s[2:3]
	v_cndmask_b32_e64 v158, v162, v146, s[4:5]
	v_cndmask_b32_e64 v159, v163, v147, s[4:5]
	v_pk_add_f32 v[156:157], v[156:157], 1.0 op_sel_hi:[1,0]
	v_exp_f32_e32 v158, v158
	v_rcp_f32_e32 v156, v156
	v_rcp_f32_e32 v157, v157
	v_exp_f32_e32 v159, v159
	v_pk_fma_f32 v[148:149], v[110:111], v[156:157], v[152:153]
	v_pk_add_f32 v[158:159], v[158:159], 1.0 op_sel_hi:[1,0]
	v_cvt_pk_f16_f32 v124, v148, v149
	v_rcp_f32_e32 v158, v158
	v_rcp_f32_e32 v159, v159
	v_mov_b32_dpp v125, v124 quad_perm:[1,2,3,0] row_mask:0xf bank_mask:0xf bound_ctrl:1
	v_mov_b32_dpp v126, v124 quad_perm:[2,3,0,1] row_mask:0xf bank_mask:0xf bound_ctrl:1
	v_mov_b32_dpp v127, v124 quad_perm:[3,0,1,2] row_mask:0xf bank_mask:0xf bound_ctrl:1
	v_pk_fma_f32 v[150:151], v[112:113], v[158:159], v[154:155]
	s_waitcnt vmcnt(15)
	v_mfma_f32_16x16x32_f16 v[132:135], v[2:5], v[124:127], v[90:93]
	v_cvt_pk_f16_f32 v128, v150, v151
	s_nop 0
	v_mfma_f32_16x16x32_f16 v[136:139], v[10:13], v[124:127], v[90:93]
	v_mov_b32_dpp v129, v128 quad_perm:[1,2,3,0] row_mask:0xf bank_mask:0xf bound_ctrl:1
	v_mov_b32_dpp v130, v128 quad_perm:[2,3,0,1] row_mask:0xf bank_mask:0xf bound_ctrl:1
	v_mfma_f32_16x16x32_f16 v[140:143], v[18:21], v[124:127], v[90:93]
	v_mov_b32_dpp v131, v128 quad_perm:[3,0,1,2] row_mask:0xf bank_mask:0xf bound_ctrl:1
	ds_write_b32 v164, v124 offset:2112
	v_mfma_f32_16x16x32_f16 v[144:147], v[26:29], v[124:127], v[90:93]
	global_load_dwordx4 v[90:93], v[0:1], off offset:-768
	ds_write_b32 v164, v128 offset:2116
	v_mfma_f32_16x16x32_f16 v[132:135], v[6:9], v[128:131], v[132:135]
	s_nop 1
	v_mfma_f32_16x16x32_f16 v[136:139], v[14:17], v[128:131], v[136:139]
	s_nop 1
	v_mfma_f32_16x16x32_f16 v[140:143], v[22:25], v[128:131], v[140:143]
	s_nop 1
	v_mfma_f32_16x16x32_f16 v[144:147], v[30:33], v[128:131], v[144:147]
	v_pk_fma_f32 v[154:155], v[106:107], v[150:151], v[108:109]
	v_pk_fma_f32 v[152:153], v[102:103], v[148:149], v[104:105]
	v_cndmask_b32_e64 v160, v136, v132, s[0:1]
	v_cndmask_b32_e64 v161, v137, v133, s[0:1]
	v_cndmask_b32_e64 v162, v138, v134, s[0:1]
	v_cndmask_b32_e64 v160, v140, v160, s[2:3]
	v_cndmask_b32_e64 v161, v141, v161, s[2:3]
	v_cndmask_b32_e64 v163, v139, v135, s[0:1]
	v_cndmask_b32_e64 v156, v160, v144, s[4:5]
	v_cndmask_b32_e64 v157, v161, v145, s[4:5]
	v_exp_f32_e32 v156, v156
	v_exp_f32_e32 v157, v157
	v_cndmask_b32_e64 v162, v142, v162, s[2:3]
	v_cndmask_b32_e64 v163, v143, v163, s[2:3]
	v_cndmask_b32_e64 v158, v162, v146, s[4:5]
	v_cndmask_b32_e64 v159, v163, v147, s[4:5]
	v_pk_add_f32 v[156:157], v[156:157], 1.0 op_sel_hi:[1,0]
	v_exp_f32_e32 v158, v158
	v_rcp_f32_e32 v156, v156
	v_rcp_f32_e32 v157, v157
	v_exp_f32_e32 v159, v159
	v_pk_fma_f32 v[148:149], v[110:111], v[156:157], v[152:153]
	v_pk_add_f32 v[158:159], v[158:159], 1.0 op_sel_hi:[1,0]
	v_cvt_pk_f16_f32 v124, v148, v149
	v_rcp_f32_e32 v158, v158
	v_rcp_f32_e32 v159, v159
	v_mov_b32_dpp v125, v124 quad_perm:[1,2,3,0] row_mask:0xf bank_mask:0xf bound_ctrl:1
	v_mov_b32_dpp v126, v124 quad_perm:[2,3,0,1] row_mask:0xf bank_mask:0xf bound_ctrl:1
	v_mov_b32_dpp v127, v124 quad_perm:[3,0,1,2] row_mask:0xf bank_mask:0xf bound_ctrl:1
	v_pk_fma_f32 v[150:151], v[112:113], v[158:159], v[154:155]
	s_waitcnt vmcnt(15)
	v_mfma_f32_16x16x32_f16 v[132:135], v[2:5], v[124:127], v[82:85]
	v_cvt_pk_f16_f32 v128, v150, v151
	s_nop 0
	v_mfma_f32_16x16x32_f16 v[136:139], v[10:13], v[124:127], v[82:85]
	v_mov_b32_dpp v129, v128 quad_perm:[1,2,3,0] row_mask:0xf bank_mask:0xf bound_ctrl:1
	v_mov_b32_dpp v130, v128 quad_perm:[2,3,0,1] row_mask:0xf bank_mask:0xf bound_ctrl:1
	v_mfma_f32_16x16x32_f16 v[140:143], v[18:21], v[124:127], v[82:85]
	v_mov_b32_dpp v131, v128 quad_perm:[3,0,1,2] row_mask:0xf bank_mask:0xf bound_ctrl:1
	ds_write_b32 v164, v124 offset:2640
	v_mfma_f32_16x16x32_f16 v[144:147], v[26:29], v[124:127], v[82:85]
	global_load_dwordx4 v[82:85], v[0:1], off offset:-512
	ds_write_b32 v164, v128 offset:2644
	v_mfma_f32_16x16x32_f16 v[132:135], v[6:9], v[128:131], v[132:135]
	s_nop 1
	v_mfma_f32_16x16x32_f16 v[136:139], v[14:17], v[128:131], v[136:139]
	s_nop 1
	v_mfma_f32_16x16x32_f16 v[140:143], v[22:25], v[128:131], v[140:143]
	s_nop 1
	v_mfma_f32_16x16x32_f16 v[144:147], v[30:33], v[128:131], v[144:147]
	v_pk_fma_f32 v[154:155], v[106:107], v[150:151], v[108:109]
	v_pk_fma_f32 v[152:153], v[102:103], v[148:149], v[104:105]
	v_cndmask_b32_e64 v160, v136, v132, s[0:1]
	v_cndmask_b32_e64 v161, v137, v133, s[0:1]
	v_cndmask_b32_e64 v162, v138, v134, s[0:1]
	v_cndmask_b32_e64 v160, v140, v160, s[2:3]
	v_cndmask_b32_e64 v161, v141, v161, s[2:3]
	v_cndmask_b32_e64 v163, v139, v135, s[0:1]
	v_cndmask_b32_e64 v156, v160, v144, s[4:5]
	v_cndmask_b32_e64 v157, v161, v145, s[4:5]
	v_exp_f32_e32 v156, v156
	v_exp_f32_e32 v157, v157
	v_cndmask_b32_e64 v162, v142, v162, s[2:3]
	v_cndmask_b32_e64 v163, v143, v163, s[2:3]
	v_cndmask_b32_e64 v158, v162, v146, s[4:5]
	v_cndmask_b32_e64 v159, v163, v147, s[4:5]
	v_pk_add_f32 v[156:157], v[156:157], 1.0 op_sel_hi:[1,0]
	v_exp_f32_e32 v158, v158
	v_rcp_f32_e32 v156, v156
	v_rcp_f32_e32 v157, v157
	v_exp_f32_e32 v159, v159
	v_pk_fma_f32 v[148:149], v[110:111], v[156:157], v[152:153]
	v_pk_add_f32 v[158:159], v[158:159], 1.0 op_sel_hi:[1,0]
	v_cvt_pk_f16_f32 v124, v148, v149
	v_rcp_f32_e32 v158, v158
	v_rcp_f32_e32 v159, v159
	v_mov_b32_dpp v125, v124 quad_perm:[1,2,3,0] row_mask:0xf bank_mask:0xf bound_ctrl:1
	v_mov_b32_dpp v126, v124 quad_perm:[2,3,0,1] row_mask:0xf bank_mask:0xf bound_ctrl:1
	v_mov_b32_dpp v127, v124 quad_perm:[3,0,1,2] row_mask:0xf bank_mask:0xf bound_ctrl:1
	v_pk_fma_f32 v[150:151], v[112:113], v[158:159], v[154:155]
	s_waitcnt vmcnt(15)
	v_mfma_f32_16x16x32_f16 v[132:135], v[2:5], v[124:127], v[74:77]
	v_cvt_pk_f16_f32 v128, v150, v151
	s_nop 0
	v_mfma_f32_16x16x32_f16 v[136:139], v[10:13], v[124:127], v[74:77]
	v_mov_b32_dpp v129, v128 quad_perm:[1,2,3,0] row_mask:0xf bank_mask:0xf bound_ctrl:1
	v_mov_b32_dpp v130, v128 quad_perm:[2,3,0,1] row_mask:0xf bank_mask:0xf bound_ctrl:1
	v_mfma_f32_16x16x32_f16 v[140:143], v[18:21], v[124:127], v[74:77]
	v_mov_b32_dpp v131, v128 quad_perm:[3,0,1,2] row_mask:0xf bank_mask:0xf bound_ctrl:1
	ds_write_b32 v164, v124 offset:3168
	v_mfma_f32_16x16x32_f16 v[144:147], v[26:29], v[124:127], v[74:77]
	global_load_dwordx4 v[74:77], v[0:1], off offset:-256
	ds_write_b32 v164, v128 offset:3172
	v_mfma_f32_16x16x32_f16 v[132:135], v[6:9], v[128:131], v[132:135]
	s_nop 1
	v_mfma_f32_16x16x32_f16 v[136:139], v[14:17], v[128:131], v[136:139]
	s_nop 1
	v_mfma_f32_16x16x32_f16 v[140:143], v[22:25], v[128:131], v[140:143]
	s_nop 1
	v_mfma_f32_16x16x32_f16 v[144:147], v[30:33], v[128:131], v[144:147]
	v_pk_fma_f32 v[154:155], v[106:107], v[150:151], v[108:109]
	v_pk_fma_f32 v[152:153], v[102:103], v[148:149], v[104:105]
	v_cndmask_b32_e64 v160, v136, v132, s[0:1]
	v_cndmask_b32_e64 v161, v137, v133, s[0:1]
	v_cndmask_b32_e64 v162, v138, v134, s[0:1]
	v_cndmask_b32_e64 v160, v140, v160, s[2:3]
	v_cndmask_b32_e64 v161, v141, v161, s[2:3]
	v_cndmask_b32_e64 v163, v139, v135, s[0:1]
	v_cndmask_b32_e64 v156, v160, v144, s[4:5]
	v_cndmask_b32_e64 v157, v161, v145, s[4:5]
	v_exp_f32_e32 v156, v156
	v_exp_f32_e32 v157, v157
	v_cndmask_b32_e64 v162, v142, v162, s[2:3]
	v_cndmask_b32_e64 v163, v143, v163, s[2:3]
	v_cndmask_b32_e64 v158, v162, v146, s[4:5]
	v_cndmask_b32_e64 v159, v163, v147, s[4:5]
	v_pk_add_f32 v[156:157], v[156:157], 1.0 op_sel_hi:[1,0]
	v_exp_f32_e32 v158, v158
	v_rcp_f32_e32 v156, v156
	v_rcp_f32_e32 v157, v157
	v_exp_f32_e32 v159, v159
	v_pk_fma_f32 v[148:149], v[110:111], v[156:157], v[152:153]
	v_pk_add_f32 v[158:159], v[158:159], 1.0 op_sel_hi:[1,0]
	v_cvt_pk_f16_f32 v124, v148, v149
	v_rcp_f32_e32 v158, v158
	v_rcp_f32_e32 v159, v159
	v_mov_b32_dpp v125, v124 quad_perm:[1,2,3,0] row_mask:0xf bank_mask:0xf bound_ctrl:1
	v_mov_b32_dpp v126, v124 quad_perm:[2,3,0,1] row_mask:0xf bank_mask:0xf bound_ctrl:1
	v_mov_b32_dpp v127, v124 quad_perm:[3,0,1,2] row_mask:0xf bank_mask:0xf bound_ctrl:1
	v_pk_fma_f32 v[150:151], v[112:113], v[158:159], v[154:155]
	s_waitcnt vmcnt(15)
	v_mfma_f32_16x16x32_f16 v[132:135], v[2:5], v[124:127], v[66:69]
	v_cvt_pk_f16_f32 v128, v150, v151
	s_nop 0
	v_mfma_f32_16x16x32_f16 v[136:139], v[10:13], v[124:127], v[66:69]
	v_mov_b32_dpp v129, v128 quad_perm:[1,2,3,0] row_mask:0xf bank_mask:0xf bound_ctrl:1
	v_mov_b32_dpp v130, v128 quad_perm:[2,3,0,1] row_mask:0xf bank_mask:0xf bound_ctrl:1
	v_mfma_f32_16x16x32_f16 v[140:143], v[18:21], v[124:127], v[66:69]
	v_mov_b32_dpp v131, v128 quad_perm:[3,0,1,2] row_mask:0xf bank_mask:0xf bound_ctrl:1
	ds_write_b32 v164, v124 offset:3696
	v_mfma_f32_16x16x32_f16 v[144:147], v[26:29], v[124:127], v[66:69]
	global_load_dwordx4 v[66:69], v[0:1], off offset:0
	ds_write_b32 v164, v128 offset:3700
	v_mfma_f32_16x16x32_f16 v[132:135], v[6:9], v[128:131], v[132:135]
	s_nop 1
	v_mfma_f32_16x16x32_f16 v[136:139], v[14:17], v[128:131], v[136:139]
	s_nop 1
	v_mfma_f32_16x16x32_f16 v[140:143], v[22:25], v[128:131], v[140:143]
	s_nop 1
	v_mfma_f32_16x16x32_f16 v[144:147], v[30:33], v[128:131], v[144:147]
	v_pk_fma_f32 v[154:155], v[106:107], v[150:151], v[108:109]
	v_pk_fma_f32 v[152:153], v[102:103], v[148:149], v[104:105]
	v_cndmask_b32_e64 v160, v136, v132, s[0:1]
	v_cndmask_b32_e64 v161, v137, v133, s[0:1]
	v_cndmask_b32_e64 v162, v138, v134, s[0:1]
	v_cndmask_b32_e64 v160, v140, v160, s[2:3]
	v_cndmask_b32_e64 v161, v141, v161, s[2:3]
	v_cndmask_b32_e64 v163, v139, v135, s[0:1]
	v_cndmask_b32_e64 v156, v160, v144, s[4:5]
	v_cndmask_b32_e64 v157, v161, v145, s[4:5]
	v_exp_f32_e32 v156, v156
	v_exp_f32_e32 v157, v157
	v_cndmask_b32_e64 v162, v142, v162, s[2:3]
	v_cndmask_b32_e64 v163, v143, v163, s[2:3]
	v_cndmask_b32_e64 v158, v162, v146, s[4:5]
	v_cndmask_b32_e64 v159, v163, v147, s[4:5]
	v_pk_add_f32 v[156:157], v[156:157], 1.0 op_sel_hi:[1,0]
	v_exp_f32_e32 v158, v158
	v_rcp_f32_e32 v156, v156
	v_rcp_f32_e32 v157, v157
	v_exp_f32_e32 v159, v159
	v_pk_fma_f32 v[148:149], v[110:111], v[156:157], v[152:153]
	v_pk_add_f32 v[158:159], v[158:159], 1.0 op_sel_hi:[1,0]
	v_cvt_pk_f16_f32 v124, v148, v149
	v_rcp_f32_e32 v158, v158
	v_rcp_f32_e32 v159, v159
	v_mov_b32_dpp v125, v124 quad_perm:[1,2,3,0] row_mask:0xf bank_mask:0xf bound_ctrl:1
	v_mov_b32_dpp v126, v124 quad_perm:[2,3,0,1] row_mask:0xf bank_mask:0xf bound_ctrl:1
	v_mov_b32_dpp v127, v124 quad_perm:[3,0,1,2] row_mask:0xf bank_mask:0xf bound_ctrl:1
	v_pk_fma_f32 v[150:151], v[112:113], v[158:159], v[154:155]
	s_waitcnt vmcnt(15)
	v_mfma_f32_16x16x32_f16 v[132:135], v[2:5], v[124:127], v[58:61]
	v_cvt_pk_f16_f32 v128, v150, v151
	s_nop 0
	v_mfma_f32_16x16x32_f16 v[136:139], v[10:13], v[124:127], v[58:61]
	v_mov_b32_dpp v129, v128 quad_perm:[1,2,3,0] row_mask:0xf bank_mask:0xf bound_ctrl:1
	v_mov_b32_dpp v130, v128 quad_perm:[2,3,0,1] row_mask:0xf bank_mask:0xf bound_ctrl:1
	v_mfma_f32_16x16x32_f16 v[140:143], v[18:21], v[124:127], v[58:61]
	v_mov_b32_dpp v131, v128 quad_perm:[3,0,1,2] row_mask:0xf bank_mask:0xf bound_ctrl:1
	ds_write_b32 v164, v124 offset:4224
	v_mfma_f32_16x16x32_f16 v[144:147], v[26:29], v[124:127], v[58:61]
	global_load_dwordx4 v[58:61], v[0:1], off offset:256
	ds_write_b32 v164, v128 offset:4228
	v_mfma_f32_16x16x32_f16 v[132:135], v[6:9], v[128:131], v[132:135]
	s_nop 1
	v_mfma_f32_16x16x32_f16 v[136:139], v[14:17], v[128:131], v[136:139]
	s_nop 1
	v_mfma_f32_16x16x32_f16 v[140:143], v[22:25], v[128:131], v[140:143]
	s_nop 1
	v_mfma_f32_16x16x32_f16 v[144:147], v[30:33], v[128:131], v[144:147]
	v_pk_fma_f32 v[154:155], v[106:107], v[150:151], v[108:109]
	v_pk_fma_f32 v[152:153], v[102:103], v[148:149], v[104:105]
	v_cndmask_b32_e64 v160, v136, v132, s[0:1]
	v_cndmask_b32_e64 v161, v137, v133, s[0:1]
	v_cndmask_b32_e64 v162, v138, v134, s[0:1]
	v_cndmask_b32_e64 v160, v140, v160, s[2:3]
	v_cndmask_b32_e64 v161, v141, v161, s[2:3]
	v_cndmask_b32_e64 v163, v139, v135, s[0:1]
	v_cndmask_b32_e64 v156, v160, v144, s[4:5]
	v_cndmask_b32_e64 v157, v161, v145, s[4:5]
	v_exp_f32_e32 v156, v156
	v_exp_f32_e32 v157, v157
	v_cndmask_b32_e64 v162, v142, v162, s[2:3]
	v_cndmask_b32_e64 v163, v143, v163, s[2:3]
	v_cndmask_b32_e64 v158, v162, v146, s[4:5]
	v_cndmask_b32_e64 v159, v163, v147, s[4:5]
	v_pk_add_f32 v[156:157], v[156:157], 1.0 op_sel_hi:[1,0]
	v_exp_f32_e32 v158, v158
	v_rcp_f32_e32 v156, v156
	v_rcp_f32_e32 v157, v157
	v_exp_f32_e32 v159, v159
	v_pk_fma_f32 v[148:149], v[110:111], v[156:157], v[152:153]
	v_pk_add_f32 v[158:159], v[158:159], 1.0 op_sel_hi:[1,0]
	v_cvt_pk_f16_f32 v124, v148, v149
	v_rcp_f32_e32 v158, v158
	v_rcp_f32_e32 v159, v159
	v_mov_b32_dpp v125, v124 quad_perm:[1,2,3,0] row_mask:0xf bank_mask:0xf bound_ctrl:1
	v_mov_b32_dpp v126, v124 quad_perm:[2,3,0,1] row_mask:0xf bank_mask:0xf bound_ctrl:1
	v_mov_b32_dpp v127, v124 quad_perm:[3,0,1,2] row_mask:0xf bank_mask:0xf bound_ctrl:1
	v_pk_fma_f32 v[150:151], v[112:113], v[158:159], v[154:155]
	s_waitcnt vmcnt(15)
	v_mfma_f32_16x16x32_f16 v[132:135], v[2:5], v[124:127], v[54:57]
	v_cvt_pk_f16_f32 v128, v150, v151
	s_nop 0
	v_mfma_f32_16x16x32_f16 v[136:139], v[10:13], v[124:127], v[54:57]
	v_mov_b32_dpp v129, v128 quad_perm:[1,2,3,0] row_mask:0xf bank_mask:0xf bound_ctrl:1
	v_mov_b32_dpp v130, v128 quad_perm:[2,3,0,1] row_mask:0xf bank_mask:0xf bound_ctrl:1
	v_mfma_f32_16x16x32_f16 v[140:143], v[18:21], v[124:127], v[54:57]
	v_mov_b32_dpp v131, v128 quad_perm:[3,0,1,2] row_mask:0xf bank_mask:0xf bound_ctrl:1
	ds_write_b32 v164, v124 offset:4752
	v_mfma_f32_16x16x32_f16 v[144:147], v[26:29], v[124:127], v[54:57]
	global_load_dwordx4 v[54:57], v[0:1], off offset:512
	ds_write_b32 v164, v128 offset:4756
	v_mfma_f32_16x16x32_f16 v[132:135], v[6:9], v[128:131], v[132:135]
	s_nop 1
	v_mfma_f32_16x16x32_f16 v[136:139], v[14:17], v[128:131], v[136:139]
	s_nop 1
	v_mfma_f32_16x16x32_f16 v[140:143], v[22:25], v[128:131], v[140:143]
	s_nop 1
	v_mfma_f32_16x16x32_f16 v[144:147], v[30:33], v[128:131], v[144:147]
	v_pk_fma_f32 v[154:155], v[106:107], v[150:151], v[108:109]
	v_pk_fma_f32 v[152:153], v[102:103], v[148:149], v[104:105]
	v_cndmask_b32_e64 v160, v136, v132, s[0:1]
	v_cndmask_b32_e64 v161, v137, v133, s[0:1]
	v_cndmask_b32_e64 v162, v138, v134, s[0:1]
	v_cndmask_b32_e64 v160, v140, v160, s[2:3]
	v_cndmask_b32_e64 v161, v141, v161, s[2:3]
	v_cndmask_b32_e64 v163, v139, v135, s[0:1]
	v_cndmask_b32_e64 v156, v160, v144, s[4:5]
	v_cndmask_b32_e64 v157, v161, v145, s[4:5]
	v_exp_f32_e32 v156, v156
	v_exp_f32_e32 v157, v157
	v_cndmask_b32_e64 v162, v142, v162, s[2:3]
	v_cndmask_b32_e64 v163, v143, v163, s[2:3]
	v_cndmask_b32_e64 v158, v162, v146, s[4:5]
	v_cndmask_b32_e64 v159, v163, v147, s[4:5]
	v_pk_add_f32 v[156:157], v[156:157], 1.0 op_sel_hi:[1,0]
	v_exp_f32_e32 v158, v158
	v_rcp_f32_e32 v156, v156
	v_rcp_f32_e32 v157, v157
	v_exp_f32_e32 v159, v159
	v_pk_fma_f32 v[148:149], v[110:111], v[156:157], v[152:153]
	v_pk_add_f32 v[158:159], v[158:159], 1.0 op_sel_hi:[1,0]
	v_cvt_pk_f16_f32 v124, v148, v149
	v_rcp_f32_e32 v158, v158
	v_rcp_f32_e32 v159, v159
	v_mov_b32_dpp v125, v124 quad_perm:[1,2,3,0] row_mask:0xf bank_mask:0xf bound_ctrl:1
	v_mov_b32_dpp v126, v124 quad_perm:[2,3,0,1] row_mask:0xf bank_mask:0xf bound_ctrl:1
	v_mov_b32_dpp v127, v124 quad_perm:[3,0,1,2] row_mask:0xf bank_mask:0xf bound_ctrl:1
	v_pk_fma_f32 v[150:151], v[112:113], v[158:159], v[154:155]
	s_waitcnt vmcnt(15)
	v_mfma_f32_16x16x32_f16 v[132:135], v[2:5], v[124:127], v[50:53]
	v_cvt_pk_f16_f32 v128, v150, v151
	s_nop 0
	v_mfma_f32_16x16x32_f16 v[136:139], v[10:13], v[124:127], v[50:53]
	v_mov_b32_dpp v129, v128 quad_perm:[1,2,3,0] row_mask:0xf bank_mask:0xf bound_ctrl:1
	v_mov_b32_dpp v130, v128 quad_perm:[2,3,0,1] row_mask:0xf bank_mask:0xf bound_ctrl:1
	v_mfma_f32_16x16x32_f16 v[140:143], v[18:21], v[124:127], v[50:53]
	v_mov_b32_dpp v131, v128 quad_perm:[3,0,1,2] row_mask:0xf bank_mask:0xf bound_ctrl:1
	ds_write_b32 v164, v124 offset:5280
	v_mfma_f32_16x16x32_f16 v[144:147], v[26:29], v[124:127], v[50:53]
	global_load_dwordx4 v[50:53], v[0:1], off offset:768
	ds_write_b32 v164, v128 offset:5284
	v_mfma_f32_16x16x32_f16 v[132:135], v[6:9], v[128:131], v[132:135]
	s_nop 1
	v_mfma_f32_16x16x32_f16 v[136:139], v[14:17], v[128:131], v[136:139]
	s_nop 1
	v_mfma_f32_16x16x32_f16 v[140:143], v[22:25], v[128:131], v[140:143]
	s_nop 1
	v_mfma_f32_16x16x32_f16 v[144:147], v[30:33], v[128:131], v[144:147]
	v_pk_fma_f32 v[154:155], v[106:107], v[150:151], v[108:109]
	v_pk_fma_f32 v[152:153], v[102:103], v[148:149], v[104:105]
	v_cndmask_b32_e64 v160, v136, v132, s[0:1]
	v_cndmask_b32_e64 v161, v137, v133, s[0:1]
	v_cndmask_b32_e64 v162, v138, v134, s[0:1]
	v_cndmask_b32_e64 v160, v140, v160, s[2:3]
	v_cndmask_b32_e64 v161, v141, v161, s[2:3]
	v_cndmask_b32_e64 v163, v139, v135, s[0:1]
	v_cndmask_b32_e64 v156, v160, v144, s[4:5]
	v_cndmask_b32_e64 v157, v161, v145, s[4:5]
	v_exp_f32_e32 v156, v156
	v_exp_f32_e32 v157, v157
	v_cndmask_b32_e64 v162, v142, v162, s[2:3]
	v_cndmask_b32_e64 v163, v143, v163, s[2:3]
	v_cndmask_b32_e64 v158, v162, v146, s[4:5]
	v_cndmask_b32_e64 v159, v163, v147, s[4:5]
	v_pk_add_f32 v[156:157], v[156:157], 1.0 op_sel_hi:[1,0]
	v_exp_f32_e32 v158, v158
	v_rcp_f32_e32 v156, v156
	v_rcp_f32_e32 v157, v157
	v_exp_f32_e32 v159, v159
	v_pk_fma_f32 v[148:149], v[110:111], v[156:157], v[152:153]
	v_pk_add_f32 v[158:159], v[158:159], 1.0 op_sel_hi:[1,0]
	v_cvt_pk_f16_f32 v124, v148, v149
	v_rcp_f32_e32 v158, v158
	v_rcp_f32_e32 v159, v159
	v_mov_b32_dpp v125, v124 quad_perm:[1,2,3,0] row_mask:0xf bank_mask:0xf bound_ctrl:1
	v_mov_b32_dpp v126, v124 quad_perm:[2,3,0,1] row_mask:0xf bank_mask:0xf bound_ctrl:1
	v_mov_b32_dpp v127, v124 quad_perm:[3,0,1,2] row_mask:0xf bank_mask:0xf bound_ctrl:1
	v_pk_fma_f32 v[150:151], v[112:113], v[158:159], v[154:155]
	s_waitcnt vmcnt(15)
	v_mfma_f32_16x16x32_f16 v[132:135], v[2:5], v[124:127], v[46:49]
	v_cvt_pk_f16_f32 v128, v150, v151
	s_nop 0
	v_mfma_f32_16x16x32_f16 v[136:139], v[10:13], v[124:127], v[46:49]
	v_mov_b32_dpp v129, v128 quad_perm:[1,2,3,0] row_mask:0xf bank_mask:0xf bound_ctrl:1
	v_mov_b32_dpp v130, v128 quad_perm:[2,3,0,1] row_mask:0xf bank_mask:0xf bound_ctrl:1
	v_mfma_f32_16x16x32_f16 v[140:143], v[18:21], v[124:127], v[46:49]
	v_mov_b32_dpp v131, v128 quad_perm:[3,0,1,2] row_mask:0xf bank_mask:0xf bound_ctrl:1
	ds_write_b32 v164, v124 offset:5808
	v_mfma_f32_16x16x32_f16 v[144:147], v[26:29], v[124:127], v[46:49]
	global_load_dwordx4 v[46:49], v[0:1], off offset:1024
	ds_write_b32 v164, v128 offset:5812
	v_mfma_f32_16x16x32_f16 v[132:135], v[6:9], v[128:131], v[132:135]
	s_nop 1
	v_mfma_f32_16x16x32_f16 v[136:139], v[14:17], v[128:131], v[136:139]
	s_nop 1
	v_mfma_f32_16x16x32_f16 v[140:143], v[22:25], v[128:131], v[140:143]
	s_nop 1
	v_mfma_f32_16x16x32_f16 v[144:147], v[30:33], v[128:131], v[144:147]
	v_pk_fma_f32 v[154:155], v[106:107], v[150:151], v[108:109]
	v_pk_fma_f32 v[152:153], v[102:103], v[148:149], v[104:105]
	v_cndmask_b32_e64 v160, v136, v132, s[0:1]
	v_cndmask_b32_e64 v161, v137, v133, s[0:1]
	v_cndmask_b32_e64 v162, v138, v134, s[0:1]
	v_cndmask_b32_e64 v160, v140, v160, s[2:3]
	v_cndmask_b32_e64 v161, v141, v161, s[2:3]
	v_cndmask_b32_e64 v163, v139, v135, s[0:1]
	v_cndmask_b32_e64 v156, v160, v144, s[4:5]
	v_cndmask_b32_e64 v157, v161, v145, s[4:5]
	v_exp_f32_e32 v156, v156
	v_exp_f32_e32 v157, v157
	v_cndmask_b32_e64 v162, v142, v162, s[2:3]
	v_cndmask_b32_e64 v163, v143, v163, s[2:3]
	v_cndmask_b32_e64 v158, v162, v146, s[4:5]
	v_cndmask_b32_e64 v159, v163, v147, s[4:5]
	v_pk_add_f32 v[156:157], v[156:157], 1.0 op_sel_hi:[1,0]
	v_exp_f32_e32 v158, v158
	v_rcp_f32_e32 v156, v156
	v_rcp_f32_e32 v157, v157
	v_exp_f32_e32 v159, v159
	v_pk_fma_f32 v[148:149], v[110:111], v[156:157], v[152:153]
	v_pk_add_f32 v[158:159], v[158:159], 1.0 op_sel_hi:[1,0]
	v_cvt_pk_f16_f32 v124, v148, v149
	v_rcp_f32_e32 v158, v158
	v_rcp_f32_e32 v159, v159
	v_mov_b32_dpp v125, v124 quad_perm:[1,2,3,0] row_mask:0xf bank_mask:0xf bound_ctrl:1
	v_mov_b32_dpp v126, v124 quad_perm:[2,3,0,1] row_mask:0xf bank_mask:0xf bound_ctrl:1
	v_mov_b32_dpp v127, v124 quad_perm:[3,0,1,2] row_mask:0xf bank_mask:0xf bound_ctrl:1
	v_pk_fma_f32 v[150:151], v[112:113], v[158:159], v[154:155]
	s_waitcnt vmcnt(15)
	v_mfma_f32_16x16x32_f16 v[132:135], v[2:5], v[124:127], v[42:45]
	v_cvt_pk_f16_f32 v128, v150, v151
	s_nop 0
	v_mfma_f32_16x16x32_f16 v[136:139], v[10:13], v[124:127], v[42:45]
	v_mov_b32_dpp v129, v128 quad_perm:[1,2,3,0] row_mask:0xf bank_mask:0xf bound_ctrl:1
	v_mov_b32_dpp v130, v128 quad_perm:[2,3,0,1] row_mask:0xf bank_mask:0xf bound_ctrl:1
	v_mfma_f32_16x16x32_f16 v[140:143], v[18:21], v[124:127], v[42:45]
	v_mov_b32_dpp v131, v128 quad_perm:[3,0,1,2] row_mask:0xf bank_mask:0xf bound_ctrl:1
	ds_write_b32 v164, v124 offset:6336
	v_mfma_f32_16x16x32_f16 v[144:147], v[26:29], v[124:127], v[42:45]
	global_load_dwordx4 v[42:45], v[0:1], off offset:1280
	ds_write_b32 v164, v128 offset:6340
	v_mfma_f32_16x16x32_f16 v[132:135], v[6:9], v[128:131], v[132:135]
	s_nop 1
	v_mfma_f32_16x16x32_f16 v[136:139], v[14:17], v[128:131], v[136:139]
	s_nop 1
	v_mfma_f32_16x16x32_f16 v[140:143], v[22:25], v[128:131], v[140:143]
	s_nop 1
	v_mfma_f32_16x16x32_f16 v[144:147], v[30:33], v[128:131], v[144:147]
	v_pk_fma_f32 v[154:155], v[106:107], v[150:151], v[108:109]
	v_pk_fma_f32 v[152:153], v[102:103], v[148:149], v[104:105]
	v_cndmask_b32_e64 v160, v136, v132, s[0:1]
	v_cndmask_b32_e64 v161, v137, v133, s[0:1]
	v_cndmask_b32_e64 v162, v138, v134, s[0:1]
	v_cndmask_b32_e64 v160, v140, v160, s[2:3]
	v_cndmask_b32_e64 v161, v141, v161, s[2:3]
	v_cndmask_b32_e64 v163, v139, v135, s[0:1]
	v_cndmask_b32_e64 v156, v160, v144, s[4:5]
	v_cndmask_b32_e64 v157, v161, v145, s[4:5]
	v_exp_f32_e32 v156, v156
	v_exp_f32_e32 v157, v157
	v_cndmask_b32_e64 v162, v142, v162, s[2:3]
	v_cndmask_b32_e64 v163, v143, v163, s[2:3]
	v_cndmask_b32_e64 v158, v162, v146, s[4:5]
	v_cndmask_b32_e64 v159, v163, v147, s[4:5]
	v_pk_add_f32 v[156:157], v[156:157], 1.0 op_sel_hi:[1,0]
	v_exp_f32_e32 v158, v158
	v_rcp_f32_e32 v156, v156
	v_rcp_f32_e32 v157, v157
	v_exp_f32_e32 v159, v159
	v_pk_fma_f32 v[148:149], v[110:111], v[156:157], v[152:153]
	v_pk_add_f32 v[158:159], v[158:159], 1.0 op_sel_hi:[1,0]
	v_cvt_pk_f16_f32 v124, v148, v149
	v_rcp_f32_e32 v158, v158
	v_rcp_f32_e32 v159, v159
	v_mov_b32_dpp v125, v124 quad_perm:[1,2,3,0] row_mask:0xf bank_mask:0xf bound_ctrl:1
	v_mov_b32_dpp v126, v124 quad_perm:[2,3,0,1] row_mask:0xf bank_mask:0xf bound_ctrl:1
	v_mov_b32_dpp v127, v124 quad_perm:[3,0,1,2] row_mask:0xf bank_mask:0xf bound_ctrl:1
	v_pk_fma_f32 v[150:151], v[112:113], v[158:159], v[154:155]
	s_waitcnt vmcnt(15)
	v_mfma_f32_16x16x32_f16 v[132:135], v[2:5], v[124:127], v[38:41]
	v_cvt_pk_f16_f32 v128, v150, v151
	s_nop 0
	v_mfma_f32_16x16x32_f16 v[136:139], v[10:13], v[124:127], v[38:41]
	v_mov_b32_dpp v129, v128 quad_perm:[1,2,3,0] row_mask:0xf bank_mask:0xf bound_ctrl:1
	v_mov_b32_dpp v130, v128 quad_perm:[2,3,0,1] row_mask:0xf bank_mask:0xf bound_ctrl:1
	v_mfma_f32_16x16x32_f16 v[140:143], v[18:21], v[124:127], v[38:41]
	v_mov_b32_dpp v131, v128 quad_perm:[3,0,1,2] row_mask:0xf bank_mask:0xf bound_ctrl:1
	ds_write_b32 v164, v124 offset:6864
	v_mfma_f32_16x16x32_f16 v[144:147], v[26:29], v[124:127], v[38:41]
	global_load_dwordx4 v[38:41], v[0:1], off offset:1536
	ds_write_b32 v164, v128 offset:6868
	v_mfma_f32_16x16x32_f16 v[132:135], v[6:9], v[128:131], v[132:135]
	s_nop 1
	v_mfma_f32_16x16x32_f16 v[136:139], v[14:17], v[128:131], v[136:139]
	s_nop 1
	v_mfma_f32_16x16x32_f16 v[140:143], v[22:25], v[128:131], v[140:143]
	s_nop 1
	v_mfma_f32_16x16x32_f16 v[144:147], v[30:33], v[128:131], v[144:147]
	v_pk_fma_f32 v[154:155], v[106:107], v[150:151], v[108:109]
	v_pk_fma_f32 v[152:153], v[102:103], v[148:149], v[104:105]
	v_cndmask_b32_e64 v160, v136, v132, s[0:1]
	v_cndmask_b32_e64 v161, v137, v133, s[0:1]
	v_cndmask_b32_e64 v162, v138, v134, s[0:1]
	v_cndmask_b32_e64 v160, v140, v160, s[2:3]
	v_cndmask_b32_e64 v161, v141, v161, s[2:3]
	v_cndmask_b32_e64 v163, v139, v135, s[0:1]
	v_cndmask_b32_e64 v156, v160, v144, s[4:5]
	v_cndmask_b32_e64 v157, v161, v145, s[4:5]
	v_exp_f32_e32 v156, v156
	v_exp_f32_e32 v157, v157
	v_cndmask_b32_e64 v162, v142, v162, s[2:3]
	v_cndmask_b32_e64 v163, v143, v163, s[2:3]
	v_cndmask_b32_e64 v158, v162, v146, s[4:5]
	v_cndmask_b32_e64 v159, v163, v147, s[4:5]
	v_pk_add_f32 v[156:157], v[156:157], 1.0 op_sel_hi:[1,0]
	v_exp_f32_e32 v158, v158
	v_rcp_f32_e32 v156, v156
	v_rcp_f32_e32 v157, v157
	v_exp_f32_e32 v159, v159
	v_pk_fma_f32 v[148:149], v[110:111], v[156:157], v[152:153]
	v_pk_add_f32 v[158:159], v[158:159], 1.0 op_sel_hi:[1,0]
	v_cvt_pk_f16_f32 v124, v148, v149
	v_rcp_f32_e32 v158, v158
	v_rcp_f32_e32 v159, v159
	v_mov_b32_dpp v125, v124 quad_perm:[1,2,3,0] row_mask:0xf bank_mask:0xf bound_ctrl:1
	v_mov_b32_dpp v126, v124 quad_perm:[2,3,0,1] row_mask:0xf bank_mask:0xf bound_ctrl:1
	v_mov_b32_dpp v127, v124 quad_perm:[3,0,1,2] row_mask:0xf bank_mask:0xf bound_ctrl:1
	v_pk_fma_f32 v[150:151], v[112:113], v[158:159], v[154:155]
	s_waitcnt vmcnt(15)
	v_mfma_f32_16x16x32_f16 v[132:135], v[2:5], v[124:127], v[34:37]
	v_cvt_pk_f16_f32 v128, v150, v151
	s_nop 0
	v_mfma_f32_16x16x32_f16 v[136:139], v[10:13], v[124:127], v[34:37]
	v_mov_b32_dpp v129, v128 quad_perm:[1,2,3,0] row_mask:0xf bank_mask:0xf bound_ctrl:1
	v_mov_b32_dpp v130, v128 quad_perm:[2,3,0,1] row_mask:0xf bank_mask:0xf bound_ctrl:1
	v_mfma_f32_16x16x32_f16 v[140:143], v[18:21], v[124:127], v[34:37]
	v_mov_b32_dpp v131, v128 quad_perm:[3,0,1,2] row_mask:0xf bank_mask:0xf bound_ctrl:1
	ds_write_b32 v164, v124 offset:7392
	v_mfma_f32_16x16x32_f16 v[144:147], v[26:29], v[124:127], v[34:37]
	global_load_dwordx4 v[34:37], v[0:1], off offset:1792
	ds_write_b32 v164, v128 offset:7396
	v_mfma_f32_16x16x32_f16 v[132:135], v[6:9], v[128:131], v[132:135]
	s_nop 1
	v_mfma_f32_16x16x32_f16 v[136:139], v[14:17], v[128:131], v[136:139]
	s_nop 1
	v_mfma_f32_16x16x32_f16 v[140:143], v[22:25], v[128:131], v[140:143]
	s_nop 1
	v_mfma_f32_16x16x32_f16 v[144:147], v[30:33], v[128:131], v[144:147]
	v_pk_fma_f32 v[154:155], v[106:107], v[150:151], v[108:109]
	v_pk_fma_f32 v[152:153], v[102:103], v[148:149], v[104:105]
	v_cndmask_b32_e64 v160, v136, v132, s[0:1]
	v_cndmask_b32_e64 v161, v137, v133, s[0:1]
	v_cndmask_b32_e64 v162, v138, v134, s[0:1]
	v_cndmask_b32_e64 v160, v140, v160, s[2:3]
	v_cndmask_b32_e64 v161, v141, v161, s[2:3]
	v_cndmask_b32_e64 v163, v139, v135, s[0:1]
	v_cndmask_b32_e64 v156, v160, v144, s[4:5]
	v_cndmask_b32_e64 v157, v161, v145, s[4:5]
	v_exp_f32_e32 v156, v156
	v_exp_f32_e32 v157, v157
	v_cndmask_b32_e64 v162, v142, v162, s[2:3]
	v_cndmask_b32_e64 v163, v143, v163, s[2:3]
	v_cndmask_b32_e64 v158, v162, v146, s[4:5]
	v_cndmask_b32_e64 v159, v163, v147, s[4:5]
	v_pk_add_f32 v[156:157], v[156:157], 1.0 op_sel_hi:[1,0]
	v_exp_f32_e32 v158, v158
	v_rcp_f32_e32 v156, v156
	v_rcp_f32_e32 v157, v157
	v_exp_f32_e32 v159, v159
	v_pk_fma_f32 v[148:149], v[110:111], v[156:157], v[152:153]
	v_pk_add_f32 v[158:159], v[158:159], 1.0 op_sel_hi:[1,0]
	v_cvt_pk_f16_f32 v124, v148, v149
	v_rcp_f32_e32 v158, v158
	v_rcp_f32_e32 v159, v159
	v_mov_b32_dpp v125, v124 quad_perm:[1,2,3,0] row_mask:0xf bank_mask:0xf bound_ctrl:1
	v_mov_b32_dpp v126, v124 quad_perm:[2,3,0,1] row_mask:0xf bank_mask:0xf bound_ctrl:1
	v_mov_b32_dpp v127, v124 quad_perm:[3,0,1,2] row_mask:0xf bank_mask:0xf bound_ctrl:1
	v_pk_fma_f32 v[150:151], v[112:113], v[158:159], v[154:155]
	s_waitcnt vmcnt(15)
	v_mfma_f32_16x16x32_f16 v[132:135], v[2:5], v[124:127], v[98:101]
	v_cvt_pk_f16_f32 v128, v150, v151
	s_nop 0
	v_mfma_f32_16x16x32_f16 v[136:139], v[10:13], v[124:127], v[98:101]
	v_mov_b32_dpp v129, v128 quad_perm:[1,2,3,0] row_mask:0xf bank_mask:0xf bound_ctrl:1
	v_mov_b32_dpp v130, v128 quad_perm:[2,3,0,1] row_mask:0xf bank_mask:0xf bound_ctrl:1
	v_mfma_f32_16x16x32_f16 v[140:143], v[18:21], v[124:127], v[98:101]
	v_mov_b32_dpp v131, v128 quad_perm:[3,0,1,2] row_mask:0xf bank_mask:0xf bound_ctrl:1
	ds_write_b32 v164, v124 offset:7920
	v_mfma_f32_16x16x32_f16 v[144:147], v[26:29], v[124:127], v[98:101]
	global_load_dwordx4 v[98:101], v[0:1], off offset:2048
	ds_write_b32 v164, v128 offset:7924
	s_waitcnt lgkmcnt(0)
	s_barrier
	s_add_i32 s12, s12, 1
	v_lshl_add_u64 v[0:1], v[0:1], 0, s[6:7]
	v_mfma_f32_16x16x32_f16 v[132:135], v[6:9], v[128:131], v[132:135]
	s_nop 1
	v_mfma_f32_16x16x32_f16 v[136:139], v[14:17], v[128:131], v[136:139]
	s_nop 1
	v_mfma_f32_16x16x32_f16 v[140:143], v[22:25], v[128:131], v[140:143]
	s_nop 1
	v_mfma_f32_16x16x32_f16 v[144:147], v[30:33], v[128:131], v[144:147]
	s_cmp_lt_u32 s12, 64
	s_cbranch_scc1 .LBB3_169
	s_branch .LBB3_168
